# as v73 plus first K-loop iteration of every GEMM peeled with zero accumulator input (first-touch MFMAs take C=0), removing the 128 per-tile accumulator-zeroing moves
# speedup vs baseline: 1.0189x; 1.0064x over previous
.LBB0_409:
	s_ashr_i32 s21, s20, 31
	s_lshl_b64 s[22:23], s[20:21], 20
	s_add_u32 s22, s82, s22
	s_addc_u32 s23, s83, s23
	s_and_b64 s[24:25], s[6:7], exec
	s_cselect_b32 s21, s23, s27
	s_cselect_b32 s60, s22, s26
	s_ashr_i32 s19, s18, 31
	s_lshl_b64 s[24:25], s[18:19], 20
	s_add_u32 s24, s3, s24
	s_addc_u32 s25, s33, s25
	s_and_b64 s[30:31], s[6:7], exec
	s_cselect_b32 s19, s25, s29
	s_cselect_b32 s61, s24, s28
	s_add_u32 s26, s26, 0x80080
	s_addc_u32 s27, s27, 0
	s_add_u32 s62, s28, 0x100
	s_addc_u32 s63, s29, 0
	s_mov_b32 s64, -2
	ds_read_b128 v[152:155], v148
	ds_read_b128 v[156:159], v148 offset:1024
	ds_read_b128 v[160:163], v148 offset:2048
	ds_read_b128 v[164:167], v148 offset:3072
	ds_read_b128 v[168:171], v149
	ds_read_b128 v[172:175], v149 offset:1024
	ds_read_b128 v[176:179], v149 offset:2048
	ds_read_b128 v[180:183], v149 offset:3072
	s_add_u32 s28, s26, 0xfff80080
	s_addc_u32 s29, s27, -1
	s_cmp_eq_u32 s64, 28
	s_cselect_b32 s31, s21, s29
	s_cselect_b32 s30, s60, s28
	s_cselect_b32 s29, s19, s63
	s_cselect_b32 s28, s61, s62
	v_lshl_add_u64 v[184:185], s[26:27], 0, v[138:139]
	s_add_i32 m0, s17, 0xc000
	ds_read_b128 v[188:191], v150
	ds_read_b128 v[192:195], v150 offset:1024
	ds_read_b128 v[196:199], v150 offset:2048
	ds_read_b128 v[200:203], v150 offset:3072
	ds_read_b128 v[204:207], v150 offset:4096
	ds_read_b128 v[208:211], v150 offset:5120
	ds_read_b128 v[212:215], v150 offset:6144
	ds_read_b128 v[216:219], v150 offset:7168
	global_load_lds_dwordx4 v[184:185], off
	v_lshl_add_u64 v[184:185], s[26:27], 0, v[140:141]
	s_add_i32 m0, s17, 0xe000
	s_nop 0
	global_load_lds_dwordx4 v[184:185], off
	s_waitcnt vmcnt(8)
	s_waitcnt lgkmcnt(0)
	s_barrier
	s_setprio 1
	s_waitcnt lgkmcnt(0)
	v_mfma_f32_16x16x32_f16 v[126:129], v[152:155], v[188:191], 0
	v_mfma_f32_16x16x32_f16 v[122:125], v[160:163], v[188:191], 0
	v_mfma_f32_16x16x32_f16 v[118:121], v[152:155], v[196:199], 0
	v_mfma_f32_16x16x32_f16 v[114:117], v[160:163], v[196:199], 0
	v_mfma_f32_16x16x32_f16 v[102:105], v[152:155], v[204:207], 0
	v_mfma_f32_16x16x32_f16 v[98:101], v[160:163], v[204:207], 0
	v_mfma_f32_16x16x32_f16 v[86:89], v[152:155], v[212:215], 0
	v_mfma_f32_16x16x32_f16 v[82:85], v[160:163], v[212:215], 0
	v_mfma_f32_16x16x32_f16 v[126:129], v[156:159], v[192:195], v[126:129]
	v_mfma_f32_16x16x32_f16 v[122:125], v[164:167], v[192:195], v[122:125]
	v_mfma_f32_16x16x32_f16 v[118:121], v[156:159], v[200:203], v[118:121]
	v_mfma_f32_16x16x32_f16 v[114:117], v[164:167], v[200:203], v[114:117]
	v_mfma_f32_16x16x32_f16 v[102:105], v[156:159], v[208:211], v[102:105]
	v_mfma_f32_16x16x32_f16 v[98:101], v[164:167], v[208:211], v[98:101]
	v_mfma_f32_16x16x32_f16 v[86:89], v[156:159], v[216:219], v[86:89]
	v_mfma_f32_16x16x32_f16 v[82:85], v[164:167], v[216:219], v[82:85]
	s_setprio 0
	s_setprio 1
	v_mfma_f32_16x16x32_f16 v[110:113], v[168:171], v[188:191], 0
	v_mfma_f32_16x16x32_f16 v[106:109], v[176:179], v[188:191], 0
	v_mfma_f32_16x16x32_f16 v[94:97], v[168:171], v[196:199], 0
	v_mfma_f32_16x16x32_f16 v[90:93], v[176:179], v[196:199], 0
	v_mfma_f32_16x16x32_f16 v[78:81], v[168:171], v[204:207], 0
	v_mfma_f32_16x16x32_f16 v[74:77], v[176:179], v[204:207], 0
	v_mfma_f32_16x16x32_f16 v[70:73], v[168:171], v[212:215], 0
	v_mfma_f32_16x16x32_f16 v[66:69], v[176:179], v[212:215], 0
	v_mfma_f32_16x16x32_f16 v[110:113], v[172:175], v[192:195], v[110:113]
	v_mfma_f32_16x16x32_f16 v[106:109], v[180:183], v[192:195], v[106:109]
	v_mfma_f32_16x16x32_f16 v[94:97], v[172:175], v[200:203], v[94:97]
	v_mfma_f32_16x16x32_f16 v[90:93], v[180:183], v[200:203], v[90:93]
	s_setprio 2
	s_barrier
	v_mfma_f32_16x16x32_f16 v[78:81], v[172:175], v[208:211], v[78:81]
	v_mfma_f32_16x16x32_f16 v[74:77], v[180:183], v[208:211], v[74:77]
	v_mfma_f32_16x16x32_f16 v[70:73], v[172:175], v[216:219], v[70:73]
	v_mfma_f32_16x16x32_f16 v[66:69], v[180:183], v[216:219], v[66:69]
	s_setprio 0
	s_nop 0
	s_add_i32 s65, s48, s34
	v_lshl_add_u64 v[184:185], s[28:29], 0, v[134:135]
	s_mov_b32 m0, s65
	ds_read_b128 v[188:191], v150 offset:16384
	ds_read_b128 v[192:195], v150 offset:17408
	ds_read_b128 v[196:199], v150 offset:18432
	ds_read_b128 v[200:203], v150 offset:19456
	ds_read_b128 v[204:207], v150 offset:20480
	ds_read_b128 v[208:211], v150 offset:21504
	ds_read_b128 v[212:215], v150 offset:22528
	ds_read_b128 v[216:219], v150 offset:23552
	global_load_lds_dwordx4 v[184:185], off
	s_add_i32 m0, s65, 0x2000
	s_add_u32 s66, s28, 0x80000
	v_lshl_add_u64 v[220:221], s[28:29], 0, v[130:131]
	s_addc_u32 s67, s29, 0
	s_add_i32 s65, s49, s34
	global_load_lds_dwordx4 v[220:221], off
	v_lshl_add_u64 v[222:223], s[66:67], 0, v[134:135]
	s_mov_b32 m0, s65
	v_lshl_add_u64 v[224:225], s[30:31], 0, v[132:133]
	global_load_lds_dwordx4 v[222:223], off
	v_lshl_add_u64 v[222:223], s[66:67], 0, v[130:131]
	s_add_i32 m0, s65, 0x2000
	s_nop 0
	global_load_lds_dwordx4 v[222:223], off
	v_lshl_add_u64 v[222:223], s[30:31], 0, v[136:137]
	s_mov_b32 m0, s17
	s_nop 0
	global_load_lds_dwordx4 v[222:223], off
	s_mov_b32 m0, s37
	s_nop 0
	global_load_lds_dwordx4 v[224:225], off
	s_waitcnt vmcnt(8)
	s_waitcnt lgkmcnt(0)
	s_barrier
	s_setprio 1
	s_waitcnt lgkmcnt(0)
	v_mfma_f32_16x16x32_f16 v[62:65], v[152:155], v[188:191], 0
	v_mfma_f32_16x16x32_f16 v[58:61], v[160:163], v[188:191], 0
	v_mfma_f32_16x16x32_f16 v[54:57], v[152:155], v[196:199], 0
	v_mfma_f32_16x16x32_f16 v[50:53], v[160:163], v[196:199], 0
	v_mfma_f32_16x16x32_f16 v[38:41], v[152:155], v[204:207], 0
	v_mfma_f32_16x16x32_f16 v[34:37], v[160:163], v[204:207], 0
	v_mfma_f32_16x16x32_f16 v[22:25], v[152:155], v[212:215], 0
	v_mfma_f32_16x16x32_f16 v[18:21], v[160:163], v[212:215], 0
	v_mfma_f32_16x16x32_f16 v[62:65], v[156:159], v[192:195], v[62:65]
	v_mfma_f32_16x16x32_f16 v[58:61], v[164:167], v[192:195], v[58:61]
	v_mfma_f32_16x16x32_f16 v[54:57], v[156:159], v[200:203], v[54:57]
	v_mfma_f32_16x16x32_f16 v[50:53], v[164:167], v[200:203], v[50:53]
	v_mfma_f32_16x16x32_f16 v[38:41], v[156:159], v[208:211], v[38:41]
	v_mfma_f32_16x16x32_f16 v[34:37], v[164:167], v[208:211], v[34:37]
	v_mfma_f32_16x16x32_f16 v[22:25], v[156:159], v[216:219], v[22:25]
	v_mfma_f32_16x16x32_f16 v[18:21], v[164:167], v[216:219], v[18:21]
	s_setprio 0
	s_setprio 1
	v_mfma_f32_16x16x32_f16 v[46:49], v[168:171], v[188:191], 0
	v_mfma_f32_16x16x32_f16 v[42:45], v[176:179], v[188:191], 0
	v_mfma_f32_16x16x32_f16 v[30:33], v[168:171], v[196:199], 0
	v_mfma_f32_16x16x32_f16 v[26:29], v[176:179], v[196:199], 0
	v_mfma_f32_16x16x32_f16 v[14:17], v[168:171], v[204:207], 0
	v_mfma_f32_16x16x32_f16 v[10:13], v[176:179], v[204:207], 0
	v_mfma_f32_16x16x32_f16 v[6:9], v[168:171], v[212:215], 0
	v_mfma_f32_16x16x32_f16 v[2:5], v[176:179], v[212:215], 0
	v_mfma_f32_16x16x32_f16 v[46:49], v[172:175], v[192:195], v[46:49]
	v_mfma_f32_16x16x32_f16 v[42:45], v[180:183], v[192:195], v[42:45]
	v_mfma_f32_16x16x32_f16 v[30:33], v[172:175], v[200:203], v[30:33]
	v_mfma_f32_16x16x32_f16 v[26:29], v[180:183], v[200:203], v[26:29]
	s_setprio 2
	s_barrier
	v_mfma_f32_16x16x32_f16 v[14:17], v[172:175], v[208:211], v[14:17]
	v_mfma_f32_16x16x32_f16 v[10:13], v[180:183], v[208:211], v[10:13]
	v_mfma_f32_16x16x32_f16 v[6:9], v[172:175], v[216:219], v[6:9]
	v_mfma_f32_16x16x32_f16 v[2:5], v[180:183], v[216:219], v[2:5]
	s_setprio 0
	s_nop 0
	s_add_i32 s65, 0, 0x18000
	v_add_u32_e32 v151, s65, v146
	s_add_i32 s66, 0, 0x1c000
	ds_read_b128 v[152:155], v151
	ds_read_b128 v[156:159], v151 offset:1024
	ds_read_b128 v[160:163], v151 offset:2048
	ds_read_b128 v[164:167], v151 offset:3072
	v_add_u32_e32 v151, s66, v146
	ds_read_b128 v[168:171], v151
	ds_read_b128 v[172:175], v151 offset:1024
	ds_read_b128 v[176:179], v151 offset:2048
	ds_read_b128 v[180:183], v151 offset:3072
	s_add_u32 s30, s30, 0x80000
	s_addc_u32 s31, s31, 0
	s_mov_b32 m0, s38
	v_lshl_add_u64 v[226:227], s[30:31], 0, v[136:137]
	ds_read_b128 v[188:191], v150 offset:32768
	ds_read_b128 v[192:195], v150 offset:33792
	ds_read_b128 v[196:199], v150 offset:34816
	ds_read_b128 v[200:203], v150 offset:35840
	ds_read_b128 v[204:207], v150 offset:36864
	ds_read_b128 v[208:211], v150 offset:37888
	ds_read_b128 v[212:215], v150 offset:38912
	ds_read_b128 v[216:219], v150 offset:39936
	global_load_lds_dwordx4 v[226:227], off
	v_lshl_add_u64 v[226:227], s[30:31], 0, v[132:133]
	s_mov_b32 m0, s39
	s_nop 0
	global_load_lds_dwordx4 v[226:227], off
	s_waitcnt vmcnt(8)
	s_waitcnt lgkmcnt(0)
	s_barrier
	s_setprio 1
	s_waitcnt lgkmcnt(0)
	v_mfma_f32_16x16x32_f16 v[126:129], v[152:155], v[188:191], v[126:129]
	v_mfma_f32_16x16x32_f16 v[122:125], v[160:163], v[188:191], v[122:125]
	v_mfma_f32_16x16x32_f16 v[118:121], v[152:155], v[196:199], v[118:121]
	v_mfma_f32_16x16x32_f16 v[114:117], v[160:163], v[196:199], v[114:117]
	v_mfma_f32_16x16x32_f16 v[102:105], v[152:155], v[204:207], v[102:105]
	v_mfma_f32_16x16x32_f16 v[98:101], v[160:163], v[204:207], v[98:101]
	v_mfma_f32_16x16x32_f16 v[86:89], v[152:155], v[212:215], v[86:89]
	v_mfma_f32_16x16x32_f16 v[82:85], v[160:163], v[212:215], v[82:85]
	v_mfma_f32_16x16x32_f16 v[126:129], v[156:159], v[192:195], v[126:129]
	v_mfma_f32_16x16x32_f16 v[122:125], v[164:167], v[192:195], v[122:125]
	v_mfma_f32_16x16x32_f16 v[118:121], v[156:159], v[200:203], v[118:121]
	v_mfma_f32_16x16x32_f16 v[114:117], v[164:167], v[200:203], v[114:117]
	v_mfma_f32_16x16x32_f16 v[102:105], v[156:159], v[208:211], v[102:105]
	v_mfma_f32_16x16x32_f16 v[98:101], v[164:167], v[208:211], v[98:101]
	v_mfma_f32_16x16x32_f16 v[86:89], v[156:159], v[216:219], v[86:89]
	v_mfma_f32_16x16x32_f16 v[82:85], v[164:167], v[216:219], v[82:85]
	s_setprio 0
	s_setprio 1
	v_mfma_f32_16x16x32_f16 v[110:113], v[168:171], v[188:191], v[110:113]
	v_mfma_f32_16x16x32_f16 v[106:109], v[176:179], v[188:191], v[106:109]
	v_mfma_f32_16x16x32_f16 v[94:97], v[168:171], v[196:199], v[94:97]
	v_mfma_f32_16x16x32_f16 v[90:93], v[176:179], v[196:199], v[90:93]
	v_mfma_f32_16x16x32_f16 v[78:81], v[168:171], v[204:207], v[78:81]
	v_mfma_f32_16x16x32_f16 v[74:77], v[176:179], v[204:207], v[74:77]
	v_mfma_f32_16x16x32_f16 v[70:73], v[168:171], v[212:215], v[70:73]
	v_mfma_f32_16x16x32_f16 v[66:69], v[176:179], v[212:215], v[66:69]
	v_mfma_f32_16x16x32_f16 v[110:113], v[172:175], v[192:195], v[110:113]
	v_mfma_f32_16x16x32_f16 v[106:109], v[180:183], v[192:195], v[106:109]
	v_mfma_f32_16x16x32_f16 v[94:97], v[172:175], v[200:203], v[94:97]
	v_mfma_f32_16x16x32_f16 v[90:93], v[180:183], v[200:203], v[90:93]
	s_setprio 2
	s_barrier
	v_mfma_f32_16x16x32_f16 v[78:81], v[172:175], v[208:211], v[78:81]
	v_mfma_f32_16x16x32_f16 v[74:77], v[180:183], v[208:211], v[74:77]
	v_mfma_f32_16x16x32_f16 v[70:73], v[172:175], v[216:219], v[70:73]
	v_mfma_f32_16x16x32_f16 v[66:69], v[180:183], v[216:219], v[66:69]
	s_setprio 0
	s_nop 0
	s_add_i32 s30, s65, s34
	v_lshl_add_u64 v[184:185], v[184:185], 0, s[12:13]
	s_mov_b32 m0, s30
	ds_read_b128 v[188:191], v150 offset:49152
	ds_read_b128 v[192:195], v150 offset:50176
	ds_read_b128 v[196:199], v150 offset:51200
	ds_read_b128 v[200:203], v150 offset:52224
	ds_read_b128 v[204:207], v150 offset:53248
	ds_read_b128 v[208:211], v150 offset:54272
	ds_read_b128 v[212:215], v150 offset:55296
	ds_read_b128 v[216:219], v150 offset:56320
	global_load_lds_dwordx4 v[184:185], off
	s_add_i32 m0, s30, 0x2000
	s_add_u32 s28, s28, 0x80080
	v_lshl_add_u64 v[184:185], v[220:221], 0, s[12:13]
	s_addc_u32 s29, s29, 0
	s_add_i32 s30, s66, s34
	global_load_lds_dwordx4 v[184:185], off
	v_lshl_add_u64 v[184:185], s[28:29], 0, v[134:135]
	s_mov_b32 m0, s30
	s_nop 0
	global_load_lds_dwordx4 v[184:185], off
	v_lshl_add_u64 v[184:185], s[28:29], 0, v[130:131]
	s_add_i32 m0, s30, 0x2000
	s_nop 0
	global_load_lds_dwordx4 v[184:185], off
	v_lshl_add_u64 v[184:185], v[222:223], 0, s[12:13]
	s_mov_b32 m0, s41
	s_nop 0
	global_load_lds_dwordx4 v[184:185], off
	v_lshl_add_u64 v[184:185], v[224:225], 0, s[12:13]
	s_mov_b32 m0, s46
	s_nop 0
	global_load_lds_dwordx4 v[184:185], off
	s_waitcnt vmcnt(8)
	s_waitcnt lgkmcnt(0)
	s_barrier
	s_setprio 1
	s_waitcnt lgkmcnt(0)
	v_mfma_f32_16x16x32_f16 v[62:65], v[152:155], v[188:191], v[62:65]
	v_mfma_f32_16x16x32_f16 v[58:61], v[160:163], v[188:191], v[58:61]
	v_mfma_f32_16x16x32_f16 v[54:57], v[152:155], v[196:199], v[54:57]
	v_mfma_f32_16x16x32_f16 v[50:53], v[160:163], v[196:199], v[50:53]
	v_mfma_f32_16x16x32_f16 v[38:41], v[152:155], v[204:207], v[38:41]
	v_mfma_f32_16x16x32_f16 v[34:37], v[160:163], v[204:207], v[34:37]
	v_mfma_f32_16x16x32_f16 v[22:25], v[152:155], v[212:215], v[22:25]
	v_mfma_f32_16x16x32_f16 v[18:21], v[160:163], v[212:215], v[18:21]
	v_mfma_f32_16x16x32_f16 v[62:65], v[156:159], v[192:195], v[62:65]
	v_mfma_f32_16x16x32_f16 v[58:61], v[164:167], v[192:195], v[58:61]
	v_mfma_f32_16x16x32_f16 v[54:57], v[156:159], v[200:203], v[54:57]
	v_mfma_f32_16x16x32_f16 v[50:53], v[164:167], v[200:203], v[50:53]
	v_mfma_f32_16x16x32_f16 v[38:41], v[156:159], v[208:211], v[38:41]
	v_mfma_f32_16x16x32_f16 v[34:37], v[164:167], v[208:211], v[34:37]
	v_mfma_f32_16x16x32_f16 v[22:25], v[156:159], v[216:219], v[22:25]
	v_mfma_f32_16x16x32_f16 v[18:21], v[164:167], v[216:219], v[18:21]
	s_setprio 0
	s_setprio 1
	v_mfma_f32_16x16x32_f16 v[46:49], v[168:171], v[188:191], v[46:49]
	v_mfma_f32_16x16x32_f16 v[42:45], v[176:179], v[188:191], v[42:45]
	v_mfma_f32_16x16x32_f16 v[30:33], v[168:171], v[196:199], v[30:33]
	v_mfma_f32_16x16x32_f16 v[26:29], v[176:179], v[196:199], v[26:29]
	v_mfma_f32_16x16x32_f16 v[14:17], v[168:171], v[204:207], v[14:17]
	v_mfma_f32_16x16x32_f16 v[10:13], v[176:179], v[204:207], v[10:13]
	v_mfma_f32_16x16x32_f16 v[6:9], v[168:171], v[212:215], v[6:9]
	v_mfma_f32_16x16x32_f16 v[2:5], v[176:179], v[212:215], v[2:5]
	v_mfma_f32_16x16x32_f16 v[46:49], v[172:175], v[192:195], v[46:49]
	v_mfma_f32_16x16x32_f16 v[42:45], v[180:183], v[192:195], v[42:45]
	v_mfma_f32_16x16x32_f16 v[30:33], v[172:175], v[200:203], v[30:33]
	v_mfma_f32_16x16x32_f16 v[26:29], v[180:183], v[200:203], v[26:29]
	s_setprio 2
	s_barrier
	v_mfma_f32_16x16x32_f16 v[14:17], v[172:175], v[208:211], v[14:17]
	v_mfma_f32_16x16x32_f16 v[10:13], v[180:183], v[208:211], v[10:13]
	v_mfma_f32_16x16x32_f16 v[6:9], v[172:175], v[216:219], v[6:9]
	v_mfma_f32_16x16x32_f16 v[2:5], v[180:183], v[216:219], v[2:5]
	s_setprio 0
	s_nop 0
	s_add_i32 s64, s64, 2
	s_add_u32 s26, s26, 0x100
	s_addc_u32 s27, s27, 0
	s_add_u32 s62, s62, 0x100
	s_addc_u32 s63, s63, 0
	s_cmp_gt_u32 s64, 29
	s_cbranch_scc0 .LBB0_410
	s_branch .Lpeel_exit_0

.Lpeel_exit_0:
	s_and_b64 vcc, exec, s[14:15]
	s_cbranch_vccz .LBB0_413
	s_barrier

.LBB0_627:
	s_ashr_i32 s19, s18, 31
	s_lshl_b64 s[20:21], s[18:19], 20
	s_add_u32 s20, s15, s20
	s_addc_u32 s21, s33, s21
	s_and_b64 s[22:23], s[6:7], exec
	s_cselect_b32 s19, s21, s27
	s_cselect_b32 s51, s20, s26
	s_ashr_i32 s17, s16, 31
	s_lshl_b64 s[22:23], s[16:17], 20
	s_add_u32 s22, s34, s22
	s_addc_u32 s23, s35, s23
	s_and_b64 s[30:31], s[6:7], exec
	s_cselect_b32 s17, s23, s29
	s_cselect_b32 s60, s22, s28
	s_add_u32 s26, s26, 0x80080
	s_addc_u32 s27, s27, 0
	s_add_u32 s61, s28, 0x100
	s_addc_u32 s62, s29, 0
	s_mov_b32 s63, -2
	ds_read_b128 v[146:149], v154
	ds_read_b128 v[158:161], v154 offset:1024
	ds_read_b128 v[162:165], v154 offset:2048
	ds_read_b128 v[166:169], v154 offset:3072
	ds_read_b128 v[170:173], v155
	ds_read_b128 v[174:177], v155 offset:1024
	ds_read_b128 v[178:181], v155 offset:2048
	ds_read_b128 v[182:185], v155 offset:3072
	s_add_u32 s28, s26, 0xfff80080
	s_addc_u32 s29, s27, -1
	s_cmp_eq_u32 s63, 28
	s_cselect_b32 s31, s19, s29
	s_cselect_b32 s30, s51, s28
	s_cselect_b32 s29, s17, s62
	s_cselect_b32 s28, s60, s61
	v_lshl_add_u64 v[150:151], s[26:27], 0, v[138:139]
	s_add_i32 m0, s25, 0xc000
	ds_read_b128 v[188:191], v156
	ds_read_b128 v[192:195], v156 offset:1024
	ds_read_b128 v[196:199], v156 offset:2048
	ds_read_b128 v[200:203], v156 offset:3072
	ds_read_b128 v[204:207], v156 offset:4096
	ds_read_b128 v[208:211], v156 offset:5120
	ds_read_b128 v[212:215], v156 offset:6144
	ds_read_b128 v[216:219], v156 offset:7168
	global_load_lds_dwordx4 v[150:151], off
	v_lshl_add_u64 v[150:151], s[26:27], 0, v[140:141]
	s_add_i32 m0, s25, 0xe000
	s_nop 0
	global_load_lds_dwordx4 v[150:151], off
	s_waitcnt vmcnt(8)
	s_waitcnt lgkmcnt(0)
	s_barrier
	s_setprio 1
	s_waitcnt lgkmcnt(0)
	v_mfma_f32_16x16x32_f16 v[126:129], v[146:149], v[188:191], 0
	v_mfma_f32_16x16x32_f16 v[122:125], v[162:165], v[188:191], 0
	v_mfma_f32_16x16x32_f16 v[110:113], v[146:149], v[196:199], 0
	v_mfma_f32_16x16x32_f16 v[106:109], v[162:165], v[196:199], 0
	v_mfma_f32_16x16x32_f16 v[94:97], v[146:149], v[204:207], 0
	v_mfma_f32_16x16x32_f16 v[90:93], v[162:165], v[204:207], 0
	v_mfma_f32_16x16x32_f16 v[78:81], v[146:149], v[212:215], 0
	v_mfma_f32_16x16x32_f16 v[74:77], v[162:165], v[212:215], 0
	v_mfma_f32_16x16x32_f16 v[126:129], v[158:161], v[192:195], v[126:129]
	v_mfma_f32_16x16x32_f16 v[122:125], v[166:169], v[192:195], v[122:125]
	v_mfma_f32_16x16x32_f16 v[110:113], v[158:161], v[200:203], v[110:113]
	v_mfma_f32_16x16x32_f16 v[106:109], v[166:169], v[200:203], v[106:109]
	v_mfma_f32_16x16x32_f16 v[94:97], v[158:161], v[208:211], v[94:97]
	v_mfma_f32_16x16x32_f16 v[90:93], v[166:169], v[208:211], v[90:93]
	v_mfma_f32_16x16x32_f16 v[78:81], v[158:161], v[216:219], v[78:81]
	v_mfma_f32_16x16x32_f16 v[74:77], v[166:169], v[216:219], v[74:77]
	s_setprio 0
	s_setprio 1
	v_mfma_f32_16x16x32_f16 v[118:121], v[170:173], v[188:191], 0
	v_mfma_f32_16x16x32_f16 v[114:117], v[178:181], v[188:191], 0
	v_mfma_f32_16x16x32_f16 v[102:105], v[170:173], v[196:199], 0
	v_mfma_f32_16x16x32_f16 v[98:101], v[178:181], v[196:199], 0
	v_mfma_f32_16x16x32_f16 v[86:89], v[170:173], v[204:207], 0
	v_mfma_f32_16x16x32_f16 v[82:85], v[178:181], v[204:207], 0
	v_mfma_f32_16x16x32_f16 v[70:73], v[170:173], v[212:215], 0
	v_mfma_f32_16x16x32_f16 v[66:69], v[178:181], v[212:215], 0
	v_mfma_f32_16x16x32_f16 v[118:121], v[174:177], v[192:195], v[118:121]
	v_mfma_f32_16x16x32_f16 v[114:117], v[182:185], v[192:195], v[114:117]
	v_mfma_f32_16x16x32_f16 v[102:105], v[174:177], v[200:203], v[102:105]
	v_mfma_f32_16x16x32_f16 v[98:101], v[182:185], v[200:203], v[98:101]
	s_setprio 2
	s_barrier
	v_mfma_f32_16x16x32_f16 v[86:89], v[174:177], v[208:211], v[86:89]
	v_mfma_f32_16x16x32_f16 v[82:85], v[182:185], v[208:211], v[82:85]
	v_mfma_f32_16x16x32_f16 v[70:73], v[174:177], v[216:219], v[70:73]
	v_mfma_f32_16x16x32_f16 v[66:69], v[182:185], v[216:219], v[66:69]
	s_setprio 0
	s_nop 0
	s_add_i32 s64, s48, s36
	v_lshl_add_u64 v[150:151], s[28:29], 0, v[132:133]
	s_mov_b32 m0, s64
	ds_read_b128 v[188:191], v156 offset:16384
	ds_read_b128 v[192:195], v156 offset:17408
	ds_read_b128 v[196:199], v156 offset:18432
	ds_read_b128 v[200:203], v156 offset:19456
	ds_read_b128 v[204:207], v156 offset:20480
	ds_read_b128 v[208:211], v156 offset:21504
	ds_read_b128 v[212:215], v156 offset:22528
	ds_read_b128 v[216:219], v156 offset:23552
	global_load_lds_dwordx4 v[150:151], off
	s_add_i32 m0, s64, 0x2000
	s_add_u32 s64, s28, 0x80000
	v_lshl_add_u64 v[220:221], s[28:29], 0, v[136:137]
	s_addc_u32 s65, s29, 0
	s_add_i32 s66, s49, s36
	global_load_lds_dwordx4 v[220:221], off
	v_lshl_add_u64 v[222:223], s[64:65], 0, v[132:133]
	s_mov_b32 m0, s66
	v_lshl_add_u64 v[224:225], s[30:31], 0, v[134:135]
	global_load_lds_dwordx4 v[222:223], off
	v_lshl_add_u64 v[222:223], s[64:65], 0, v[136:137]
	s_add_i32 m0, s66, 0x2000
	s_nop 0
	global_load_lds_dwordx4 v[222:223], off
	v_lshl_add_u64 v[222:223], s[30:31], 0, v[130:131]
	s_mov_b32 m0, s25
	s_nop 0
	global_load_lds_dwordx4 v[222:223], off
	s_mov_b32 m0, s37
	s_nop 0
	global_load_lds_dwordx4 v[224:225], off
	s_waitcnt vmcnt(8)
	s_waitcnt lgkmcnt(0)
	s_barrier
	s_setprio 1
	s_waitcnt lgkmcnt(0)
	v_mfma_f32_16x16x32_f16 v[62:65], v[146:149], v[188:191], 0
	v_mfma_f32_16x16x32_f16 v[58:61], v[162:165], v[188:191], 0
	v_mfma_f32_16x16x32_f16 v[46:49], v[146:149], v[196:199], 0
	v_mfma_f32_16x16x32_f16 v[42:45], v[162:165], v[196:199], 0
	v_mfma_f32_16x16x32_f16 v[30:33], v[146:149], v[204:207], 0
	v_mfma_f32_16x16x32_f16 v[26:29], v[162:165], v[204:207], 0
	v_mfma_f32_16x16x32_f16 v[14:17], v[146:149], v[212:215], 0
	v_mfma_f32_16x16x32_f16 v[10:13], v[162:165], v[212:215], 0
	v_mfma_f32_16x16x32_f16 v[62:65], v[158:161], v[192:195], v[62:65]
	v_mfma_f32_16x16x32_f16 v[58:61], v[166:169], v[192:195], v[58:61]
	v_mfma_f32_16x16x32_f16 v[46:49], v[158:161], v[200:203], v[46:49]
	v_mfma_f32_16x16x32_f16 v[42:45], v[166:169], v[200:203], v[42:45]
	v_mfma_f32_16x16x32_f16 v[30:33], v[158:161], v[208:211], v[30:33]
	v_mfma_f32_16x16x32_f16 v[26:29], v[166:169], v[208:211], v[26:29]
	v_mfma_f32_16x16x32_f16 v[14:17], v[158:161], v[216:219], v[14:17]
	v_mfma_f32_16x16x32_f16 v[10:13], v[166:169], v[216:219], v[10:13]
	s_setprio 0
	s_setprio 1
	v_mfma_f32_16x16x32_f16 v[54:57], v[170:173], v[188:191], 0
	v_mfma_f32_16x16x32_f16 v[50:53], v[178:181], v[188:191], 0
	v_mfma_f32_16x16x32_f16 v[38:41], v[170:173], v[196:199], 0
	v_mfma_f32_16x16x32_f16 v[34:37], v[178:181], v[196:199], 0
	v_mfma_f32_16x16x32_f16 v[22:25], v[170:173], v[204:207], 0
	v_mfma_f32_16x16x32_f16 v[18:21], v[178:181], v[204:207], 0
	v_mfma_f32_16x16x32_f16 v[6:9], v[170:173], v[212:215], 0
	v_mfma_f32_16x16x32_f16 v[2:5], v[178:181], v[212:215], 0
	v_mfma_f32_16x16x32_f16 v[54:57], v[174:177], v[192:195], v[54:57]
	v_mfma_f32_16x16x32_f16 v[50:53], v[182:185], v[192:195], v[50:53]
	v_mfma_f32_16x16x32_f16 v[38:41], v[174:177], v[200:203], v[38:41]
	v_mfma_f32_16x16x32_f16 v[34:37], v[182:185], v[200:203], v[34:37]
	s_setprio 2
	s_barrier
	v_mfma_f32_16x16x32_f16 v[22:25], v[174:177], v[208:211], v[22:25]
	v_mfma_f32_16x16x32_f16 v[18:21], v[182:185], v[208:211], v[18:21]
	v_mfma_f32_16x16x32_f16 v[6:9], v[174:177], v[216:219], v[6:9]
	v_mfma_f32_16x16x32_f16 v[2:5], v[182:185], v[216:219], v[2:5]
	s_setprio 0
	s_nop 0
	s_add_i32 s64, 0, 0x18000
	v_add_u32_e32 v157, s64, v152
	s_add_i32 s65, 0, 0x1c000
	ds_read_b128 v[146:149], v157
	ds_read_b128 v[158:161], v157 offset:1024
	ds_read_b128 v[162:165], v157 offset:2048
	ds_read_b128 v[166:169], v157 offset:3072
	v_add_u32_e32 v157, s65, v152
	ds_read_b128 v[170:173], v157
	ds_read_b128 v[174:177], v157 offset:1024
	ds_read_b128 v[178:181], v157 offset:2048
	ds_read_b128 v[182:185], v157 offset:3072
	s_add_u32 s30, s30, 0x80000
	s_addc_u32 s31, s31, 0
	s_mov_b32 m0, s38
	v_lshl_add_u64 v[226:227], s[30:31], 0, v[130:131]
	ds_read_b128 v[188:191], v156 offset:32768
	ds_read_b128 v[192:195], v156 offset:33792
	ds_read_b128 v[196:199], v156 offset:34816
	ds_read_b128 v[200:203], v156 offset:35840
	ds_read_b128 v[204:207], v156 offset:36864
	ds_read_b128 v[208:211], v156 offset:37888
	ds_read_b128 v[212:215], v156 offset:38912
	ds_read_b128 v[216:219], v156 offset:39936
	global_load_lds_dwordx4 v[226:227], off
	v_lshl_add_u64 v[226:227], s[30:31], 0, v[134:135]
	s_mov_b32 m0, s39
	s_nop 0
	global_load_lds_dwordx4 v[226:227], off
	s_waitcnt vmcnt(8)
	s_waitcnt lgkmcnt(0)
	s_barrier
	s_setprio 1
	s_waitcnt lgkmcnt(0)
	v_mfma_f32_16x16x32_f16 v[126:129], v[146:149], v[188:191], v[126:129]
	v_mfma_f32_16x16x32_f16 v[122:125], v[162:165], v[188:191], v[122:125]
	v_mfma_f32_16x16x32_f16 v[110:113], v[146:149], v[196:199], v[110:113]
	v_mfma_f32_16x16x32_f16 v[106:109], v[162:165], v[196:199], v[106:109]
	v_mfma_f32_16x16x32_f16 v[94:97], v[146:149], v[204:207], v[94:97]
	v_mfma_f32_16x16x32_f16 v[90:93], v[162:165], v[204:207], v[90:93]
	v_mfma_f32_16x16x32_f16 v[78:81], v[146:149], v[212:215], v[78:81]
	v_mfma_f32_16x16x32_f16 v[74:77], v[162:165], v[212:215], v[74:77]
	v_mfma_f32_16x16x32_f16 v[126:129], v[158:161], v[192:195], v[126:129]
	v_mfma_f32_16x16x32_f16 v[122:125], v[166:169], v[192:195], v[122:125]
	v_mfma_f32_16x16x32_f16 v[110:113], v[158:161], v[200:203], v[110:113]
	v_mfma_f32_16x16x32_f16 v[106:109], v[166:169], v[200:203], v[106:109]
	v_mfma_f32_16x16x32_f16 v[94:97], v[158:161], v[208:211], v[94:97]
	v_mfma_f32_16x16x32_f16 v[90:93], v[166:169], v[208:211], v[90:93]
	v_mfma_f32_16x16x32_f16 v[78:81], v[158:161], v[216:219], v[78:81]
	v_mfma_f32_16x16x32_f16 v[74:77], v[166:169], v[216:219], v[74:77]
	s_setprio 0
	s_setprio 1
	v_mfma_f32_16x16x32_f16 v[118:121], v[170:173], v[188:191], v[118:121]
	v_mfma_f32_16x16x32_f16 v[114:117], v[178:181], v[188:191], v[114:117]
	v_mfma_f32_16x16x32_f16 v[102:105], v[170:173], v[196:199], v[102:105]
	v_mfma_f32_16x16x32_f16 v[98:101], v[178:181], v[196:199], v[98:101]
	v_mfma_f32_16x16x32_f16 v[86:89], v[170:173], v[204:207], v[86:89]
	v_mfma_f32_16x16x32_f16 v[82:85], v[178:181], v[204:207], v[82:85]
	v_mfma_f32_16x16x32_f16 v[70:73], v[170:173], v[212:215], v[70:73]
	v_mfma_f32_16x16x32_f16 v[66:69], v[178:181], v[212:215], v[66:69]
	v_mfma_f32_16x16x32_f16 v[118:121], v[174:177], v[192:195], v[118:121]
	v_mfma_f32_16x16x32_f16 v[114:117], v[182:185], v[192:195], v[114:117]
	v_mfma_f32_16x16x32_f16 v[102:105], v[174:177], v[200:203], v[102:105]
	v_mfma_f32_16x16x32_f16 v[98:101], v[182:185], v[200:203], v[98:101]
	s_setprio 2
	s_barrier
	v_mfma_f32_16x16x32_f16 v[86:89], v[174:177], v[208:211], v[86:89]
	v_mfma_f32_16x16x32_f16 v[82:85], v[182:185], v[208:211], v[82:85]
	v_mfma_f32_16x16x32_f16 v[70:73], v[174:177], v[216:219], v[70:73]
	v_mfma_f32_16x16x32_f16 v[66:69], v[182:185], v[216:219], v[66:69]
	s_setprio 0
	s_nop 0
	s_add_i32 s30, s64, s36
	v_lshl_add_u64 v[150:151], v[150:151], 0, s[10:11]
	s_mov_b32 m0, s30
	ds_read_b128 v[188:191], v156 offset:49152
	ds_read_b128 v[192:195], v156 offset:50176
	ds_read_b128 v[196:199], v156 offset:51200
	ds_read_b128 v[200:203], v156 offset:52224
	ds_read_b128 v[204:207], v156 offset:53248
	ds_read_b128 v[208:211], v156 offset:54272
	ds_read_b128 v[212:215], v156 offset:55296
	ds_read_b128 v[216:219], v156 offset:56320
	global_load_lds_dwordx4 v[150:151], off
	s_add_i32 m0, s30, 0x2000
	s_add_u32 s28, s28, 0x80080
	v_lshl_add_u64 v[150:151], v[220:221], 0, s[10:11]
	s_addc_u32 s29, s29, 0
	s_add_i32 s30, s65, s36
	global_load_lds_dwordx4 v[150:151], off
	v_lshl_add_u64 v[150:151], s[28:29], 0, v[132:133]
	s_mov_b32 m0, s30
	s_nop 0
	global_load_lds_dwordx4 v[150:151], off
	v_lshl_add_u64 v[150:151], s[28:29], 0, v[136:137]
	s_add_i32 m0, s30, 0x2000
	s_nop 0
	global_load_lds_dwordx4 v[150:151], off
	v_lshl_add_u64 v[150:151], v[222:223], 0, s[10:11]
	s_mov_b32 m0, s41
	s_nop 0
	global_load_lds_dwordx4 v[150:151], off
	v_lshl_add_u64 v[150:151], v[224:225], 0, s[10:11]
	s_mov_b32 m0, s46
	s_nop 0
	global_load_lds_dwordx4 v[150:151], off
	s_waitcnt vmcnt(8)
	s_waitcnt lgkmcnt(0)
	s_barrier
	s_setprio 1
	s_waitcnt lgkmcnt(0)
	v_mfma_f32_16x16x32_f16 v[62:65], v[146:149], v[188:191], v[62:65]
	v_mfma_f32_16x16x32_f16 v[58:61], v[162:165], v[188:191], v[58:61]
	v_mfma_f32_16x16x32_f16 v[46:49], v[146:149], v[196:199], v[46:49]
	v_mfma_f32_16x16x32_f16 v[42:45], v[162:165], v[196:199], v[42:45]
	v_mfma_f32_16x16x32_f16 v[30:33], v[146:149], v[204:207], v[30:33]
	v_mfma_f32_16x16x32_f16 v[26:29], v[162:165], v[204:207], v[26:29]
	v_mfma_f32_16x16x32_f16 v[14:17], v[146:149], v[212:215], v[14:17]
	v_mfma_f32_16x16x32_f16 v[10:13], v[162:165], v[212:215], v[10:13]
	v_mfma_f32_16x16x32_f16 v[62:65], v[158:161], v[192:195], v[62:65]
	v_mfma_f32_16x16x32_f16 v[58:61], v[166:169], v[192:195], v[58:61]
	v_mfma_f32_16x16x32_f16 v[46:49], v[158:161], v[200:203], v[46:49]
	v_mfma_f32_16x16x32_f16 v[42:45], v[166:169], v[200:203], v[42:45]
	v_mfma_f32_16x16x32_f16 v[30:33], v[158:161], v[208:211], v[30:33]
	v_mfma_f32_16x16x32_f16 v[26:29], v[166:169], v[208:211], v[26:29]
	v_mfma_f32_16x16x32_f16 v[14:17], v[158:161], v[216:219], v[14:17]
	v_mfma_f32_16x16x32_f16 v[10:13], v[166:169], v[216:219], v[10:13]
	s_setprio 0
	s_setprio 1
	v_mfma_f32_16x16x32_f16 v[54:57], v[170:173], v[188:191], v[54:57]
	v_mfma_f32_16x16x32_f16 v[50:53], v[178:181], v[188:191], v[50:53]
	v_mfma_f32_16x16x32_f16 v[38:41], v[170:173], v[196:199], v[38:41]
	v_mfma_f32_16x16x32_f16 v[34:37], v[178:181], v[196:199], v[34:37]
	v_mfma_f32_16x16x32_f16 v[22:25], v[170:173], v[204:207], v[22:25]
	v_mfma_f32_16x16x32_f16 v[18:21], v[178:181], v[204:207], v[18:21]
	v_mfma_f32_16x16x32_f16 v[6:9], v[170:173], v[212:215], v[6:9]
	v_mfma_f32_16x16x32_f16 v[2:5], v[178:181], v[212:215], v[2:5]
	v_mfma_f32_16x16x32_f16 v[54:57], v[174:177], v[192:195], v[54:57]
	v_mfma_f32_16x16x32_f16 v[50:53], v[182:185], v[192:195], v[50:53]
	v_mfma_f32_16x16x32_f16 v[38:41], v[174:177], v[200:203], v[38:41]
	v_mfma_f32_16x16x32_f16 v[34:37], v[182:185], v[200:203], v[34:37]
	s_setprio 2
	s_barrier
	v_mfma_f32_16x16x32_f16 v[22:25], v[174:177], v[208:211], v[22:25]
	v_mfma_f32_16x16x32_f16 v[18:21], v[182:185], v[208:211], v[18:21]
	v_mfma_f32_16x16x32_f16 v[6:9], v[174:177], v[216:219], v[6:9]
	v_mfma_f32_16x16x32_f16 v[2:5], v[182:185], v[216:219], v[2:5]
	s_setprio 0
	s_nop 0
	s_add_i32 s63, s63, 2
	s_add_u32 s26, s26, 0x100
	s_addc_u32 s27, s27, 0
	s_add_u32 s61, s61, 0x100
	s_addc_u32 s62, s62, 0
	s_cmp_gt_u32 s63, 29
	s_cbranch_scc0 .LBB0_628
	s_branch .Lpeel_exit_1

.Lpeel_exit_1:
	s_and_b64 vcc, exec, s[12:13]
	s_cbranch_vccz .LBB0_631
	s_barrier

.LBB0_757:
	s_ashr_i32 s19, s18, 31
	s_lshl_b64 s[20:21], s[18:19], 20
	s_add_u32 s20, s82, s20
	s_addc_u32 s21, s83, s21
	s_and_b64 s[22:23], s[6:7], exec
	s_cselect_b32 s19, s21, s27
	s_cselect_b32 s49, s20, s26
	s_ashr_i32 s17, s16, 31
	s_lshl_b64 s[22:23], s[16:17], 20
	s_add_u32 s22, s3, s22
	s_addc_u32 s23, s33, s23
	s_and_b64 s[30:31], s[6:7], exec
	s_cselect_b32 s17, s23, s29
	s_cselect_b32 s50, s22, s28
	s_add_u32 s26, s26, 0x80080
	s_addc_u32 s27, s27, 0
	s_add_u32 s51, s28, 0x100
	s_addc_u32 s60, s29, 0
	s_mov_b32 s61, -2
	ds_read_b128 v[146:149], v152
	ds_read_b128 v[156:159], v152 offset:1024
	ds_read_b128 v[160:163], v152 offset:2048
	ds_read_b128 v[164:167], v152 offset:3072
	ds_read_b128 v[168:171], v153
	ds_read_b128 v[172:175], v153 offset:1024
	ds_read_b128 v[176:179], v153 offset:2048
	ds_read_b128 v[180:183], v153 offset:3072
	s_add_u32 s28, s26, 0xfff80080
	s_addc_u32 s29, s27, -1
	s_cmp_eq_u32 s61, 28
	s_cselect_b32 s31, s19, s29
	s_cselect_b32 s30, s49, s28
	s_cselect_b32 s29, s17, s60
	s_cselect_b32 s28, s50, s51
	v_lshl_add_u64 v[184:185], s[26:27], 0, v[138:139]
	s_add_i32 m0, s25, 0xc000
	ds_read_b128 v[188:191], v154
	ds_read_b128 v[192:195], v154 offset:1024
	ds_read_b128 v[196:199], v154 offset:2048
	ds_read_b128 v[200:203], v154 offset:3072
	ds_read_b128 v[204:207], v154 offset:4096
	ds_read_b128 v[208:211], v154 offset:5120
	ds_read_b128 v[212:215], v154 offset:6144
	ds_read_b128 v[216:219], v154 offset:7168
	global_load_lds_dwordx4 v[184:185], off
	v_lshl_add_u64 v[184:185], s[26:27], 0, v[140:141]
	s_add_i32 m0, s25, 0xe000
	s_nop 0
	global_load_lds_dwordx4 v[184:185], off
	s_waitcnt vmcnt(8)
	s_waitcnt lgkmcnt(0)
	s_barrier
	s_setprio 1
	s_waitcnt lgkmcnt(0)
	v_mfma_f32_16x16x32_f16 v[126:129], v[146:149], v[188:191], 0
	v_mfma_f32_16x16x32_f16 v[122:125], v[160:163], v[188:191], 0
	v_mfma_f32_16x16x32_f16 v[110:113], v[146:149], v[196:199], 0
	v_mfma_f32_16x16x32_f16 v[106:109], v[160:163], v[196:199], 0
	v_mfma_f32_16x16x32_f16 v[94:97], v[146:149], v[204:207], 0
	v_mfma_f32_16x16x32_f16 v[90:93], v[160:163], v[204:207], 0
	v_mfma_f32_16x16x32_f16 v[78:81], v[146:149], v[212:215], 0
	v_mfma_f32_16x16x32_f16 v[74:77], v[160:163], v[212:215], 0
	v_mfma_f32_16x16x32_f16 v[126:129], v[156:159], v[192:195], v[126:129]
	v_mfma_f32_16x16x32_f16 v[122:125], v[164:167], v[192:195], v[122:125]
	v_mfma_f32_16x16x32_f16 v[110:113], v[156:159], v[200:203], v[110:113]
	v_mfma_f32_16x16x32_f16 v[106:109], v[164:167], v[200:203], v[106:109]
	v_mfma_f32_16x16x32_f16 v[94:97], v[156:159], v[208:211], v[94:97]
	v_mfma_f32_16x16x32_f16 v[90:93], v[164:167], v[208:211], v[90:93]
	v_mfma_f32_16x16x32_f16 v[78:81], v[156:159], v[216:219], v[78:81]
	v_mfma_f32_16x16x32_f16 v[74:77], v[164:167], v[216:219], v[74:77]
	s_setprio 0
	s_setprio 1
	v_mfma_f32_16x16x32_f16 v[118:121], v[168:171], v[188:191], 0
	v_mfma_f32_16x16x32_f16 v[114:117], v[176:179], v[188:191], 0
	v_mfma_f32_16x16x32_f16 v[102:105], v[168:171], v[196:199], 0
	v_mfma_f32_16x16x32_f16 v[98:101], v[176:179], v[196:199], 0
	v_mfma_f32_16x16x32_f16 v[86:89], v[168:171], v[204:207], 0
	v_mfma_f32_16x16x32_f16 v[82:85], v[176:179], v[204:207], 0
	v_mfma_f32_16x16x32_f16 v[70:73], v[168:171], v[212:215], 0
	v_mfma_f32_16x16x32_f16 v[66:69], v[176:179], v[212:215], 0
	v_mfma_f32_16x16x32_f16 v[118:121], v[172:175], v[192:195], v[118:121]
	v_mfma_f32_16x16x32_f16 v[114:117], v[180:183], v[192:195], v[114:117]
	v_mfma_f32_16x16x32_f16 v[102:105], v[172:175], v[200:203], v[102:105]
	v_mfma_f32_16x16x32_f16 v[98:101], v[180:183], v[200:203], v[98:101]
	s_setprio 2
	s_barrier
	v_mfma_f32_16x16x32_f16 v[86:89], v[172:175], v[208:211], v[86:89]
	v_mfma_f32_16x16x32_f16 v[82:85], v[180:183], v[208:211], v[82:85]
	v_mfma_f32_16x16x32_f16 v[70:73], v[172:175], v[216:219], v[70:73]
	v_mfma_f32_16x16x32_f16 v[66:69], v[180:183], v[216:219], v[66:69]
	s_setprio 0
	s_nop 0
	s_add_i32 s62, s44, s34
	v_lshl_add_u64 v[184:185], s[28:29], 0, v[134:135]
	s_mov_b32 m0, s62
	ds_read_b128 v[188:191], v154 offset:16384
	ds_read_b128 v[192:195], v154 offset:17408
	ds_read_b128 v[196:199], v154 offset:18432
	ds_read_b128 v[200:203], v154 offset:19456
	ds_read_b128 v[204:207], v154 offset:20480
	ds_read_b128 v[208:211], v154 offset:21504
	ds_read_b128 v[212:215], v154 offset:22528
	ds_read_b128 v[216:219], v154 offset:23552
	global_load_lds_dwordx4 v[184:185], off
	s_add_i32 m0, s62, 0x2000
	s_add_u32 s62, s28, 0x80000
	v_lshl_add_u64 v[220:221], s[28:29], 0, v[130:131]
	s_addc_u32 s63, s29, 0
	s_add_i32 s64, s45, s34
	global_load_lds_dwordx4 v[220:221], off
	v_lshl_add_u64 v[222:223], s[62:63], 0, v[134:135]
	s_mov_b32 m0, s64
	v_lshl_add_u64 v[224:225], s[30:31], 0, v[132:133]
	global_load_lds_dwordx4 v[222:223], off
	v_lshl_add_u64 v[222:223], s[62:63], 0, v[130:131]
	s_add_i32 m0, s64, 0x2000
	s_nop 0
	global_load_lds_dwordx4 v[222:223], off
	v_lshl_add_u64 v[222:223], s[30:31], 0, v[136:137]
	s_mov_b32 m0, s25
	s_nop 0
	global_load_lds_dwordx4 v[222:223], off
	s_mov_b32 m0, s37
	s_nop 0
	global_load_lds_dwordx4 v[224:225], off
	s_waitcnt vmcnt(8)
	s_waitcnt lgkmcnt(0)
	s_barrier
	s_setprio 1
	s_waitcnt lgkmcnt(0)
	v_mfma_f32_16x16x32_f16 v[62:65], v[146:149], v[188:191], 0
	v_mfma_f32_16x16x32_f16 v[58:61], v[160:163], v[188:191], 0
	v_mfma_f32_16x16x32_f16 v[46:49], v[146:149], v[196:199], 0
	v_mfma_f32_16x16x32_f16 v[42:45], v[160:163], v[196:199], 0
	v_mfma_f32_16x16x32_f16 v[30:33], v[146:149], v[204:207], 0
	v_mfma_f32_16x16x32_f16 v[26:29], v[160:163], v[204:207], 0
	v_mfma_f32_16x16x32_f16 v[14:17], v[146:149], v[212:215], 0
	v_mfma_f32_16x16x32_f16 v[10:13], v[160:163], v[212:215], 0
	v_mfma_f32_16x16x32_f16 v[62:65], v[156:159], v[192:195], v[62:65]
	v_mfma_f32_16x16x32_f16 v[58:61], v[164:167], v[192:195], v[58:61]
	v_mfma_f32_16x16x32_f16 v[46:49], v[156:159], v[200:203], v[46:49]
	v_mfma_f32_16x16x32_f16 v[42:45], v[164:167], v[200:203], v[42:45]
	v_mfma_f32_16x16x32_f16 v[30:33], v[156:159], v[208:211], v[30:33]
	v_mfma_f32_16x16x32_f16 v[26:29], v[164:167], v[208:211], v[26:29]
	v_mfma_f32_16x16x32_f16 v[14:17], v[156:159], v[216:219], v[14:17]
	v_mfma_f32_16x16x32_f16 v[10:13], v[164:167], v[216:219], v[10:13]
	s_setprio 0
	s_setprio 1
	v_mfma_f32_16x16x32_f16 v[54:57], v[168:171], v[188:191], 0
	v_mfma_f32_16x16x32_f16 v[50:53], v[176:179], v[188:191], 0
	v_mfma_f32_16x16x32_f16 v[38:41], v[168:171], v[196:199], 0
	v_mfma_f32_16x16x32_f16 v[34:37], v[176:179], v[196:199], 0
	v_mfma_f32_16x16x32_f16 v[22:25], v[168:171], v[204:207], 0
	v_mfma_f32_16x16x32_f16 v[18:21], v[176:179], v[204:207], 0
	v_mfma_f32_16x16x32_f16 v[6:9], v[168:171], v[212:215], 0
	v_mfma_f32_16x16x32_f16 v[2:5], v[176:179], v[212:215], 0
	v_mfma_f32_16x16x32_f16 v[54:57], v[172:175], v[192:195], v[54:57]
	v_mfma_f32_16x16x32_f16 v[50:53], v[180:183], v[192:195], v[50:53]
	v_mfma_f32_16x16x32_f16 v[38:41], v[172:175], v[200:203], v[38:41]
	v_mfma_f32_16x16x32_f16 v[34:37], v[180:183], v[200:203], v[34:37]
	s_setprio 2
	s_barrier
	v_mfma_f32_16x16x32_f16 v[22:25], v[172:175], v[208:211], v[22:25]
	v_mfma_f32_16x16x32_f16 v[18:21], v[180:183], v[208:211], v[18:21]
	v_mfma_f32_16x16x32_f16 v[6:9], v[172:175], v[216:219], v[6:9]
	v_mfma_f32_16x16x32_f16 v[2:5], v[180:183], v[216:219], v[2:5]
	s_setprio 0
	s_nop 0
	s_add_i32 s62, 0, 0x18000
	s_add_i32 s63, 0, 0x1c000
	v_add_u32_e32 v164, s62, v150
	v_add_u32_e32 v180, s63, v150
	ds_read_b128 v[146:149], v164
	ds_read_b128 v[156:159], v164 offset:1024
	ds_read_b128 v[160:163], v164 offset:2048
	ds_read_b128 v[164:167], v164 offset:3072
	ds_read_b128 v[168:171], v180
	ds_read_b128 v[172:175], v180 offset:1024
	ds_read_b128 v[176:179], v180 offset:2048
	ds_read_b128 v[180:183], v180 offset:3072
	s_add_u32 s30, s30, 0x80000
	s_addc_u32 s31, s31, 0
	s_mov_b32 m0, s38
	v_lshl_add_u64 v[226:227], s[30:31], 0, v[136:137]
	ds_read_b128 v[188:191], v154 offset:32768
	ds_read_b128 v[192:195], v154 offset:33792
	ds_read_b128 v[196:199], v154 offset:34816
	ds_read_b128 v[200:203], v154 offset:35840
	ds_read_b128 v[204:207], v154 offset:36864
	ds_read_b128 v[208:211], v154 offset:37888
	ds_read_b128 v[212:215], v154 offset:38912
	ds_read_b128 v[216:219], v154 offset:39936
	global_load_lds_dwordx4 v[226:227], off
	v_lshl_add_u64 v[226:227], s[30:31], 0, v[132:133]
	s_mov_b32 m0, s39
	s_nop 0
	global_load_lds_dwordx4 v[226:227], off
	s_waitcnt vmcnt(8)
	s_waitcnt lgkmcnt(0)
	s_barrier
	s_setprio 1
	s_waitcnt lgkmcnt(0)
	v_mfma_f32_16x16x32_f16 v[126:129], v[146:149], v[188:191], v[126:129]
	v_mfma_f32_16x16x32_f16 v[122:125], v[160:163], v[188:191], v[122:125]
	v_mfma_f32_16x16x32_f16 v[110:113], v[146:149], v[196:199], v[110:113]
	v_mfma_f32_16x16x32_f16 v[106:109], v[160:163], v[196:199], v[106:109]
	v_mfma_f32_16x16x32_f16 v[94:97], v[146:149], v[204:207], v[94:97]
	v_mfma_f32_16x16x32_f16 v[90:93], v[160:163], v[204:207], v[90:93]
	v_mfma_f32_16x16x32_f16 v[78:81], v[146:149], v[212:215], v[78:81]
	v_mfma_f32_16x16x32_f16 v[74:77], v[160:163], v[212:215], v[74:77]
	v_mfma_f32_16x16x32_f16 v[126:129], v[156:159], v[192:195], v[126:129]
	v_mfma_f32_16x16x32_f16 v[122:125], v[164:167], v[192:195], v[122:125]
	v_mfma_f32_16x16x32_f16 v[110:113], v[156:159], v[200:203], v[110:113]
	v_mfma_f32_16x16x32_f16 v[106:109], v[164:167], v[200:203], v[106:109]
	v_mfma_f32_16x16x32_f16 v[94:97], v[156:159], v[208:211], v[94:97]
	v_mfma_f32_16x16x32_f16 v[90:93], v[164:167], v[208:211], v[90:93]
	v_mfma_f32_16x16x32_f16 v[78:81], v[156:159], v[216:219], v[78:81]
	v_mfma_f32_16x16x32_f16 v[74:77], v[164:167], v[216:219], v[74:77]
	s_setprio 0
	s_setprio 1
	v_mfma_f32_16x16x32_f16 v[118:121], v[168:171], v[188:191], v[118:121]
	v_mfma_f32_16x16x32_f16 v[114:117], v[176:179], v[188:191], v[114:117]
	v_mfma_f32_16x16x32_f16 v[102:105], v[168:171], v[196:199], v[102:105]
	v_mfma_f32_16x16x32_f16 v[98:101], v[176:179], v[196:199], v[98:101]
	v_mfma_f32_16x16x32_f16 v[86:89], v[168:171], v[204:207], v[86:89]
	v_mfma_f32_16x16x32_f16 v[82:85], v[176:179], v[204:207], v[82:85]
	v_mfma_f32_16x16x32_f16 v[70:73], v[168:171], v[212:215], v[70:73]
	v_mfma_f32_16x16x32_f16 v[66:69], v[176:179], v[212:215], v[66:69]
	v_mfma_f32_16x16x32_f16 v[118:121], v[172:175], v[192:195], v[118:121]
	v_mfma_f32_16x16x32_f16 v[114:117], v[180:183], v[192:195], v[114:117]
	v_mfma_f32_16x16x32_f16 v[102:105], v[172:175], v[200:203], v[102:105]
	v_mfma_f32_16x16x32_f16 v[98:101], v[180:183], v[200:203], v[98:101]
	s_setprio 2
	s_barrier
	v_mfma_f32_16x16x32_f16 v[86:89], v[172:175], v[208:211], v[86:89]
	v_mfma_f32_16x16x32_f16 v[82:85], v[180:183], v[208:211], v[82:85]
	v_mfma_f32_16x16x32_f16 v[70:73], v[172:175], v[216:219], v[70:73]
	v_mfma_f32_16x16x32_f16 v[66:69], v[180:183], v[216:219], v[66:69]
	s_setprio 0
	s_nop 0
	s_add_i32 s30, s62, s34
	v_lshl_add_u64 v[184:185], v[184:185], 0, s[12:13]
	s_mov_b32 m0, s30
	ds_read_b128 v[188:191], v154 offset:49152
	ds_read_b128 v[192:195], v154 offset:50176
	ds_read_b128 v[196:199], v154 offset:51200
	ds_read_b128 v[200:203], v154 offset:52224
	ds_read_b128 v[204:207], v154 offset:53248
	ds_read_b128 v[208:211], v154 offset:54272
	ds_read_b128 v[212:215], v154 offset:55296
	ds_read_b128 v[216:219], v154 offset:56320
	global_load_lds_dwordx4 v[184:185], off
	s_add_i32 m0, s30, 0x2000
	s_add_u32 s28, s28, 0x80080
	v_lshl_add_u64 v[184:185], v[220:221], 0, s[12:13]
	s_addc_u32 s29, s29, 0
	s_add_i32 s30, s63, s34
	global_load_lds_dwordx4 v[184:185], off
	v_lshl_add_u64 v[184:185], s[28:29], 0, v[134:135]
	s_mov_b32 m0, s30
	s_nop 0
	global_load_lds_dwordx4 v[184:185], off
	v_lshl_add_u64 v[184:185], s[28:29], 0, v[130:131]
	s_add_i32 m0, s30, 0x2000
	s_nop 0
	global_load_lds_dwordx4 v[184:185], off
	v_lshl_add_u64 v[184:185], v[222:223], 0, s[12:13]
	s_mov_b32 m0, s41
	s_nop 0
	global_load_lds_dwordx4 v[184:185], off
	v_lshl_add_u64 v[184:185], v[224:225], 0, s[12:13]
	s_mov_b32 m0, s42
	s_nop 0
	global_load_lds_dwordx4 v[184:185], off
	s_waitcnt vmcnt(8)
	s_waitcnt lgkmcnt(0)
	s_barrier
	s_setprio 1
	s_waitcnt lgkmcnt(0)
	v_mfma_f32_16x16x32_f16 v[62:65], v[146:149], v[188:191], v[62:65]
	v_mfma_f32_16x16x32_f16 v[58:61], v[160:163], v[188:191], v[58:61]
	v_mfma_f32_16x16x32_f16 v[46:49], v[146:149], v[196:199], v[46:49]
	v_mfma_f32_16x16x32_f16 v[42:45], v[160:163], v[196:199], v[42:45]
	v_mfma_f32_16x16x32_f16 v[30:33], v[146:149], v[204:207], v[30:33]
	v_mfma_f32_16x16x32_f16 v[26:29], v[160:163], v[204:207], v[26:29]
	v_mfma_f32_16x16x32_f16 v[14:17], v[146:149], v[212:215], v[14:17]
	v_mfma_f32_16x16x32_f16 v[10:13], v[160:163], v[212:215], v[10:13]
	v_mfma_f32_16x16x32_f16 v[62:65], v[156:159], v[192:195], v[62:65]
	v_mfma_f32_16x16x32_f16 v[58:61], v[164:167], v[192:195], v[58:61]
	v_mfma_f32_16x16x32_f16 v[46:49], v[156:159], v[200:203], v[46:49]
	v_mfma_f32_16x16x32_f16 v[42:45], v[164:167], v[200:203], v[42:45]
	v_mfma_f32_16x16x32_f16 v[30:33], v[156:159], v[208:211], v[30:33]
	v_mfma_f32_16x16x32_f16 v[26:29], v[164:167], v[208:211], v[26:29]
	v_mfma_f32_16x16x32_f16 v[14:17], v[156:159], v[216:219], v[14:17]
	v_mfma_f32_16x16x32_f16 v[10:13], v[164:167], v[216:219], v[10:13]
	s_setprio 0
	s_setprio 1
	v_mfma_f32_16x16x32_f16 v[54:57], v[168:171], v[188:191], v[54:57]
	v_mfma_f32_16x16x32_f16 v[50:53], v[176:179], v[188:191], v[50:53]
	v_mfma_f32_16x16x32_f16 v[38:41], v[168:171], v[196:199], v[38:41]
	v_mfma_f32_16x16x32_f16 v[34:37], v[176:179], v[196:199], v[34:37]
	v_mfma_f32_16x16x32_f16 v[22:25], v[168:171], v[204:207], v[22:25]
	v_mfma_f32_16x16x32_f16 v[18:21], v[176:179], v[204:207], v[18:21]
	v_mfma_f32_16x16x32_f16 v[6:9], v[168:171], v[212:215], v[6:9]
	v_mfma_f32_16x16x32_f16 v[2:5], v[176:179], v[212:215], v[2:5]
	v_mfma_f32_16x16x32_f16 v[54:57], v[172:175], v[192:195], v[54:57]
	v_mfma_f32_16x16x32_f16 v[50:53], v[180:183], v[192:195], v[50:53]
	v_mfma_f32_16x16x32_f16 v[38:41], v[172:175], v[200:203], v[38:41]
	v_mfma_f32_16x16x32_f16 v[34:37], v[180:183], v[200:203], v[34:37]
	s_setprio 2
	s_barrier
	v_mfma_f32_16x16x32_f16 v[22:25], v[172:175], v[208:211], v[22:25]
	v_mfma_f32_16x16x32_f16 v[18:21], v[180:183], v[208:211], v[18:21]
	v_mfma_f32_16x16x32_f16 v[6:9], v[172:175], v[216:219], v[6:9]
	v_mfma_f32_16x16x32_f16 v[2:5], v[180:183], v[216:219], v[2:5]
	s_setprio 0
	s_nop 0
	s_add_i32 s61, s61, 2
	s_add_u32 s26, s26, 0x100
	s_addc_u32 s27, s27, 0
	s_add_u32 s51, s51, 0x100
	s_addc_u32 s60, s60, 0
	s_cmp_gt_u32 s61, 29
	s_cbranch_scc0 .LBB0_758
	s_branch .Lpeel_exit_2

.LBB0_840:
	s_add_u32 s22, s22, 0xb0080
	s_addc_u32 s23, s23, 0
	s_add_u32 s46, s24, 0x100
	s_addc_u32 s47, s25, 0
	s_mov_b32 s48, -2
	ds_read_b128 v[26:29], v190
	ds_read_b128 v[30:33], v190 offset:1024
	ds_read_b128 v[18:21], v190 offset:2048
	ds_read_b128 v[22:25], v190 offset:3072
	ds_read_b128 v[10:13], v191
	ds_read_b128 v[14:17], v191 offset:1024
	ds_read_b128 v[2:5], v191 offset:2048
	ds_read_b128 v[6:9], v191 offset:3072
	s_add_u32 s24, s22, 0xfff50080
	s_addc_u32 s25, s23, -1
	s_cmp_eq_u32 s48, 40
	s_cselect_b32 s27, s9, s25
	s_cselect_b32 s26, s8, s24
	s_cselect_b32 s25, s21, s47
	s_cselect_b32 s24, s20, s46
	v_lshl_add_u64 v[218:219], s[22:23], 0, v[170:171]
	s_add_i32 m0, s31, 0xc000
	ds_read_b128 v[178:181], v192
	ds_read_b128 v[182:185], v192 offset:1024
	ds_read_b128 v[194:197], v192 offset:2048
	ds_read_b128 v[198:201], v192 offset:3072
	ds_read_b128 v[202:205], v192 offset:4096
	ds_read_b128 v[206:209], v192 offset:5120
	ds_read_b128 v[210:213], v192 offset:6144
	ds_read_b128 v[214:217], v192 offset:7168
	global_load_lds_dwordx4 v[218:219], off
	v_lshl_add_u64 v[218:219], s[22:23], 0, v[172:173]
	s_add_i32 m0, s31, 0xe000
	s_nop 0
	global_load_lds_dwordx4 v[218:219], off
	s_waitcnt vmcnt(8)
	s_waitcnt lgkmcnt(0)
	s_barrier
	s_setprio 1
	s_waitcnt lgkmcnt(0)
	v_mfma_f32_16x16x128_f8f6f4 v[158:161], v[26:33], v[178:185], 0
	v_mfma_f32_16x16x128_f8f6f4 v[154:157], v[18:25], v[178:185], 0
	v_mfma_f32_16x16x128_f8f6f4 v[142:145], v[26:33], v[194:201], 0
	v_mfma_f32_16x16x128_f8f6f4 v[138:141], v[18:25], v[194:201], 0
	v_mfma_f32_16x16x128_f8f6f4 v[126:129], v[26:33], v[202:209], 0
	v_mfma_f32_16x16x128_f8f6f4 v[122:125], v[18:25], v[202:209], 0
	v_mfma_f32_16x16x128_f8f6f4 v[110:113], v[26:33], v[210:217], 0
	v_mfma_f32_16x16x128_f8f6f4 v[106:109], v[18:25], v[210:217], 0
	s_setprio 0
	s_setprio 1
	v_mfma_f32_16x16x128_f8f6f4 v[150:153], v[10:17], v[178:185], 0
	v_mfma_f32_16x16x128_f8f6f4 v[146:149], v[2:9], v[178:185], 0
	v_mfma_f32_16x16x128_f8f6f4 v[134:137], v[10:17], v[194:201], 0
	v_mfma_f32_16x16x128_f8f6f4 v[130:133], v[2:9], v[194:201], 0
	v_mfma_f32_16x16x128_f8f6f4 v[118:121], v[10:17], v[202:209], 0
	v_mfma_f32_16x16x128_f8f6f4 v[114:117], v[2:9], v[202:209], 0
	s_setprio 2
	s_barrier
	v_mfma_f32_16x16x128_f8f6f4 v[102:105], v[10:17], v[210:217], 0
	v_mfma_f32_16x16x128_f8f6f4 v[98:101], v[2:9], v[210:217], 0
	s_setprio 0
	s_nop 0
	s_add_i32 s49, s40, s30
	v_lshl_add_u64 v[178:179], s[24:25], 0, v[164:165]
	s_mov_b32 m0, s49
	ds_read_b128 v[194:197], v192 offset:16384
	ds_read_b128 v[198:201], v192 offset:17408
	ds_read_b128 v[202:205], v192 offset:18432
	ds_read_b128 v[206:209], v192 offset:19456
	ds_read_b128 v[210:213], v192 offset:20480
	ds_read_b128 v[214:217], v192 offset:21504
	ds_read_b128 v[218:221], v192 offset:22528
	ds_read_b128 v[222:225], v192 offset:23552
	global_load_lds_dwordx4 v[178:179], off
	s_add_i32 m0, s49, 0x2000
	s_add_u32 s50, s24, 0xb0000
	v_lshl_add_u64 v[180:181], s[24:25], 0, v[168:169]
	s_addc_u32 s51, s25, 0
	s_add_i32 s49, s41, s30
	global_load_lds_dwordx4 v[180:181], off
	v_lshl_add_u64 v[182:183], s[50:51], 0, v[164:165]
	s_mov_b32 m0, s49
	v_lshl_add_u64 v[184:185], s[26:27], 0, v[166:167]
	global_load_lds_dwordx4 v[182:183], off
	v_lshl_add_u64 v[182:183], s[50:51], 0, v[168:169]
	s_add_i32 m0, s49, 0x2000
	s_nop 0
	global_load_lds_dwordx4 v[182:183], off
	v_lshl_add_u64 v[182:183], s[26:27], 0, v[162:163]
	s_mov_b32 m0, s31
	s_nop 0
	global_load_lds_dwordx4 v[182:183], off
	s_mov_b32 m0, s33
	s_nop 0
	global_load_lds_dwordx4 v[184:185], off
	s_waitcnt vmcnt(8)
	s_waitcnt lgkmcnt(0)
	s_barrier
	s_setprio 1
	s_waitcnt lgkmcnt(0)
	v_mfma_f32_16x16x128_f8f6f4 v[94:97], v[26:33], v[194:201], 0
	v_mfma_f32_16x16x128_f8f6f4 v[90:93], v[18:25], v[194:201], 0
	v_mfma_f32_16x16x128_f8f6f4 v[78:81], v[26:33], v[202:209], 0
	v_mfma_f32_16x16x128_f8f6f4 v[74:77], v[18:25], v[202:209], 0
	v_mfma_f32_16x16x128_f8f6f4 v[62:65], v[26:33], v[210:217], 0
	v_mfma_f32_16x16x128_f8f6f4 v[58:61], v[18:25], v[210:217], 0
	v_mfma_f32_16x16x128_f8f6f4 v[46:49], v[26:33], v[218:225], 0
	v_mfma_f32_16x16x128_f8f6f4 v[42:45], v[18:25], v[218:225], 0
	s_setprio 0
	s_setprio 1
	v_mfma_f32_16x16x128_f8f6f4 v[86:89], v[10:17], v[194:201], 0
	v_mfma_f32_16x16x128_f8f6f4 v[82:85], v[2:9], v[194:201], 0
	v_mfma_f32_16x16x128_f8f6f4 v[70:73], v[10:17], v[202:209], 0
	v_mfma_f32_16x16x128_f8f6f4 v[66:69], v[2:9], v[202:209], 0
	v_mfma_f32_16x16x128_f8f6f4 v[54:57], v[10:17], v[210:217], 0
	v_mfma_f32_16x16x128_f8f6f4 v[50:53], v[2:9], v[210:217], 0
	s_setprio 2
	s_barrier
	v_mfma_f32_16x16x128_f8f6f4 v[38:41], v[10:17], v[218:225], 0
	v_mfma_f32_16x16x128_f8f6f4 v[34:37], v[2:9], v[218:225], 0
	s_setprio 0
	s_nop 0
	s_add_i32 s49, 0, 0x18000
	s_add_i32 s50, 0, 0x1c000
	v_add_u32_e32 v14, s49, v188
	v_add_u32_e32 v30, s50, v188
	ds_read_b128 v[2:5], v14
	ds_read_b128 v[6:9], v14 offset:1024
	ds_read_b128 v[10:13], v14 offset:2048
	ds_read_b128 v[14:17], v14 offset:3072
	ds_read_b128 v[18:21], v30
	ds_read_b128 v[22:25], v30 offset:1024
	ds_read_b128 v[26:29], v30 offset:2048
	ds_read_b128 v[30:33], v30 offset:3072
	s_add_u32 s26, s26, 0xb0000
	s_addc_u32 s27, s27, 0
	s_mov_b32 m0, s34
	v_lshl_add_u64 v[226:227], s[26:27], 0, v[162:163]
	ds_read_b128 v[194:197], v192 offset:32768
	ds_read_b128 v[198:201], v192 offset:33792
	ds_read_b128 v[202:205], v192 offset:34816
	ds_read_b128 v[206:209], v192 offset:35840
	ds_read_b128 v[210:213], v192 offset:36864
	ds_read_b128 v[214:217], v192 offset:37888
	ds_read_b128 v[218:221], v192 offset:38912
	ds_read_b128 v[222:225], v192 offset:39936
	global_load_lds_dwordx4 v[226:227], off
	v_lshl_add_u64 v[226:227], s[26:27], 0, v[166:167]
	s_mov_b32 m0, s35
	s_nop 0
	global_load_lds_dwordx4 v[226:227], off
	s_waitcnt vmcnt(8)
	s_waitcnt lgkmcnt(0)
	s_barrier
	s_setprio 1
	s_waitcnt lgkmcnt(0)
	v_mfma_f32_16x16x128_f8f6f4 v[158:161], v[2:9], v[194:201], v[158:161]
	v_mfma_f32_16x16x128_f8f6f4 v[154:157], v[10:17], v[194:201], v[154:157]
	v_mfma_f32_16x16x128_f8f6f4 v[142:145], v[2:9], v[202:209], v[142:145]
	v_mfma_f32_16x16x128_f8f6f4 v[138:141], v[10:17], v[202:209], v[138:141]
	v_mfma_f32_16x16x128_f8f6f4 v[126:129], v[2:9], v[210:217], v[126:129]
	v_mfma_f32_16x16x128_f8f6f4 v[122:125], v[10:17], v[210:217], v[122:125]
	v_mfma_f32_16x16x128_f8f6f4 v[110:113], v[2:9], v[218:225], v[110:113]
	v_mfma_f32_16x16x128_f8f6f4 v[106:109], v[10:17], v[218:225], v[106:109]
	s_setprio 0
	s_setprio 1
	v_mfma_f32_16x16x128_f8f6f4 v[150:153], v[18:25], v[194:201], v[150:153]
	v_mfma_f32_16x16x128_f8f6f4 v[146:149], v[26:33], v[194:201], v[146:149]
	v_mfma_f32_16x16x128_f8f6f4 v[134:137], v[18:25], v[202:209], v[134:137]
	v_mfma_f32_16x16x128_f8f6f4 v[130:133], v[26:33], v[202:209], v[130:133]
	v_mfma_f32_16x16x128_f8f6f4 v[118:121], v[18:25], v[210:217], v[118:121]
	v_mfma_f32_16x16x128_f8f6f4 v[114:117], v[26:33], v[210:217], v[114:117]
	s_setprio 2
	s_barrier
	v_mfma_f32_16x16x128_f8f6f4 v[102:105], v[18:25], v[218:225], v[102:105]
	v_mfma_f32_16x16x128_f8f6f4 v[98:101], v[26:33], v[218:225], v[98:101]
	s_setprio 0
	s_nop 0
	s_add_i32 s26, s49, s30
	v_lshl_add_u64 v[178:179], v[178:179], 0, s[12:13]
	s_mov_b32 m0, s26
	ds_read_b128 v[194:197], v192 offset:49152
	ds_read_b128 v[198:201], v192 offset:50176
	ds_read_b128 v[202:205], v192 offset:51200
	ds_read_b128 v[206:209], v192 offset:52224
	ds_read_b128 v[210:213], v192 offset:53248
	ds_read_b128 v[214:217], v192 offset:54272
	ds_read_b128 v[218:221], v192 offset:55296
	ds_read_b128 v[222:225], v192 offset:56320
	global_load_lds_dwordx4 v[178:179], off
	s_add_i32 m0, s26, 0x2000
	s_add_u32 s24, s24, 0xb0080
	v_lshl_add_u64 v[178:179], v[180:181], 0, s[12:13]
	s_addc_u32 s25, s25, 0
	s_add_i32 s26, s50, s30
	global_load_lds_dwordx4 v[178:179], off
	v_lshl_add_u64 v[178:179], s[24:25], 0, v[164:165]
	s_mov_b32 m0, s26
	s_nop 0
	global_load_lds_dwordx4 v[178:179], off
	v_lshl_add_u64 v[178:179], s[24:25], 0, v[168:169]
	s_add_i32 m0, s26, 0x2000
	s_nop 0
	global_load_lds_dwordx4 v[178:179], off
	v_lshl_add_u64 v[178:179], v[182:183], 0, s[12:13]
	s_mov_b32 m0, s37
	s_nop 0
	global_load_lds_dwordx4 v[178:179], off
	v_lshl_add_u64 v[178:179], v[184:185], 0, s[12:13]
	s_mov_b32 m0, s38
	s_nop 0
	global_load_lds_dwordx4 v[178:179], off
	s_waitcnt vmcnt(8)
	s_waitcnt lgkmcnt(0)
	s_barrier
	s_setprio 1
	s_waitcnt lgkmcnt(0)
	v_mfma_f32_16x16x128_f8f6f4 v[94:97], v[2:9], v[194:201], v[94:97]
	v_mfma_f32_16x16x128_f8f6f4 v[90:93], v[10:17], v[194:201], v[90:93]
	v_mfma_f32_16x16x128_f8f6f4 v[78:81], v[2:9], v[202:209], v[78:81]
	v_mfma_f32_16x16x128_f8f6f4 v[74:77], v[10:17], v[202:209], v[74:77]
	v_mfma_f32_16x16x128_f8f6f4 v[62:65], v[2:9], v[210:217], v[62:65]
	v_mfma_f32_16x16x128_f8f6f4 v[58:61], v[10:17], v[210:217], v[58:61]
	v_mfma_f32_16x16x128_f8f6f4 v[46:49], v[2:9], v[218:225], v[46:49]
	v_mfma_f32_16x16x128_f8f6f4 v[42:45], v[10:17], v[218:225], v[42:45]
	s_setprio 0
	s_setprio 1
	v_mfma_f32_16x16x128_f8f6f4 v[86:89], v[18:25], v[194:201], v[86:89]
	v_mfma_f32_16x16x128_f8f6f4 v[82:85], v[26:33], v[194:201], v[82:85]
	v_mfma_f32_16x16x128_f8f6f4 v[70:73], v[18:25], v[202:209], v[70:73]
	v_mfma_f32_16x16x128_f8f6f4 v[66:69], v[26:33], v[202:209], v[66:69]
	v_mfma_f32_16x16x128_f8f6f4 v[54:57], v[18:25], v[210:217], v[54:57]
	v_mfma_f32_16x16x128_f8f6f4 v[50:53], v[26:33], v[210:217], v[50:53]
	s_setprio 2
	s_barrier
	v_mfma_f32_16x16x128_f8f6f4 v[38:41], v[18:25], v[218:225], v[38:41]
	v_mfma_f32_16x16x128_f8f6f4 v[34:37], v[26:33], v[218:225], v[34:37]
	s_setprio 0
	s_nop 0
	s_add_i32 s48, s48, 2
	s_add_u32 s22, s22, 0x100
	s_addc_u32 s23, s23, 0
	s_add_u32 s46, s46, 0x100
	s_addc_u32 s47, s47, 0
	s_cmp_gt_u32 s48, 41
	s_cbranch_scc0 .LBB0_841
	s_branch .Lpeel_exit_3

.LBB0_972:
	s_ashr_i32 s23, s22, 31
	s_lshl_b64 s[24:25], s[22:23], 20
	s_add_u32 s24, s82, s24
	s_addc_u32 s25, s83, s25
	s_and_b64 s[26:27], s[6:7], exec
	s_cselect_b32 s9, s25, s31
	s_cselect_b32 s23, s24, s30
	s_ashr_i32 s21, s20, 31
	s_lshl_b64 s[26:27], s[20:21], 20
	s_add_u32 s26, s3, s26
	s_addc_u32 s27, s33, s27
	s_and_b64 s[36:37], s[6:7], exec
	s_cselect_b32 s21, s27, s35
	s_cselect_b32 s29, s26, s34
	s_add_u32 s30, s30, 0x80080
	s_addc_u32 s31, s31, 0
	s_add_u32 s62, s34, 0x100
	s_addc_u32 s63, s35, 0
	s_mov_b32 s64, -2
	ds_read_b128 v[158:161], v155
	ds_read_b128 v[162:165], v155 offset:1024
	ds_read_b128 v[166:169], v155 offset:2048
	ds_read_b128 v[170:173], v155 offset:3072
	ds_read_b128 v[174:177], v156
	ds_read_b128 v[178:181], v156 offset:1024
	ds_read_b128 v[182:185], v156 offset:2048
	ds_read_b128 v[188:191], v156 offset:3072
	s_add_u32 s34, s30, 0xfff80080
	s_addc_u32 s35, s31, -1
	s_cmp_eq_u32 s64, 28
	s_cselect_b32 s37, s9, s35
	s_cselect_b32 s36, s23, s34
	s_cselect_b32 s35, s21, s63
	s_cselect_b32 s34, s29, s62
	v_lshl_add_u64 v[152:153], s[30:31], 0, v[144:145]
	s_add_i32 m0, s39, 0xc000
	ds_read_b128 v[192:195], v157
	ds_read_b128 v[196:199], v157 offset:1024
	ds_read_b128 v[200:203], v157 offset:2048
	ds_read_b128 v[204:207], v157 offset:3072
	ds_read_b128 v[208:211], v157 offset:4096
	ds_read_b128 v[212:215], v157 offset:5120
	ds_read_b128 v[216:219], v157 offset:6144
	ds_read_b128 v[220:223], v157 offset:7168
	global_load_lds_dwordx4 v[152:153], off
	v_lshl_add_u64 v[152:153], s[30:31], 0, v[146:147]
	s_add_i32 m0, s39, 0xe000
	s_nop 0
	global_load_lds_dwordx4 v[152:153], off
	s_waitcnt vmcnt(8)
	s_waitcnt lgkmcnt(0)
	s_barrier
	s_setprio 1
	s_waitcnt lgkmcnt(0)
	v_mfma_f32_16x16x32_f16 v[126:129], v[158:161], v[192:195], 0
	v_mfma_f32_16x16x32_f16 v[122:125], v[166:169], v[192:195], 0
	v_mfma_f32_16x16x32_f16 v[110:113], v[158:161], v[200:203], 0
	v_mfma_f32_16x16x32_f16 v[106:109], v[166:169], v[200:203], 0
	v_mfma_f32_16x16x32_f16 v[94:97], v[158:161], v[208:211], 0
	v_mfma_f32_16x16x32_f16 v[90:93], v[166:169], v[208:211], 0
	v_mfma_f32_16x16x32_f16 v[78:81], v[158:161], v[216:219], 0
	v_mfma_f32_16x16x32_f16 v[74:77], v[166:169], v[216:219], 0
	v_mfma_f32_16x16x32_f16 v[126:129], v[162:165], v[196:199], v[126:129]
	v_mfma_f32_16x16x32_f16 v[122:125], v[170:173], v[196:199], v[122:125]
	v_mfma_f32_16x16x32_f16 v[110:113], v[162:165], v[204:207], v[110:113]
	v_mfma_f32_16x16x32_f16 v[106:109], v[170:173], v[204:207], v[106:109]
	v_mfma_f32_16x16x32_f16 v[94:97], v[162:165], v[212:215], v[94:97]
	v_mfma_f32_16x16x32_f16 v[90:93], v[170:173], v[212:215], v[90:93]
	v_mfma_f32_16x16x32_f16 v[78:81], v[162:165], v[220:223], v[78:81]
	v_mfma_f32_16x16x32_f16 v[74:77], v[170:173], v[220:223], v[74:77]
	s_setprio 0
	s_setprio 1
	v_mfma_f32_16x16x32_f16 v[118:121], v[174:177], v[192:195], 0
	v_mfma_f32_16x16x32_f16 v[114:117], v[182:185], v[192:195], 0
	v_mfma_f32_16x16x32_f16 v[102:105], v[174:177], v[200:203], 0
	v_mfma_f32_16x16x32_f16 v[98:101], v[182:185], v[200:203], 0
	v_mfma_f32_16x16x32_f16 v[86:89], v[174:177], v[208:211], 0
	v_mfma_f32_16x16x32_f16 v[82:85], v[182:185], v[208:211], 0
	v_mfma_f32_16x16x32_f16 v[70:73], v[174:177], v[216:219], 0
	v_mfma_f32_16x16x32_f16 v[66:69], v[182:185], v[216:219], 0
	v_mfma_f32_16x16x32_f16 v[118:121], v[178:181], v[196:199], v[118:121]
	v_mfma_f32_16x16x32_f16 v[114:117], v[188:191], v[196:199], v[114:117]
	v_mfma_f32_16x16x32_f16 v[102:105], v[178:181], v[204:207], v[102:105]
	v_mfma_f32_16x16x32_f16 v[98:101], v[188:191], v[204:207], v[98:101]
	s_setprio 2
	s_barrier
	v_mfma_f32_16x16x32_f16 v[86:89], v[178:181], v[212:215], v[86:89]
	v_mfma_f32_16x16x32_f16 v[82:85], v[188:191], v[212:215], v[82:85]
	v_mfma_f32_16x16x32_f16 v[70:73], v[178:181], v[220:223], v[70:73]
	v_mfma_f32_16x16x32_f16 v[66:69], v[188:191], v[220:223], v[66:69]
	s_setprio 0
	s_nop 0
	s_add_i32 s65, s49, s38
	v_lshl_add_u64 v[152:153], s[34:35], 0, v[132:133]
	s_mov_b32 m0, s65
	ds_read_b128 v[192:195], v157 offset:16384
	ds_read_b128 v[196:199], v157 offset:17408
	ds_read_b128 v[200:203], v157 offset:18432
	ds_read_b128 v[204:207], v157 offset:19456
	ds_read_b128 v[208:211], v157 offset:20480
	ds_read_b128 v[212:215], v157 offset:21504
	ds_read_b128 v[216:219], v157 offset:22528
	ds_read_b128 v[220:223], v157 offset:23552
	global_load_lds_dwordx4 v[152:153], off
	s_add_i32 m0, s65, 0x2000
	s_add_u32 s66, s34, 0x80000
	v_lshl_add_u64 v[224:225], s[34:35], 0, v[136:137]
	s_addc_u32 s67, s35, 0
	s_add_i32 s65, s50, s38
	global_load_lds_dwordx4 v[224:225], off
	v_lshl_add_u64 v[226:227], s[66:67], 0, v[132:133]
	s_mov_b32 m0, s65
	v_lshl_add_u64 v[228:229], s[36:37], 0, v[134:135]
	global_load_lds_dwordx4 v[226:227], off
	v_lshl_add_u64 v[226:227], s[66:67], 0, v[136:137]
	s_add_i32 m0, s65, 0x2000
	s_nop 0
	global_load_lds_dwordx4 v[226:227], off
	v_lshl_add_u64 v[226:227], s[36:37], 0, v[130:131]
	s_mov_b32 m0, s39
	s_nop 0
	global_load_lds_dwordx4 v[226:227], off
	s_mov_b32 m0, s40
	s_nop 0
	global_load_lds_dwordx4 v[228:229], off
	s_waitcnt vmcnt(8)
	s_waitcnt lgkmcnt(0)
	s_barrier
	s_setprio 1
	s_waitcnt lgkmcnt(0)
	v_mfma_f32_16x16x32_f16 v[62:65], v[158:161], v[192:195], 0
	v_mfma_f32_16x16x32_f16 v[58:61], v[166:169], v[192:195], 0
	v_mfma_f32_16x16x32_f16 v[46:49], v[158:161], v[200:203], 0
	v_mfma_f32_16x16x32_f16 v[42:45], v[166:169], v[200:203], 0
	v_mfma_f32_16x16x32_f16 v[30:33], v[158:161], v[208:211], 0
	v_mfma_f32_16x16x32_f16 v[26:29], v[166:169], v[208:211], 0
	v_mfma_f32_16x16x32_f16 v[14:17], v[158:161], v[216:219], 0
	v_mfma_f32_16x16x32_f16 v[10:13], v[166:169], v[216:219], 0
	v_mfma_f32_16x16x32_f16 v[62:65], v[162:165], v[196:199], v[62:65]
	v_mfma_f32_16x16x32_f16 v[58:61], v[170:173], v[196:199], v[58:61]
	v_mfma_f32_16x16x32_f16 v[46:49], v[162:165], v[204:207], v[46:49]
	v_mfma_f32_16x16x32_f16 v[42:45], v[170:173], v[204:207], v[42:45]
	v_mfma_f32_16x16x32_f16 v[30:33], v[162:165], v[212:215], v[30:33]
	v_mfma_f32_16x16x32_f16 v[26:29], v[170:173], v[212:215], v[26:29]
	v_mfma_f32_16x16x32_f16 v[14:17], v[162:165], v[220:223], v[14:17]
	v_mfma_f32_16x16x32_f16 v[10:13], v[170:173], v[220:223], v[10:13]
	s_setprio 0
	s_setprio 1
	v_mfma_f32_16x16x32_f16 v[54:57], v[174:177], v[192:195], 0
	v_mfma_f32_16x16x32_f16 v[50:53], v[182:185], v[192:195], 0
	v_mfma_f32_16x16x32_f16 v[38:41], v[174:177], v[200:203], 0
	v_mfma_f32_16x16x32_f16 v[34:37], v[182:185], v[200:203], 0
	v_mfma_f32_16x16x32_f16 v[22:25], v[174:177], v[208:211], 0
	v_mfma_f32_16x16x32_f16 v[18:21], v[182:185], v[208:211], 0
	v_mfma_f32_16x16x32_f16 v[6:9], v[174:177], v[216:219], 0
	v_mfma_f32_16x16x32_f16 v[2:5], v[182:185], v[216:219], 0
	v_mfma_f32_16x16x32_f16 v[54:57], v[178:181], v[196:199], v[54:57]
	v_mfma_f32_16x16x32_f16 v[50:53], v[188:191], v[196:199], v[50:53]
	v_mfma_f32_16x16x32_f16 v[38:41], v[178:181], v[204:207], v[38:41]
	v_mfma_f32_16x16x32_f16 v[34:37], v[188:191], v[204:207], v[34:37]
	s_setprio 2
	s_barrier
	v_mfma_f32_16x16x32_f16 v[22:25], v[178:181], v[212:215], v[22:25]
	v_mfma_f32_16x16x32_f16 v[18:21], v[188:191], v[212:215], v[18:21]
	v_mfma_f32_16x16x32_f16 v[6:9], v[178:181], v[220:223], v[6:9]
	v_mfma_f32_16x16x32_f16 v[2:5], v[188:191], v[220:223], v[2:5]
	s_setprio 0
	s_nop 0
	s_add_i32 s65, 0, 0x18000
	v_add_u32_e32 v138, s65, v141
	s_add_i32 s66, 0, 0x1c000
	ds_read_b128 v[158:161], v138
	ds_read_b128 v[162:165], v138 offset:1024
	ds_read_b128 v[166:169], v138 offset:2048
	ds_read_b128 v[170:173], v138 offset:3072
	v_add_u32_e32 v138, s66, v141
	ds_read_b128 v[174:177], v138
	ds_read_b128 v[178:181], v138 offset:1024
	ds_read_b128 v[182:185], v138 offset:2048
	ds_read_b128 v[188:191], v138 offset:3072
	s_add_u32 s36, s36, 0x80000
	s_addc_u32 s37, s37, 0
	s_mov_b32 m0, s41
	v_lshl_add_u64 v[230:231], s[36:37], 0, v[130:131]
	ds_read_b128 v[192:195], v157 offset:32768
	ds_read_b128 v[196:199], v157 offset:33792
	ds_read_b128 v[200:203], v157 offset:34816
	ds_read_b128 v[204:207], v157 offset:35840
	ds_read_b128 v[208:211], v157 offset:36864
	ds_read_b128 v[212:215], v157 offset:37888
	ds_read_b128 v[216:219], v157 offset:38912
	ds_read_b128 v[220:223], v157 offset:39936
	global_load_lds_dwordx4 v[230:231], off
	v_lshl_add_u64 v[230:231], s[36:37], 0, v[134:135]
	s_mov_b32 m0, s42
	s_nop 0
	global_load_lds_dwordx4 v[230:231], off
	s_waitcnt vmcnt(8)
	s_waitcnt lgkmcnt(0)
	s_barrier
	s_setprio 1
	s_waitcnt lgkmcnt(0)
	v_mfma_f32_16x16x32_f16 v[126:129], v[158:161], v[192:195], v[126:129]
	v_mfma_f32_16x16x32_f16 v[122:125], v[166:169], v[192:195], v[122:125]
	v_mfma_f32_16x16x32_f16 v[110:113], v[158:161], v[200:203], v[110:113]
	v_mfma_f32_16x16x32_f16 v[106:109], v[166:169], v[200:203], v[106:109]
	v_mfma_f32_16x16x32_f16 v[94:97], v[158:161], v[208:211], v[94:97]
	v_mfma_f32_16x16x32_f16 v[90:93], v[166:169], v[208:211], v[90:93]
	v_mfma_f32_16x16x32_f16 v[78:81], v[158:161], v[216:219], v[78:81]
	v_mfma_f32_16x16x32_f16 v[74:77], v[166:169], v[216:219], v[74:77]
	v_mfma_f32_16x16x32_f16 v[126:129], v[162:165], v[196:199], v[126:129]
	v_mfma_f32_16x16x32_f16 v[122:125], v[170:173], v[196:199], v[122:125]
	v_mfma_f32_16x16x32_f16 v[110:113], v[162:165], v[204:207], v[110:113]
	v_mfma_f32_16x16x32_f16 v[106:109], v[170:173], v[204:207], v[106:109]
	v_mfma_f32_16x16x32_f16 v[94:97], v[162:165], v[212:215], v[94:97]
	v_mfma_f32_16x16x32_f16 v[90:93], v[170:173], v[212:215], v[90:93]
	v_mfma_f32_16x16x32_f16 v[78:81], v[162:165], v[220:223], v[78:81]
	v_mfma_f32_16x16x32_f16 v[74:77], v[170:173], v[220:223], v[74:77]
	s_setprio 0
	s_setprio 1
	v_mfma_f32_16x16x32_f16 v[118:121], v[174:177], v[192:195], v[118:121]
	v_mfma_f32_16x16x32_f16 v[114:117], v[182:185], v[192:195], v[114:117]
	v_mfma_f32_16x16x32_f16 v[102:105], v[174:177], v[200:203], v[102:105]
	v_mfma_f32_16x16x32_f16 v[98:101], v[182:185], v[200:203], v[98:101]
	v_mfma_f32_16x16x32_f16 v[86:89], v[174:177], v[208:211], v[86:89]
	v_mfma_f32_16x16x32_f16 v[82:85], v[182:185], v[208:211], v[82:85]
	v_mfma_f32_16x16x32_f16 v[70:73], v[174:177], v[216:219], v[70:73]
	v_mfma_f32_16x16x32_f16 v[66:69], v[182:185], v[216:219], v[66:69]
	v_mfma_f32_16x16x32_f16 v[118:121], v[178:181], v[196:199], v[118:121]
	v_mfma_f32_16x16x32_f16 v[114:117], v[188:191], v[196:199], v[114:117]
	v_mfma_f32_16x16x32_f16 v[102:105], v[178:181], v[204:207], v[102:105]
	v_mfma_f32_16x16x32_f16 v[98:101], v[188:191], v[204:207], v[98:101]
	s_setprio 2
	s_barrier
	v_mfma_f32_16x16x32_f16 v[86:89], v[178:181], v[212:215], v[86:89]
	v_mfma_f32_16x16x32_f16 v[82:85], v[188:191], v[212:215], v[82:85]
	v_mfma_f32_16x16x32_f16 v[70:73], v[178:181], v[220:223], v[70:73]
	v_mfma_f32_16x16x32_f16 v[66:69], v[188:191], v[220:223], v[66:69]
	s_setprio 0
	s_nop 0
	s_add_i32 s36, s65, s38
	v_lshl_add_u64 v[152:153], v[152:153], 0, s[16:17]
	s_mov_b32 m0, s36
	ds_read_b128 v[192:195], v157 offset:49152
	ds_read_b128 v[196:199], v157 offset:50176
	ds_read_b128 v[200:203], v157 offset:51200
	ds_read_b128 v[204:207], v157 offset:52224
	ds_read_b128 v[208:211], v157 offset:53248
	ds_read_b128 v[212:215], v157 offset:54272
	ds_read_b128 v[216:219], v157 offset:55296
	ds_read_b128 v[220:223], v157 offset:56320
	global_load_lds_dwordx4 v[152:153], off
	s_add_i32 m0, s36, 0x2000
	s_add_u32 s34, s34, 0x80080
	v_lshl_add_u64 v[152:153], v[224:225], 0, s[16:17]
	s_addc_u32 s35, s35, 0
	s_add_i32 s36, s66, s38
	global_load_lds_dwordx4 v[152:153], off
	v_lshl_add_u64 v[152:153], s[34:35], 0, v[132:133]
	s_mov_b32 m0, s36
	s_nop 0
	global_load_lds_dwordx4 v[152:153], off
	v_lshl_add_u64 v[152:153], s[34:35], 0, v[136:137]
	s_add_i32 m0, s36, 0x2000
	s_nop 0
	global_load_lds_dwordx4 v[152:153], off
	v_lshl_add_u64 v[152:153], v[226:227], 0, s[16:17]
	s_mov_b32 m0, s45
	s_nop 0
	global_load_lds_dwordx4 v[152:153], off
	v_lshl_add_u64 v[152:153], v[228:229], 0, s[16:17]
	s_mov_b32 m0, s46
	s_nop 0
	global_load_lds_dwordx4 v[152:153], off
	s_waitcnt vmcnt(8)
	s_waitcnt lgkmcnt(0)
	s_barrier
	s_setprio 1
	s_waitcnt lgkmcnt(0)
	v_mfma_f32_16x16x32_f16 v[62:65], v[158:161], v[192:195], v[62:65]
	v_mfma_f32_16x16x32_f16 v[58:61], v[166:169], v[192:195], v[58:61]
	v_mfma_f32_16x16x32_f16 v[46:49], v[158:161], v[200:203], v[46:49]
	v_mfma_f32_16x16x32_f16 v[42:45], v[166:169], v[200:203], v[42:45]
	v_mfma_f32_16x16x32_f16 v[30:33], v[158:161], v[208:211], v[30:33]
	v_mfma_f32_16x16x32_f16 v[26:29], v[166:169], v[208:211], v[26:29]
	v_mfma_f32_16x16x32_f16 v[14:17], v[158:161], v[216:219], v[14:17]
	v_mfma_f32_16x16x32_f16 v[10:13], v[166:169], v[216:219], v[10:13]
	v_mfma_f32_16x16x32_f16 v[62:65], v[162:165], v[196:199], v[62:65]
	v_mfma_f32_16x16x32_f16 v[58:61], v[170:173], v[196:199], v[58:61]
	v_mfma_f32_16x16x32_f16 v[46:49], v[162:165], v[204:207], v[46:49]
	v_mfma_f32_16x16x32_f16 v[42:45], v[170:173], v[204:207], v[42:45]
	v_mfma_f32_16x16x32_f16 v[30:33], v[162:165], v[212:215], v[30:33]
	v_mfma_f32_16x16x32_f16 v[26:29], v[170:173], v[212:215], v[26:29]
	v_mfma_f32_16x16x32_f16 v[14:17], v[162:165], v[220:223], v[14:17]
	v_mfma_f32_16x16x32_f16 v[10:13], v[170:173], v[220:223], v[10:13]
	s_setprio 0
	s_setprio 1
	v_mfma_f32_16x16x32_f16 v[54:57], v[174:177], v[192:195], v[54:57]
	v_mfma_f32_16x16x32_f16 v[50:53], v[182:185], v[192:195], v[50:53]
	v_mfma_f32_16x16x32_f16 v[38:41], v[174:177], v[200:203], v[38:41]
	v_mfma_f32_16x16x32_f16 v[34:37], v[182:185], v[200:203], v[34:37]
	v_mfma_f32_16x16x32_f16 v[22:25], v[174:177], v[208:211], v[22:25]
	v_mfma_f32_16x16x32_f16 v[18:21], v[182:185], v[208:211], v[18:21]
	v_mfma_f32_16x16x32_f16 v[6:9], v[174:177], v[216:219], v[6:9]
	v_mfma_f32_16x16x32_f16 v[2:5], v[182:185], v[216:219], v[2:5]
	v_mfma_f32_16x16x32_f16 v[54:57], v[178:181], v[196:199], v[54:57]
	v_mfma_f32_16x16x32_f16 v[50:53], v[188:191], v[196:199], v[50:53]
	v_mfma_f32_16x16x32_f16 v[38:41], v[178:181], v[204:207], v[38:41]
	v_mfma_f32_16x16x32_f16 v[34:37], v[188:191], v[204:207], v[34:37]
	s_setprio 2
	s_barrier
	v_mfma_f32_16x16x32_f16 v[22:25], v[178:181], v[212:215], v[22:25]
	v_mfma_f32_16x16x32_f16 v[18:21], v[188:191], v[212:215], v[18:21]
	v_mfma_f32_16x16x32_f16 v[6:9], v[178:181], v[220:223], v[6:9]
	v_mfma_f32_16x16x32_f16 v[2:5], v[188:191], v[220:223], v[2:5]
	s_setprio 0
	s_nop 0
	s_add_i32 s64, s64, 2
	s_add_u32 s30, s30, 0x100
	s_addc_u32 s31, s31, 0
	s_add_u32 s62, s62, 0x100
	s_addc_u32 s63, s63, 0
	s_cmp_gt_u32 s64, 29
	s_cbranch_scc0 .LBB0_973
	s_branch .Lpeel_exit_4

.Lpeel_exit_4:
	s_and_b64 vcc, exec, s[18:19]
	s_cbranch_vccz .LBB0_976
	s_barrier

.LBB0_1119:
	s_lshl_b64 s[22:23], s[20:21], 18
	s_add_u32 s21, s31, s22
	s_addc_u32 s28, s33, s23
	s_and_b64 s[22:23], s[6:7], exec
	s_cselect_b32 s23, s28, s27
	s_cselect_b32 s22, s21, s26
	s_add_u32 s24, s24, 0x28080
	s_addc_u32 s25, s25, 0
	s_add_u32 s21, s26, 0x100
	s_addc_u32 s50, s27, 0
	s_mov_b32 s51, -2
	ds_read_b128 v[88:91], v85
	ds_read_b128 v[92:95], v85 offset:1024
	ds_read_b128 v[96:99], v85 offset:2048
	ds_read_b128 v[100:103], v85 offset:3072
	s_add_u32 s26, s24, 0xfffd8080
	s_addc_u32 s27, s25, -1
	s_cmp_eq_u32 s51, 4
	s_cselect_b32 s29, s1, s27
	s_cselect_b32 s28, s0, s26
	s_cselect_b32 s27, s23, s50
	s_cselect_b32 s26, s22, s21
	v_lshl_add_u64 v[136:137], s[24:25], 0, v[76:77]
	s_add_i32 m0, s15, 0xc000
	ds_read_b128 v[104:107], v86
	ds_read_b128 v[108:111], v86 offset:1024
	ds_read_b128 v[112:115], v86 offset:2048
	ds_read_b128 v[116:119], v86 offset:3072
	ds_read_b128 v[120:123], v86 offset:4096
	ds_read_b128 v[124:127], v86 offset:5120
	ds_read_b128 v[128:131], v86 offset:6144
	ds_read_b128 v[132:135], v86 offset:7168
	global_load_lds_dwordx4 v[136:137], off
	v_lshl_add_u64 v[136:137], s[24:25], 0, v[78:79]
	s_add_i32 m0, s15, 0xe000
	s_nop 0
	global_load_lds_dwordx4 v[136:137], off
	s_waitcnt vmcnt(8)
	s_waitcnt lgkmcnt(0)
	s_barrier
	s_setprio 1
	s_waitcnt lgkmcnt(0)
	v_mfma_f32_16x16x32_f16 v[62:65], v[88:91], v[104:107], 0
	v_mfma_f32_16x16x32_f16 v[58:61], v[96:99], v[104:107], 0
	v_mfma_f32_16x16x32_f16 v[54:57], v[88:91], v[112:115], 0
	v_mfma_f32_16x16x32_f16 v[50:53], v[96:99], v[112:115], 0
	v_mfma_f32_16x16x32_f16 v[46:49], v[88:91], v[120:123], 0
	v_mfma_f32_16x16x32_f16 v[42:45], v[96:99], v[120:123], 0
	v_mfma_f32_16x16x32_f16 v[38:41], v[88:91], v[128:131], 0
	v_mfma_f32_16x16x32_f16 v[34:37], v[96:99], v[128:131], 0
	v_mfma_f32_16x16x32_f16 v[62:65], v[92:95], v[108:111], v[62:65]
	v_mfma_f32_16x16x32_f16 v[58:61], v[100:103], v[108:111], v[58:61]
	v_mfma_f32_16x16x32_f16 v[54:57], v[92:95], v[116:119], v[54:57]
	v_mfma_f32_16x16x32_f16 v[50:53], v[100:103], v[116:119], v[50:53]
	s_setprio 2
	s_barrier
	v_mfma_f32_16x16x32_f16 v[46:49], v[92:95], v[124:127], v[46:49]
	v_mfma_f32_16x16x32_f16 v[42:45], v[100:103], v[124:127], v[42:45]
	v_mfma_f32_16x16x32_f16 v[38:41], v[92:95], v[132:135], v[38:41]
	v_mfma_f32_16x16x32_f16 v[34:37], v[100:103], v[132:135], v[34:37]
	s_setprio 0
	s_setprio 1
	s_setprio 0
	s_nop 0
	s_add_i32 s60, s48, s34
	v_lshl_add_u64 v[136:137], s[26:27], 0, v[70:71]
	s_mov_b32 m0, s60
	ds_read_b128 v[104:107], v86 offset:16384
	ds_read_b128 v[108:111], v86 offset:17408
	ds_read_b128 v[112:115], v86 offset:18432
	ds_read_b128 v[116:119], v86 offset:19456
	ds_read_b128 v[120:123], v86 offset:20480
	ds_read_b128 v[124:127], v86 offset:21504
	ds_read_b128 v[128:131], v86 offset:22528
	ds_read_b128 v[132:135], v86 offset:23552
	global_load_lds_dwordx4 v[136:137], off
	s_add_i32 m0, s60, 0x2000
	s_add_u32 s60, s26, 0x20000
	v_lshl_add_u64 v[138:139], s[26:27], 0, v[66:67]
	s_addc_u32 s61, s27, 0
	global_load_lds_dwordx4 v[138:139], off
	v_lshl_add_u64 v[140:141], s[60:61], 0, v[70:71]
	s_mov_b32 m0, s35
	v_lshl_add_u64 v[142:143], s[28:29], 0, v[68:69]
	global_load_lds_dwordx4 v[140:141], off
	v_lshl_add_u64 v[140:141], s[60:61], 0, v[66:67]
	s_mov_b32 m0, s36
	s_nop 0
	global_load_lds_dwordx4 v[140:141], off
	v_lshl_add_u64 v[140:141], s[28:29], 0, v[72:73]
	s_mov_b32 m0, s15
	s_nop 0
	global_load_lds_dwordx4 v[140:141], off
	s_mov_b32 m0, s37
	s_nop 0
	global_load_lds_dwordx4 v[142:143], off
	s_waitcnt vmcnt(8)
	s_waitcnt lgkmcnt(0)
	s_barrier
	s_setprio 1
	s_waitcnt lgkmcnt(0)
	v_mfma_f32_16x16x32_f16 v[30:33], v[88:91], v[104:107], 0
	v_mfma_f32_16x16x32_f16 v[26:29], v[96:99], v[104:107], 0
	v_mfma_f32_16x16x32_f16 v[22:25], v[88:91], v[112:115], 0
	v_mfma_f32_16x16x32_f16 v[18:21], v[96:99], v[112:115], 0
	v_mfma_f32_16x16x32_f16 v[14:17], v[88:91], v[120:123], 0
	v_mfma_f32_16x16x32_f16 v[10:13], v[96:99], v[120:123], 0
	v_mfma_f32_16x16x32_f16 v[6:9], v[88:91], v[128:131], 0
	v_mfma_f32_16x16x32_f16 v[2:5], v[96:99], v[128:131], 0
	v_mfma_f32_16x16x32_f16 v[30:33], v[92:95], v[108:111], v[30:33]
	v_mfma_f32_16x16x32_f16 v[26:29], v[100:103], v[108:111], v[26:29]
	v_mfma_f32_16x16x32_f16 v[22:25], v[92:95], v[116:119], v[22:25]
	v_mfma_f32_16x16x32_f16 v[18:21], v[100:103], v[116:119], v[18:21]
	s_setprio 2
	s_barrier
	v_mfma_f32_16x16x32_f16 v[14:17], v[92:95], v[124:127], v[14:17]
	v_mfma_f32_16x16x32_f16 v[10:13], v[100:103], v[124:127], v[10:13]
	v_mfma_f32_16x16x32_f16 v[6:9], v[92:95], v[132:135], v[6:9]
	v_mfma_f32_16x16x32_f16 v[2:5], v[100:103], v[132:135], v[2:5]
	s_setprio 0
	s_setprio 1
	s_setprio 0
	s_nop 0
	s_add_i32 s60, 0, 0x18000
	v_add_u32_e32 v87, s60, v84
	ds_read_b128 v[88:91], v87
	ds_read_b128 v[92:95], v87 offset:1024
	ds_read_b128 v[96:99], v87 offset:2048
	ds_read_b128 v[100:103], v87 offset:3072
	s_add_u32 s28, s28, 0x28000
	s_addc_u32 s29, s29, 0
	s_mov_b32 m0, s38
	v_lshl_add_u64 v[144:145], s[28:29], 0, v[72:73]
	ds_read_b128 v[104:107], v86 offset:32768
	ds_read_b128 v[108:111], v86 offset:33792
	ds_read_b128 v[112:115], v86 offset:34816
	ds_read_b128 v[116:119], v86 offset:35840
	ds_read_b128 v[120:123], v86 offset:36864
	ds_read_b128 v[124:127], v86 offset:37888
	ds_read_b128 v[128:131], v86 offset:38912
	ds_read_b128 v[132:135], v86 offset:39936
	global_load_lds_dwordx4 v[144:145], off
	v_lshl_add_u64 v[144:145], s[28:29], 0, v[68:69]
	s_mov_b32 m0, s39
	s_nop 0
	global_load_lds_dwordx4 v[144:145], off
	s_waitcnt vmcnt(8)
	s_waitcnt lgkmcnt(0)
	s_barrier
	s_setprio 1
	s_waitcnt lgkmcnt(0)
	v_mfma_f32_16x16x32_f16 v[62:65], v[88:91], v[104:107], v[62:65]
	v_mfma_f32_16x16x32_f16 v[58:61], v[96:99], v[104:107], v[58:61]
	v_mfma_f32_16x16x32_f16 v[54:57], v[88:91], v[112:115], v[54:57]
	v_mfma_f32_16x16x32_f16 v[50:53], v[96:99], v[112:115], v[50:53]
	v_mfma_f32_16x16x32_f16 v[46:49], v[88:91], v[120:123], v[46:49]
	v_mfma_f32_16x16x32_f16 v[42:45], v[96:99], v[120:123], v[42:45]
	v_mfma_f32_16x16x32_f16 v[38:41], v[88:91], v[128:131], v[38:41]
	v_mfma_f32_16x16x32_f16 v[34:37], v[96:99], v[128:131], v[34:37]
	v_mfma_f32_16x16x32_f16 v[62:65], v[92:95], v[108:111], v[62:65]
	v_mfma_f32_16x16x32_f16 v[58:61], v[100:103], v[108:111], v[58:61]
	v_mfma_f32_16x16x32_f16 v[54:57], v[92:95], v[116:119], v[54:57]
	v_mfma_f32_16x16x32_f16 v[50:53], v[100:103], v[116:119], v[50:53]
	s_setprio 2
	s_barrier
	v_mfma_f32_16x16x32_f16 v[46:49], v[92:95], v[124:127], v[46:49]
	v_mfma_f32_16x16x32_f16 v[42:45], v[100:103], v[124:127], v[42:45]
	v_mfma_f32_16x16x32_f16 v[38:41], v[92:95], v[132:135], v[38:41]
	v_mfma_f32_16x16x32_f16 v[34:37], v[100:103], v[132:135], v[34:37]
	s_setprio 0
	s_setprio 1
	s_setprio 0
	s_nop 0
	s_add_i32 s28, s60, s34
	v_lshl_add_u64 v[136:137], v[136:137], 0, s[16:17]
	s_mov_b32 m0, s28
	ds_read_b128 v[104:107], v86 offset:49152
	ds_read_b128 v[108:111], v86 offset:50176
	ds_read_b128 v[112:115], v86 offset:51200
	ds_read_b128 v[116:119], v86 offset:52224
	ds_read_b128 v[120:123], v86 offset:53248
	ds_read_b128 v[124:127], v86 offset:54272
	ds_read_b128 v[128:131], v86 offset:55296
	ds_read_b128 v[132:135], v86 offset:56320
	global_load_lds_dwordx4 v[136:137], off
	s_add_i32 m0, s28, 0x2000
	s_add_u32 s26, s26, 0x20080
	v_lshl_add_u64 v[136:137], v[138:139], 0, s[16:17]
	s_addc_u32 s27, s27, 0
	global_load_lds_dwordx4 v[136:137], off
	v_lshl_add_u64 v[136:137], s[26:27], 0, v[70:71]
	s_mov_b32 m0, s45
	s_nop 0
	global_load_lds_dwordx4 v[136:137], off
	v_lshl_add_u64 v[136:137], s[26:27], 0, v[66:67]
	s_mov_b32 m0, s46
	s_nop 0
	global_load_lds_dwordx4 v[136:137], off
	v_lshl_add_u64 v[136:137], v[140:141], 0, s[16:17]
	s_mov_b32 m0, s43
	s_nop 0
	global_load_lds_dwordx4 v[136:137], off
	v_lshl_add_u64 v[136:137], v[142:143], 0, s[16:17]
	s_mov_b32 m0, s44
	s_nop 0
	global_load_lds_dwordx4 v[136:137], off
	s_waitcnt vmcnt(8)
	s_waitcnt lgkmcnt(0)
	s_barrier
	s_setprio 1
	s_waitcnt lgkmcnt(0)
	v_mfma_f32_16x16x32_f16 v[30:33], v[88:91], v[104:107], v[30:33]
	v_mfma_f32_16x16x32_f16 v[26:29], v[96:99], v[104:107], v[26:29]
	v_mfma_f32_16x16x32_f16 v[22:25], v[88:91], v[112:115], v[22:25]
	v_mfma_f32_16x16x32_f16 v[18:21], v[96:99], v[112:115], v[18:21]
	v_mfma_f32_16x16x32_f16 v[14:17], v[88:91], v[120:123], v[14:17]
	v_mfma_f32_16x16x32_f16 v[10:13], v[96:99], v[120:123], v[10:13]
	v_mfma_f32_16x16x32_f16 v[6:9], v[88:91], v[128:131], v[6:9]
	v_mfma_f32_16x16x32_f16 v[2:5], v[96:99], v[128:131], v[2:5]
	v_mfma_f32_16x16x32_f16 v[30:33], v[92:95], v[108:111], v[30:33]
	v_mfma_f32_16x16x32_f16 v[26:29], v[100:103], v[108:111], v[26:29]
	v_mfma_f32_16x16x32_f16 v[22:25], v[92:95], v[116:119], v[22:25]
	v_mfma_f32_16x16x32_f16 v[18:21], v[100:103], v[116:119], v[18:21]
	s_setprio 2
	s_barrier
	v_mfma_f32_16x16x32_f16 v[14:17], v[92:95], v[124:127], v[14:17]
	v_mfma_f32_16x16x32_f16 v[10:13], v[100:103], v[124:127], v[10:13]
	v_mfma_f32_16x16x32_f16 v[6:9], v[92:95], v[132:135], v[6:9]
	v_mfma_f32_16x16x32_f16 v[2:5], v[100:103], v[132:135], v[2:5]
	s_setprio 0
	s_setprio 1
	s_setprio 0
	s_nop 0
	s_add_i32 s51, s51, 2
	s_add_u32 s24, s24, 0x100
	s_addc_u32 s25, s25, 0
	s_add_u32 s21, s21, 0x100
	s_addc_u32 s50, s50, 0
	s_cmp_gt_u32 s51, 5
	s_cbranch_scc0 .LBB0_1120
	s_branch .Lpeel_exit_5

.LBB0_1648:
	s_add_u32 s20, s20, 0x28080
	s_addc_u32 s21, s21, 0
	s_add_u32 s48, s22, 0x100
	s_addc_u32 s49, s23, 0
	s_mov_b32 s50, -2
	ds_read_b128 v[98:101], v174
	ds_read_b128 v[102:105], v174 offset:1024
	ds_read_b128 v[158:161], v174 offset:2048
	ds_read_b128 v[164:167], v174 offset:3072
	ds_read_b128 v[178:181], v175
	ds_read_b128 v[182:185], v175 offset:1024
	ds_read_b128 v[188:191], v175 offset:2048
	ds_read_b128 v[192:195], v175 offset:3072
	s_add_u32 s22, s20, 0xfffd8080
	s_addc_u32 s23, s21, -1
	s_cmp_eq_u32 s50, 6
	s_cselect_b32 s25, s1, s23
	s_cselect_b32 s24, s0, s22
	s_cselect_b32 s23, s19, s49
	s_cselect_b32 s22, s18, s48
	v_lshl_add_u64 v[168:169], s[20:21], 0, v[150:151]
	s_add_i32 m0, s29, 0xc000
	ds_read_b128 v[196:199], v176
	ds_read_b128 v[200:203], v176 offset:1024
	ds_read_b128 v[204:207], v176 offset:2048
	ds_read_b128 v[208:211], v176 offset:3072
	ds_read_b128 v[212:215], v176 offset:4096
	ds_read_b128 v[216:219], v176 offset:5120
	ds_read_b128 v[220:223], v176 offset:6144
	ds_read_b128 v[224:227], v176 offset:7168
	global_load_lds_dwordx4 v[168:169], off
	v_lshl_add_u64 v[168:169], s[20:21], 0, v[152:153]
	s_add_i32 m0, s29, 0xe000
	s_nop 0
	global_load_lds_dwordx4 v[168:169], off
	s_waitcnt vmcnt(8)
	s_waitcnt lgkmcnt(0)
	s_barrier
	s_setprio 1
	s_waitcnt lgkmcnt(0)
	v_mfma_f32_16x16x32_f16 v[134:137], v[98:101], v[196:199], 0
	v_mfma_f32_16x16x32_f16 v[130:133], v[158:161], v[196:199], 0
	v_mfma_f32_16x16x32_f16 v[126:129], v[98:101], v[204:207], 0
	v_mfma_f32_16x16x32_f16 v[122:125], v[158:161], v[204:207], 0
	v_mfma_f32_16x16x32_f16 v[118:121], v[98:101], v[212:215], 0
	v_mfma_f32_16x16x32_f16 v[114:117], v[158:161], v[212:215], 0
	v_mfma_f32_16x16x32_f16 v[110:113], v[98:101], v[220:223], 0
	v_mfma_f32_16x16x32_f16 v[106:109], v[158:161], v[220:223], 0
	v_mfma_f32_16x16x32_f16 v[134:137], v[102:105], v[200:203], v[134:137]
	v_mfma_f32_16x16x32_f16 v[130:133], v[164:167], v[200:203], v[130:133]
	v_mfma_f32_16x16x32_f16 v[126:129], v[102:105], v[208:211], v[126:129]
	v_mfma_f32_16x16x32_f16 v[122:125], v[164:167], v[208:211], v[122:125]
	v_mfma_f32_16x16x32_f16 v[118:121], v[102:105], v[216:219], v[118:121]
	v_mfma_f32_16x16x32_f16 v[114:117], v[164:167], v[216:219], v[114:117]
	v_mfma_f32_16x16x32_f16 v[110:113], v[102:105], v[224:227], v[110:113]
	v_mfma_f32_16x16x32_f16 v[106:109], v[164:167], v[224:227], v[106:109]
	s_setprio 0
	s_setprio 1
	v_mfma_f32_16x16x32_f16 v[62:65], v[178:181], v[196:199], 0
	v_mfma_f32_16x16x32_f16 v[58:61], v[188:191], v[196:199], 0
	v_mfma_f32_16x16x32_f16 v[54:57], v[178:181], v[204:207], 0
	v_mfma_f32_16x16x32_f16 v[50:53], v[188:191], v[204:207], 0
	v_mfma_f32_16x16x32_f16 v[46:49], v[178:181], v[212:215], 0
	v_mfma_f32_16x16x32_f16 v[42:45], v[188:191], v[212:215], 0
	v_mfma_f32_16x16x32_f16 v[38:41], v[178:181], v[220:223], 0
	v_mfma_f32_16x16x32_f16 v[34:37], v[188:191], v[220:223], 0
	v_mfma_f32_16x16x32_f16 v[62:65], v[182:185], v[200:203], v[62:65]
	v_mfma_f32_16x16x32_f16 v[58:61], v[192:195], v[200:203], v[58:61]
	v_mfma_f32_16x16x32_f16 v[54:57], v[182:185], v[208:211], v[54:57]
	v_mfma_f32_16x16x32_f16 v[50:53], v[192:195], v[208:211], v[50:53]
	s_setprio 2
	s_barrier
	v_mfma_f32_16x16x32_f16 v[46:49], v[182:185], v[216:219], v[46:49]
	v_mfma_f32_16x16x32_f16 v[42:45], v[192:195], v[216:219], v[42:45]
	v_mfma_f32_16x16x32_f16 v[38:41], v[182:185], v[224:227], v[38:41]
	v_mfma_f32_16x16x32_f16 v[34:37], v[192:195], v[224:227], v[34:37]
	s_setprio 0
	s_nop 0
	s_add_i32 s51, s39, s27
	v_lshl_add_u64 v[168:169], s[22:23], 0, v[142:143]
	s_mov_b32 m0, s51
	ds_read_b128 v[196:199], v176 offset:16384
	ds_read_b128 v[200:203], v176 offset:17408
	ds_read_b128 v[204:207], v176 offset:18432
	ds_read_b128 v[208:211], v176 offset:19456
	ds_read_b128 v[212:215], v176 offset:20480
	ds_read_b128 v[216:219], v176 offset:21504
	ds_read_b128 v[220:223], v176 offset:22528
	ds_read_b128 v[224:227], v176 offset:23552
	global_load_lds_dwordx4 v[168:169], off
	s_add_i32 m0, s51, 0x2000
	s_add_u32 s60, s22, 0x28000
	v_lshl_add_u64 v[228:229], s[22:23], 0, v[138:139]
	s_addc_u32 s61, s23, 0
	s_add_i32 s51, s40, s27
	global_load_lds_dwordx4 v[228:229], off
	v_lshl_add_u64 v[230:231], s[60:61], 0, v[142:143]
	s_mov_b32 m0, s51
	v_lshl_add_u64 v[232:233], s[24:25], 0, v[140:141]
	global_load_lds_dwordx4 v[230:231], off
	v_lshl_add_u64 v[230:231], s[60:61], 0, v[138:139]
	s_add_i32 m0, s51, 0x2000
	s_nop 0
	global_load_lds_dwordx4 v[230:231], off
	v_lshl_add_u64 v[230:231], s[24:25], 0, v[144:145]
	s_mov_b32 m0, s29
	s_nop 0
	global_load_lds_dwordx4 v[230:231], off
	s_mov_b32 m0, s30
	s_nop 0
	global_load_lds_dwordx4 v[232:233], off
	s_waitcnt vmcnt(8)
	s_waitcnt lgkmcnt(0)
	s_barrier
	s_setprio 1
	s_waitcnt lgkmcnt(0)
	v_mfma_f32_16x16x32_f16 v[94:97], v[98:101], v[196:199], 0
	v_mfma_f32_16x16x32_f16 v[90:93], v[158:161], v[196:199], 0
	v_mfma_f32_16x16x32_f16 v[86:89], v[98:101], v[204:207], 0
	v_mfma_f32_16x16x32_f16 v[82:85], v[158:161], v[204:207], 0
	v_mfma_f32_16x16x32_f16 v[78:81], v[98:101], v[212:215], 0
	v_mfma_f32_16x16x32_f16 v[74:77], v[158:161], v[212:215], 0
	v_mfma_f32_16x16x32_f16 v[70:73], v[98:101], v[220:223], 0
	v_mfma_f32_16x16x32_f16 v[66:69], v[158:161], v[220:223], 0
	v_mfma_f32_16x16x32_f16 v[94:97], v[102:105], v[200:203], v[94:97]
	v_mfma_f32_16x16x32_f16 v[90:93], v[164:167], v[200:203], v[90:93]
	v_mfma_f32_16x16x32_f16 v[86:89], v[102:105], v[208:211], v[86:89]
	v_mfma_f32_16x16x32_f16 v[82:85], v[164:167], v[208:211], v[82:85]
	v_mfma_f32_16x16x32_f16 v[78:81], v[102:105], v[216:219], v[78:81]
	v_mfma_f32_16x16x32_f16 v[74:77], v[164:167], v[216:219], v[74:77]
	v_mfma_f32_16x16x32_f16 v[70:73], v[102:105], v[224:227], v[70:73]
	v_mfma_f32_16x16x32_f16 v[66:69], v[164:167], v[224:227], v[66:69]
	s_setprio 0
	s_setprio 1
	v_mfma_f32_16x16x32_f16 v[30:33], v[178:181], v[196:199], 0
	v_mfma_f32_16x16x32_f16 v[26:29], v[188:191], v[196:199], 0
	v_mfma_f32_16x16x32_f16 v[22:25], v[178:181], v[204:207], 0
	v_mfma_f32_16x16x32_f16 v[18:21], v[188:191], v[204:207], 0
	v_mfma_f32_16x16x32_f16 v[14:17], v[178:181], v[212:215], 0
	v_mfma_f32_16x16x32_f16 v[10:13], v[188:191], v[212:215], 0
	v_mfma_f32_16x16x32_f16 v[6:9], v[178:181], v[220:223], 0
	v_mfma_f32_16x16x32_f16 v[2:5], v[188:191], v[220:223], 0
	v_mfma_f32_16x16x32_f16 v[30:33], v[182:185], v[200:203], v[30:33]
	v_mfma_f32_16x16x32_f16 v[26:29], v[192:195], v[200:203], v[26:29]
	v_mfma_f32_16x16x32_f16 v[22:25], v[182:185], v[208:211], v[22:25]
	v_mfma_f32_16x16x32_f16 v[18:21], v[192:195], v[208:211], v[18:21]
	s_setprio 2
	s_barrier
	v_mfma_f32_16x16x32_f16 v[14:17], v[182:185], v[216:219], v[14:17]
	v_mfma_f32_16x16x32_f16 v[10:13], v[192:195], v[216:219], v[10:13]
	v_mfma_f32_16x16x32_f16 v[6:9], v[182:185], v[224:227], v[6:9]
	v_mfma_f32_16x16x32_f16 v[2:5], v[192:195], v[224:227], v[2:5]
	s_setprio 0
	s_nop 0
	s_add_i32 s51, 0, 0x18000
	s_add_i32 s60, 0, 0x1c000
	v_add_u32_e32 v164, s51, v163
	v_add_u32_e32 v177, s60, v163
	ds_read_b128 v[98:101], v164
	ds_read_b128 v[102:105], v164 offset:1024
	ds_read_b128 v[158:161], v164 offset:2048
	ds_read_b128 v[164:167], v164 offset:3072
	ds_read_b128 v[178:181], v177
	ds_read_b128 v[182:185], v177 offset:1024
	ds_read_b128 v[188:191], v177 offset:2048
	ds_read_b128 v[192:195], v177 offset:3072
	s_add_u32 s24, s24, 0x28000
	s_addc_u32 s25, s25, 0
	s_mov_b32 m0, s31
	v_lshl_add_u64 v[234:235], s[24:25], 0, v[144:145]
	ds_read_b128 v[196:199], v176 offset:32768
	ds_read_b128 v[200:203], v176 offset:33792
	ds_read_b128 v[204:207], v176 offset:34816
	ds_read_b128 v[208:211], v176 offset:35840
	ds_read_b128 v[212:215], v176 offset:36864
	ds_read_b128 v[216:219], v176 offset:37888
	ds_read_b128 v[220:223], v176 offset:38912
	ds_read_b128 v[224:227], v176 offset:39936
	global_load_lds_dwordx4 v[234:235], off
	v_lshl_add_u64 v[234:235], s[24:25], 0, v[140:141]
	s_mov_b32 m0, s33
	s_nop 0
	global_load_lds_dwordx4 v[234:235], off
	s_waitcnt vmcnt(8)
	s_waitcnt lgkmcnt(0)
	s_barrier
	s_setprio 1
	s_waitcnt lgkmcnt(0)
	v_mfma_f32_16x16x32_f16 v[134:137], v[98:101], v[196:199], v[134:137]
	v_mfma_f32_16x16x32_f16 v[130:133], v[158:161], v[196:199], v[130:133]
	v_mfma_f32_16x16x32_f16 v[126:129], v[98:101], v[204:207], v[126:129]
	v_mfma_f32_16x16x32_f16 v[122:125], v[158:161], v[204:207], v[122:125]
	v_mfma_f32_16x16x32_f16 v[118:121], v[98:101], v[212:215], v[118:121]
	v_mfma_f32_16x16x32_f16 v[114:117], v[158:161], v[212:215], v[114:117]
	v_mfma_f32_16x16x32_f16 v[110:113], v[98:101], v[220:223], v[110:113]
	v_mfma_f32_16x16x32_f16 v[106:109], v[158:161], v[220:223], v[106:109]
	v_mfma_f32_16x16x32_f16 v[134:137], v[102:105], v[200:203], v[134:137]
	v_mfma_f32_16x16x32_f16 v[130:133], v[164:167], v[200:203], v[130:133]
	v_mfma_f32_16x16x32_f16 v[126:129], v[102:105], v[208:211], v[126:129]
	v_mfma_f32_16x16x32_f16 v[122:125], v[164:167], v[208:211], v[122:125]
	v_mfma_f32_16x16x32_f16 v[118:121], v[102:105], v[216:219], v[118:121]
	v_mfma_f32_16x16x32_f16 v[114:117], v[164:167], v[216:219], v[114:117]
	v_mfma_f32_16x16x32_f16 v[110:113], v[102:105], v[224:227], v[110:113]
	v_mfma_f32_16x16x32_f16 v[106:109], v[164:167], v[224:227], v[106:109]
	s_setprio 0
	s_setprio 1
	v_mfma_f32_16x16x32_f16 v[62:65], v[178:181], v[196:199], v[62:65]
	v_mfma_f32_16x16x32_f16 v[58:61], v[188:191], v[196:199], v[58:61]
	v_mfma_f32_16x16x32_f16 v[54:57], v[178:181], v[204:207], v[54:57]
	v_mfma_f32_16x16x32_f16 v[50:53], v[188:191], v[204:207], v[50:53]
	v_mfma_f32_16x16x32_f16 v[46:49], v[178:181], v[212:215], v[46:49]
	v_mfma_f32_16x16x32_f16 v[42:45], v[188:191], v[212:215], v[42:45]
	v_mfma_f32_16x16x32_f16 v[38:41], v[178:181], v[220:223], v[38:41]
	v_mfma_f32_16x16x32_f16 v[34:37], v[188:191], v[220:223], v[34:37]
	v_mfma_f32_16x16x32_f16 v[62:65], v[182:185], v[200:203], v[62:65]
	v_mfma_f32_16x16x32_f16 v[58:61], v[192:195], v[200:203], v[58:61]
	v_mfma_f32_16x16x32_f16 v[54:57], v[182:185], v[208:211], v[54:57]
	v_mfma_f32_16x16x32_f16 v[50:53], v[192:195], v[208:211], v[50:53]
	s_setprio 2
	s_barrier
	v_mfma_f32_16x16x32_f16 v[46:49], v[182:185], v[216:219], v[46:49]
	v_mfma_f32_16x16x32_f16 v[42:45], v[192:195], v[216:219], v[42:45]
	v_mfma_f32_16x16x32_f16 v[38:41], v[182:185], v[224:227], v[38:41]
	v_mfma_f32_16x16x32_f16 v[34:37], v[192:195], v[224:227], v[34:37]
	s_setprio 0
	s_nop 0
	s_add_i32 s24, s51, s27
	v_lshl_add_u64 v[168:169], v[168:169], 0, s[14:15]
	s_mov_b32 m0, s24
	ds_read_b128 v[196:199], v176 offset:49152
	ds_read_b128 v[200:203], v176 offset:50176
	ds_read_b128 v[204:207], v176 offset:51200
	ds_read_b128 v[208:211], v176 offset:52224
	ds_read_b128 v[212:215], v176 offset:53248
	ds_read_b128 v[216:219], v176 offset:54272
	ds_read_b128 v[220:223], v176 offset:55296
	ds_read_b128 v[224:227], v176 offset:56320
	global_load_lds_dwordx4 v[168:169], off
	s_add_i32 m0, s24, 0x2000
	s_add_u32 s22, s22, 0x28080
	v_lshl_add_u64 v[168:169], v[228:229], 0, s[14:15]
	s_addc_u32 s23, s23, 0
	s_add_i32 s24, s60, s27
	global_load_lds_dwordx4 v[168:169], off
	v_lshl_add_u64 v[168:169], s[22:23], 0, v[142:143]
	s_mov_b32 m0, s24
	s_nop 0
	global_load_lds_dwordx4 v[168:169], off
	v_lshl_add_u64 v[168:169], s[22:23], 0, v[138:139]
	s_add_i32 m0, s24, 0x2000
	s_nop 0
	global_load_lds_dwordx4 v[168:169], off
	v_lshl_add_u64 v[168:169], v[230:231], 0, s[14:15]
	s_mov_b32 m0, s36
	s_nop 0
	global_load_lds_dwordx4 v[168:169], off
	v_lshl_add_u64 v[168:169], v[232:233], 0, s[14:15]
	s_mov_b32 m0, s37
	s_nop 0
	global_load_lds_dwordx4 v[168:169], off
	s_waitcnt vmcnt(8)
	s_waitcnt lgkmcnt(0)
	s_barrier
	s_setprio 1
	s_waitcnt lgkmcnt(0)
	v_mfma_f32_16x16x32_f16 v[94:97], v[98:101], v[196:199], v[94:97]
	v_mfma_f32_16x16x32_f16 v[90:93], v[158:161], v[196:199], v[90:93]
	v_mfma_f32_16x16x32_f16 v[86:89], v[98:101], v[204:207], v[86:89]
	v_mfma_f32_16x16x32_f16 v[82:85], v[158:161], v[204:207], v[82:85]
	v_mfma_f32_16x16x32_f16 v[78:81], v[98:101], v[212:215], v[78:81]
	v_mfma_f32_16x16x32_f16 v[74:77], v[158:161], v[212:215], v[74:77]
	v_mfma_f32_16x16x32_f16 v[70:73], v[98:101], v[220:223], v[70:73]
	v_mfma_f32_16x16x32_f16 v[66:69], v[158:161], v[220:223], v[66:69]
	v_mfma_f32_16x16x32_f16 v[94:97], v[102:105], v[200:203], v[94:97]
	v_mfma_f32_16x16x32_f16 v[90:93], v[164:167], v[200:203], v[90:93]
	v_mfma_f32_16x16x32_f16 v[86:89], v[102:105], v[208:211], v[86:89]
	v_mfma_f32_16x16x32_f16 v[82:85], v[164:167], v[208:211], v[82:85]
	v_mfma_f32_16x16x32_f16 v[78:81], v[102:105], v[216:219], v[78:81]
	v_mfma_f32_16x16x32_f16 v[74:77], v[164:167], v[216:219], v[74:77]
	v_mfma_f32_16x16x32_f16 v[70:73], v[102:105], v[224:227], v[70:73]
	v_mfma_f32_16x16x32_f16 v[66:69], v[164:167], v[224:227], v[66:69]
	s_setprio 0
	s_setprio 1
	v_mfma_f32_16x16x32_f16 v[30:33], v[178:181], v[196:199], v[30:33]
	v_mfma_f32_16x16x32_f16 v[26:29], v[188:191], v[196:199], v[26:29]
	v_mfma_f32_16x16x32_f16 v[22:25], v[178:181], v[204:207], v[22:25]
	v_mfma_f32_16x16x32_f16 v[18:21], v[188:191], v[204:207], v[18:21]
	v_mfma_f32_16x16x32_f16 v[14:17], v[178:181], v[212:215], v[14:17]
	v_mfma_f32_16x16x32_f16 v[10:13], v[188:191], v[212:215], v[10:13]
	v_mfma_f32_16x16x32_f16 v[6:9], v[178:181], v[220:223], v[6:9]
	v_mfma_f32_16x16x32_f16 v[2:5], v[188:191], v[220:223], v[2:5]
	v_mfma_f32_16x16x32_f16 v[30:33], v[182:185], v[200:203], v[30:33]
	v_mfma_f32_16x16x32_f16 v[26:29], v[192:195], v[200:203], v[26:29]
	v_mfma_f32_16x16x32_f16 v[22:25], v[182:185], v[208:211], v[22:25]
	v_mfma_f32_16x16x32_f16 v[18:21], v[192:195], v[208:211], v[18:21]
	s_setprio 2
	s_barrier
	v_mfma_f32_16x16x32_f16 v[14:17], v[182:185], v[216:219], v[14:17]
	v_mfma_f32_16x16x32_f16 v[10:13], v[192:195], v[216:219], v[10:13]
	v_mfma_f32_16x16x32_f16 v[6:9], v[182:185], v[224:227], v[6:9]
	v_mfma_f32_16x16x32_f16 v[2:5], v[192:195], v[224:227], v[2:5]
	s_setprio 0
	s_nop 0
	s_add_i32 s50, s50, 2
	s_add_u32 s20, s20, 0x100
	s_addc_u32 s21, s21, 0
	s_add_u32 s48, s48, 0x100
	s_addc_u32 s49, s49, 0
	s_cmp_gt_u32 s50, 7
	s_cbranch_scc0 .LBB0_1649
	s_branch .Lpeel_exit_6

.Lpeel_exit_6:
	s_and_b64 vcc, exec, s[16:17]
	s_cbranch_vccz .LBB0_1652
	s_barrier

.LBB0_1733:
	s_ashr_i32 s19, s18, 31
	s_lshl_b64 s[20:21], s[18:19], 19
	s_add_u32 s20, s6, s20
	s_addc_u32 s21, s7, s21
	s_and_b64 s[22:23], s[4:5], exec
	s_cselect_b32 s19, s21, s27
	s_cselect_b32 s46, s20, s26
	s_ashr_i32 s17, s16, 31
	s_lshl_b64 s[22:23], s[16:17], 19
	s_add_u32 s22, s33, s22
	s_addc_u32 s23, s34, s23
	s_and_b64 s[30:31], s[4:5], exec
	s_cselect_b32 s17, s23, s29
	s_cselect_b32 s47, s22, s28
	s_add_u32 s26, s26, 0x40080
	s_addc_u32 s27, s27, 0
	s_add_u32 s48, s28, 0x100
	s_addc_u32 s49, s29, 0
	s_mov_b32 s50, -2
	ds_read_b128 v[130:133], v177
	ds_read_b128 v[134:137], v177 offset:1024
	ds_read_b128 v[138:141], v177 offset:2048
	ds_read_b128 v[142:145], v177 offset:3072
	ds_read_b128 v[164:167], v178
	ds_read_b128 v[168:171], v178 offset:1024
	ds_read_b128 v[172:175], v178 offset:2048
	ds_read_b128 v[180:183], v178 offset:3072
	s_add_u32 s28, s26, 0xfffc0080
	s_addc_u32 s29, s27, -1
	s_cmp_eq_u32 s50, 12
	s_cselect_b32 s31, s19, s29
	s_cselect_b32 s30, s46, s28
	s_cselect_b32 s29, s17, s49
	s_cselect_b32 s28, s47, s48
	v_lshl_add_u64 v[184:185], s[26:27], 0, v[154:155]
	s_add_i32 m0, s25, 0xc000
	ds_read_b128 v[188:191], v179
	ds_read_b128 v[192:195], v179 offset:1024
	ds_read_b128 v[196:199], v179 offset:2048
	ds_read_b128 v[200:203], v179 offset:3072
	ds_read_b128 v[204:207], v179 offset:4096
	ds_read_b128 v[208:211], v179 offset:5120
	ds_read_b128 v[212:215], v179 offset:6144
	ds_read_b128 v[216:219], v179 offset:7168
	global_load_lds_dwordx4 v[184:185], off
	v_lshl_add_u64 v[184:185], s[26:27], 0, v[156:157]
	s_add_i32 m0, s25, 0xe000
	s_nop 0
	global_load_lds_dwordx4 v[184:185], off
	s_waitcnt vmcnt(8)
	s_waitcnt lgkmcnt(0)
	s_barrier
	s_setprio 1
	s_waitcnt lgkmcnt(0)
	v_mfma_f32_16x16x32_f16 v[126:129], v[130:133], v[188:191], 0
	v_mfma_f32_16x16x32_f16 v[122:125], v[138:141], v[188:191], 0
	v_mfma_f32_16x16x32_f16 v[118:121], v[130:133], v[196:199], 0
	v_mfma_f32_16x16x32_f16 v[114:117], v[138:141], v[196:199], 0
	v_mfma_f32_16x16x32_f16 v[110:113], v[130:133], v[204:207], 0
	v_mfma_f32_16x16x32_f16 v[106:109], v[138:141], v[204:207], 0
	v_mfma_f32_16x16x32_f16 v[102:105], v[130:133], v[212:215], 0
	v_mfma_f32_16x16x32_f16 v[98:101], v[138:141], v[212:215], 0
	v_mfma_f32_16x16x32_f16 v[126:129], v[134:137], v[192:195], v[126:129]
	v_mfma_f32_16x16x32_f16 v[122:125], v[142:145], v[192:195], v[122:125]
	v_mfma_f32_16x16x32_f16 v[118:121], v[134:137], v[200:203], v[118:121]
	v_mfma_f32_16x16x32_f16 v[114:117], v[142:145], v[200:203], v[114:117]
	v_mfma_f32_16x16x32_f16 v[110:113], v[134:137], v[208:211], v[110:113]
	v_mfma_f32_16x16x32_f16 v[106:109], v[142:145], v[208:211], v[106:109]
	v_mfma_f32_16x16x32_f16 v[102:105], v[134:137], v[216:219], v[102:105]
	v_mfma_f32_16x16x32_f16 v[98:101], v[142:145], v[216:219], v[98:101]
	s_setprio 0
	s_setprio 1
	v_mfma_f32_16x16x32_f16 v[62:65], v[164:167], v[188:191], 0
	v_mfma_f32_16x16x32_f16 v[58:61], v[172:175], v[188:191], 0
	v_mfma_f32_16x16x32_f16 v[54:57], v[164:167], v[196:199], 0
	v_mfma_f32_16x16x32_f16 v[50:53], v[172:175], v[196:199], 0
	v_mfma_f32_16x16x32_f16 v[46:49], v[164:167], v[204:207], 0
	v_mfma_f32_16x16x32_f16 v[42:45], v[172:175], v[204:207], 0
	v_mfma_f32_16x16x32_f16 v[38:41], v[164:167], v[212:215], 0
	v_mfma_f32_16x16x32_f16 v[34:37], v[172:175], v[212:215], 0
	v_mfma_f32_16x16x32_f16 v[62:65], v[168:171], v[192:195], v[62:65]
	v_mfma_f32_16x16x32_f16 v[58:61], v[180:183], v[192:195], v[58:61]
	v_mfma_f32_16x16x32_f16 v[54:57], v[168:171], v[200:203], v[54:57]
	v_mfma_f32_16x16x32_f16 v[50:53], v[180:183], v[200:203], v[50:53]
	s_setprio 2
	s_barrier
	v_mfma_f32_16x16x32_f16 v[46:49], v[168:171], v[208:211], v[46:49]
	v_mfma_f32_16x16x32_f16 v[42:45], v[180:183], v[208:211], v[42:45]
	v_mfma_f32_16x16x32_f16 v[38:41], v[168:171], v[216:219], v[38:41]
	v_mfma_f32_16x16x32_f16 v[34:37], v[180:183], v[216:219], v[34:37]
	s_setprio 0
	s_nop 0
	s_add_i32 s51, s43, s35
	v_lshl_add_u64 v[184:185], s[28:29], 0, v[148:149]
	s_mov_b32 m0, s51
	ds_read_b128 v[188:191], v179 offset:16384
	ds_read_b128 v[192:195], v179 offset:17408
	ds_read_b128 v[196:199], v179 offset:18432
	ds_read_b128 v[200:203], v179 offset:19456
	ds_read_b128 v[204:207], v179 offset:20480
	ds_read_b128 v[208:211], v179 offset:21504
	ds_read_b128 v[212:215], v179 offset:22528
	ds_read_b128 v[216:219], v179 offset:23552
	global_load_lds_dwordx4 v[184:185], off
	s_add_i32 m0, s51, 0x2000
	s_add_u32 s60, s28, 0x40000
	v_lshl_add_u64 v[220:221], s[28:29], 0, v[152:153]
	s_addc_u32 s61, s29, 0
	s_add_i32 s51, s44, s35
	global_load_lds_dwordx4 v[220:221], off
	v_lshl_add_u64 v[222:223], s[60:61], 0, v[148:149]
	s_mov_b32 m0, s51
	v_lshl_add_u64 v[224:225], s[30:31], 0, v[150:151]
	global_load_lds_dwordx4 v[222:223], off
	v_lshl_add_u64 v[222:223], s[60:61], 0, v[152:153]
	s_add_i32 m0, s51, 0x2000
	s_nop 0
	global_load_lds_dwordx4 v[222:223], off
	v_lshl_add_u64 v[222:223], s[30:31], 0, v[146:147]
	s_mov_b32 m0, s25
	s_nop 0
	global_load_lds_dwordx4 v[222:223], off
	s_mov_b32 m0, s36
	s_nop 0
	global_load_lds_dwordx4 v[224:225], off
	s_waitcnt vmcnt(8)
	s_waitcnt lgkmcnt(0)
	s_barrier
	s_setprio 1
	s_waitcnt lgkmcnt(0)
	v_mfma_f32_16x16x32_f16 v[94:97], v[130:133], v[188:191], 0
	v_mfma_f32_16x16x32_f16 v[90:93], v[138:141], v[188:191], 0
	v_mfma_f32_16x16x32_f16 v[86:89], v[130:133], v[196:199], 0
	v_mfma_f32_16x16x32_f16 v[82:85], v[138:141], v[196:199], 0
	v_mfma_f32_16x16x32_f16 v[78:81], v[130:133], v[204:207], 0
	v_mfma_f32_16x16x32_f16 v[74:77], v[138:141], v[204:207], 0
	v_mfma_f32_16x16x32_f16 v[70:73], v[130:133], v[212:215], 0
	v_mfma_f32_16x16x32_f16 v[66:69], v[138:141], v[212:215], 0
	v_mfma_f32_16x16x32_f16 v[94:97], v[134:137], v[192:195], v[94:97]
	v_mfma_f32_16x16x32_f16 v[90:93], v[142:145], v[192:195], v[90:93]
	v_mfma_f32_16x16x32_f16 v[86:89], v[134:137], v[200:203], v[86:89]
	v_mfma_f32_16x16x32_f16 v[82:85], v[142:145], v[200:203], v[82:85]
	v_mfma_f32_16x16x32_f16 v[78:81], v[134:137], v[208:211], v[78:81]
	v_mfma_f32_16x16x32_f16 v[74:77], v[142:145], v[208:211], v[74:77]
	v_mfma_f32_16x16x32_f16 v[70:73], v[134:137], v[216:219], v[70:73]
	v_mfma_f32_16x16x32_f16 v[66:69], v[142:145], v[216:219], v[66:69]
	s_setprio 0
	s_setprio 1
	v_mfma_f32_16x16x32_f16 v[30:33], v[164:167], v[188:191], 0
	v_mfma_f32_16x16x32_f16 v[26:29], v[172:175], v[188:191], 0
	v_mfma_f32_16x16x32_f16 v[22:25], v[164:167], v[196:199], 0
	v_mfma_f32_16x16x32_f16 v[18:21], v[172:175], v[196:199], 0
	v_mfma_f32_16x16x32_f16 v[14:17], v[164:167], v[204:207], 0
	v_mfma_f32_16x16x32_f16 v[10:13], v[172:175], v[204:207], 0
	v_mfma_f32_16x16x32_f16 v[6:9], v[164:167], v[212:215], 0
	v_mfma_f32_16x16x32_f16 v[2:5], v[172:175], v[212:215], 0
	v_mfma_f32_16x16x32_f16 v[30:33], v[168:171], v[192:195], v[30:33]
	v_mfma_f32_16x16x32_f16 v[26:29], v[180:183], v[192:195], v[26:29]
	v_mfma_f32_16x16x32_f16 v[22:25], v[168:171], v[200:203], v[22:25]
	v_mfma_f32_16x16x32_f16 v[18:21], v[180:183], v[200:203], v[18:21]
	s_setprio 2
	s_barrier
	v_mfma_f32_16x16x32_f16 v[14:17], v[168:171], v[208:211], v[14:17]
	v_mfma_f32_16x16x32_f16 v[10:13], v[180:183], v[208:211], v[10:13]
	v_mfma_f32_16x16x32_f16 v[6:9], v[168:171], v[216:219], v[6:9]
	v_mfma_f32_16x16x32_f16 v[2:5], v[180:183], v[216:219], v[2:5]
	s_setprio 0
	s_nop 0
	s_add_i32 s51, 0, 0x18000
	s_add_i32 s60, 0, 0x1c000
	v_add_u32_e32 v142, s51, v163
	v_add_u32_e32 v180, s60, v163
	ds_read_b128 v[130:133], v142
	ds_read_b128 v[134:137], v142 offset:1024
	ds_read_b128 v[138:141], v142 offset:2048
	ds_read_b128 v[142:145], v142 offset:3072
	ds_read_b128 v[164:167], v180
	ds_read_b128 v[168:171], v180 offset:1024
	ds_read_b128 v[172:175], v180 offset:2048
	ds_read_b128 v[180:183], v180 offset:3072
	s_add_u32 s30, s30, 0x40000
	s_addc_u32 s31, s31, 0
	s_mov_b32 m0, s37
	v_lshl_add_u64 v[226:227], s[30:31], 0, v[146:147]
	ds_read_b128 v[188:191], v179 offset:32768
	ds_read_b128 v[192:195], v179 offset:33792
	ds_read_b128 v[196:199], v179 offset:34816
	ds_read_b128 v[200:203], v179 offset:35840
	ds_read_b128 v[204:207], v179 offset:36864
	ds_read_b128 v[208:211], v179 offset:37888
	ds_read_b128 v[212:215], v179 offset:38912
	ds_read_b128 v[216:219], v179 offset:39936
	global_load_lds_dwordx4 v[226:227], off
	v_lshl_add_u64 v[226:227], s[30:31], 0, v[150:151]
	s_mov_b32 m0, s38
	s_nop 0
	global_load_lds_dwordx4 v[226:227], off
	s_waitcnt vmcnt(8)
	s_waitcnt lgkmcnt(0)
	s_barrier
	s_setprio 1
	s_waitcnt lgkmcnt(0)
	v_mfma_f32_16x16x32_f16 v[126:129], v[130:133], v[188:191], v[126:129]
	v_mfma_f32_16x16x32_f16 v[122:125], v[138:141], v[188:191], v[122:125]
	v_mfma_f32_16x16x32_f16 v[118:121], v[130:133], v[196:199], v[118:121]
	v_mfma_f32_16x16x32_f16 v[114:117], v[138:141], v[196:199], v[114:117]
	v_mfma_f32_16x16x32_f16 v[110:113], v[130:133], v[204:207], v[110:113]
	v_mfma_f32_16x16x32_f16 v[106:109], v[138:141], v[204:207], v[106:109]
	v_mfma_f32_16x16x32_f16 v[102:105], v[130:133], v[212:215], v[102:105]
	v_mfma_f32_16x16x32_f16 v[98:101], v[138:141], v[212:215], v[98:101]
	v_mfma_f32_16x16x32_f16 v[126:129], v[134:137], v[192:195], v[126:129]
	v_mfma_f32_16x16x32_f16 v[122:125], v[142:145], v[192:195], v[122:125]
	v_mfma_f32_16x16x32_f16 v[118:121], v[134:137], v[200:203], v[118:121]
	v_mfma_f32_16x16x32_f16 v[114:117], v[142:145], v[200:203], v[114:117]
	v_mfma_f32_16x16x32_f16 v[110:113], v[134:137], v[208:211], v[110:113]
	v_mfma_f32_16x16x32_f16 v[106:109], v[142:145], v[208:211], v[106:109]
	v_mfma_f32_16x16x32_f16 v[102:105], v[134:137], v[216:219], v[102:105]
	v_mfma_f32_16x16x32_f16 v[98:101], v[142:145], v[216:219], v[98:101]
	s_setprio 0
	s_setprio 1
	v_mfma_f32_16x16x32_f16 v[62:65], v[164:167], v[188:191], v[62:65]
	v_mfma_f32_16x16x32_f16 v[58:61], v[172:175], v[188:191], v[58:61]
	v_mfma_f32_16x16x32_f16 v[54:57], v[164:167], v[196:199], v[54:57]
	v_mfma_f32_16x16x32_f16 v[50:53], v[172:175], v[196:199], v[50:53]
	v_mfma_f32_16x16x32_f16 v[46:49], v[164:167], v[204:207], v[46:49]
	v_mfma_f32_16x16x32_f16 v[42:45], v[172:175], v[204:207], v[42:45]
	v_mfma_f32_16x16x32_f16 v[38:41], v[164:167], v[212:215], v[38:41]
	v_mfma_f32_16x16x32_f16 v[34:37], v[172:175], v[212:215], v[34:37]
	v_mfma_f32_16x16x32_f16 v[62:65], v[168:171], v[192:195], v[62:65]
	v_mfma_f32_16x16x32_f16 v[58:61], v[180:183], v[192:195], v[58:61]
	v_mfma_f32_16x16x32_f16 v[54:57], v[168:171], v[200:203], v[54:57]
	v_mfma_f32_16x16x32_f16 v[50:53], v[180:183], v[200:203], v[50:53]
	s_setprio 2
	s_barrier
	v_mfma_f32_16x16x32_f16 v[46:49], v[168:171], v[208:211], v[46:49]
	v_mfma_f32_16x16x32_f16 v[42:45], v[180:183], v[208:211], v[42:45]
	v_mfma_f32_16x16x32_f16 v[38:41], v[168:171], v[216:219], v[38:41]
	v_mfma_f32_16x16x32_f16 v[34:37], v[180:183], v[216:219], v[34:37]
	s_setprio 0
	s_nop 0
	s_add_i32 s30, s51, s35
	v_lshl_add_u64 v[184:185], v[184:185], 0, s[12:13]
	s_mov_b32 m0, s30
	ds_read_b128 v[188:191], v179 offset:49152
	ds_read_b128 v[192:195], v179 offset:50176
	ds_read_b128 v[196:199], v179 offset:51200
	ds_read_b128 v[200:203], v179 offset:52224
	ds_read_b128 v[204:207], v179 offset:53248
	ds_read_b128 v[208:211], v179 offset:54272
	ds_read_b128 v[212:215], v179 offset:55296
	ds_read_b128 v[216:219], v179 offset:56320
	global_load_lds_dwordx4 v[184:185], off
	s_add_i32 m0, s30, 0x2000
	s_add_u32 s28, s28, 0x40080
	v_lshl_add_u64 v[184:185], v[220:221], 0, s[12:13]
	s_addc_u32 s29, s29, 0
	s_add_i32 s30, s60, s35
	global_load_lds_dwordx4 v[184:185], off
	v_lshl_add_u64 v[184:185], s[28:29], 0, v[148:149]
	s_mov_b32 m0, s30
	s_nop 0
	global_load_lds_dwordx4 v[184:185], off
	v_lshl_add_u64 v[184:185], s[28:29], 0, v[152:153]
	s_add_i32 m0, s30, 0x2000
	s_nop 0
	global_load_lds_dwordx4 v[184:185], off
	v_lshl_add_u64 v[184:185], v[222:223], 0, s[12:13]
	s_mov_b32 m0, s40
	s_nop 0
	global_load_lds_dwordx4 v[184:185], off
	v_lshl_add_u64 v[184:185], v[224:225], 0, s[12:13]
	s_mov_b32 m0, s41
	s_nop 0
	global_load_lds_dwordx4 v[184:185], off
	s_waitcnt vmcnt(8)
	s_waitcnt lgkmcnt(0)
	s_barrier
	s_setprio 1
	s_waitcnt lgkmcnt(0)
	v_mfma_f32_16x16x32_f16 v[94:97], v[130:133], v[188:191], v[94:97]
	v_mfma_f32_16x16x32_f16 v[90:93], v[138:141], v[188:191], v[90:93]
	v_mfma_f32_16x16x32_f16 v[86:89], v[130:133], v[196:199], v[86:89]
	v_mfma_f32_16x16x32_f16 v[82:85], v[138:141], v[196:199], v[82:85]
	v_mfma_f32_16x16x32_f16 v[78:81], v[130:133], v[204:207], v[78:81]
	v_mfma_f32_16x16x32_f16 v[74:77], v[138:141], v[204:207], v[74:77]
	v_mfma_f32_16x16x32_f16 v[70:73], v[130:133], v[212:215], v[70:73]
	v_mfma_f32_16x16x32_f16 v[66:69], v[138:141], v[212:215], v[66:69]
	v_mfma_f32_16x16x32_f16 v[94:97], v[134:137], v[192:195], v[94:97]
	v_mfma_f32_16x16x32_f16 v[90:93], v[142:145], v[192:195], v[90:93]
	v_mfma_f32_16x16x32_f16 v[86:89], v[134:137], v[200:203], v[86:89]
	v_mfma_f32_16x16x32_f16 v[82:85], v[142:145], v[200:203], v[82:85]
	v_mfma_f32_16x16x32_f16 v[78:81], v[134:137], v[208:211], v[78:81]
	v_mfma_f32_16x16x32_f16 v[74:77], v[142:145], v[208:211], v[74:77]
	v_mfma_f32_16x16x32_f16 v[70:73], v[134:137], v[216:219], v[70:73]
	v_mfma_f32_16x16x32_f16 v[66:69], v[142:145], v[216:219], v[66:69]
	s_setprio 0
	s_setprio 1
	v_mfma_f32_16x16x32_f16 v[30:33], v[164:167], v[188:191], v[30:33]
	v_mfma_f32_16x16x32_f16 v[26:29], v[172:175], v[188:191], v[26:29]
	v_mfma_f32_16x16x32_f16 v[22:25], v[164:167], v[196:199], v[22:25]
	v_mfma_f32_16x16x32_f16 v[18:21], v[172:175], v[196:199], v[18:21]
	v_mfma_f32_16x16x32_f16 v[14:17], v[164:167], v[204:207], v[14:17]
	v_mfma_f32_16x16x32_f16 v[10:13], v[172:175], v[204:207], v[10:13]
	v_mfma_f32_16x16x32_f16 v[6:9], v[164:167], v[212:215], v[6:9]
	v_mfma_f32_16x16x32_f16 v[2:5], v[172:175], v[212:215], v[2:5]
	v_mfma_f32_16x16x32_f16 v[30:33], v[168:171], v[192:195], v[30:33]
	v_mfma_f32_16x16x32_f16 v[26:29], v[180:183], v[192:195], v[26:29]
	v_mfma_f32_16x16x32_f16 v[22:25], v[168:171], v[200:203], v[22:25]
	v_mfma_f32_16x16x32_f16 v[18:21], v[180:183], v[200:203], v[18:21]
	s_setprio 2
	s_barrier
	v_mfma_f32_16x16x32_f16 v[14:17], v[168:171], v[208:211], v[14:17]
	v_mfma_f32_16x16x32_f16 v[10:13], v[180:183], v[208:211], v[10:13]
	v_mfma_f32_16x16x32_f16 v[6:9], v[168:171], v[216:219], v[6:9]
	v_mfma_f32_16x16x32_f16 v[2:5], v[180:183], v[216:219], v[2:5]
	s_setprio 0
	s_nop 0
	s_add_i32 s50, s50, 2
	s_add_u32 s26, s26, 0x100
	s_addc_u32 s27, s27, 0
	s_add_u32 s48, s48, 0x100
	s_addc_u32 s49, s49, 0
	s_cmp_gt_u32 s50, 13
	s_cbranch_scc0 .LBB0_1734
	s_branch .Lpeel_exit_7

.LBB0_1812:
	s_ashr_i32 s25, s24, 31
	s_lshl_b64 s[26:27], s[24:25], 20
	s_add_u32 s26, s15, s26
	s_addc_u32 s27, s33, s27
	s_and_b64 s[28:29], s[4:5], exec
	s_cselect_b32 s25, s27, s35
	s_cselect_b32 s61, s26, s34
	s_ashr_i32 s23, s22, 31
	s_lshl_b64 s[28:29], s[22:23], 20
	s_add_u32 s28, s40, s28
	s_addc_u32 s29, s41, s29
	s_and_b64 s[38:39], s[4:5], exec
	s_cselect_b32 s23, s29, s37
	s_cselect_b32 s62, s28, s36
	s_add_u32 s34, s34, 0x80080
	s_addc_u32 s35, s35, 0
	s_add_u32 s63, s36, 0x100
	s_addc_u32 s64, s37, 0
	s_mov_b32 s65, -2
	ds_read_b128 v[146:149], v154
	ds_read_b128 v[158:161], v154 offset:1024
	ds_read_b128 v[164:167], v154 offset:2048
	ds_read_b128 v[168:171], v154 offset:3072
	ds_read_b128 v[172:175], v155
	ds_read_b128 v[176:179], v155 offset:1024
	ds_read_b128 v[180:183], v155 offset:2048
	ds_read_b128 v[188:191], v155 offset:3072
	s_add_u32 s36, s34, 0xfff80080
	s_addc_u32 s37, s35, -1
	s_cmp_eq_u32 s65, 28
	s_cselect_b32 s39, s25, s37
	s_cselect_b32 s38, s61, s36
	s_cselect_b32 s37, s23, s64
	s_cselect_b32 s36, s62, s63
	v_lshl_add_u64 v[150:151], s[34:35], 0, v[138:139]
	s_add_i32 m0, s31, 0xc000
	ds_read_b128 v[192:195], v156
	ds_read_b128 v[196:199], v156 offset:1024
	ds_read_b128 v[200:203], v156 offset:2048
	ds_read_b128 v[204:207], v156 offset:3072
	ds_read_b128 v[208:211], v156 offset:4096
	ds_read_b128 v[212:215], v156 offset:5120
	ds_read_b128 v[216:219], v156 offset:6144
	ds_read_b128 v[220:223], v156 offset:7168
	global_load_lds_dwordx4 v[150:151], off
	v_lshl_add_u64 v[150:151], s[34:35], 0, v[140:141]
	s_add_i32 m0, s31, 0xe000
	s_nop 0
	global_load_lds_dwordx4 v[150:151], off
	s_waitcnt vmcnt(8)
	s_waitcnt lgkmcnt(0)
	s_barrier
	s_setprio 1
	s_waitcnt lgkmcnt(0)
	v_mfma_f32_16x16x32_f16 v[126:129], v[146:149], v[192:195], 0
	v_mfma_f32_16x16x32_f16 v[122:125], v[164:167], v[192:195], 0
	v_mfma_f32_16x16x32_f16 v[110:113], v[146:149], v[200:203], 0
	v_mfma_f32_16x16x32_f16 v[106:109], v[164:167], v[200:203], 0
	v_mfma_f32_16x16x32_f16 v[94:97], v[146:149], v[208:211], 0
	v_mfma_f32_16x16x32_f16 v[90:93], v[164:167], v[208:211], 0
	v_mfma_f32_16x16x32_f16 v[78:81], v[146:149], v[216:219], 0
	v_mfma_f32_16x16x32_f16 v[74:77], v[164:167], v[216:219], 0
	v_mfma_f32_16x16x32_f16 v[126:129], v[158:161], v[196:199], v[126:129]
	v_mfma_f32_16x16x32_f16 v[122:125], v[168:171], v[196:199], v[122:125]
	v_mfma_f32_16x16x32_f16 v[110:113], v[158:161], v[204:207], v[110:113]
	v_mfma_f32_16x16x32_f16 v[106:109], v[168:171], v[204:207], v[106:109]
	v_mfma_f32_16x16x32_f16 v[94:97], v[158:161], v[212:215], v[94:97]
	v_mfma_f32_16x16x32_f16 v[90:93], v[168:171], v[212:215], v[90:93]
	v_mfma_f32_16x16x32_f16 v[78:81], v[158:161], v[220:223], v[78:81]
	v_mfma_f32_16x16x32_f16 v[74:77], v[168:171], v[220:223], v[74:77]
	s_setprio 0
	s_setprio 1
	v_mfma_f32_16x16x32_f16 v[118:121], v[172:175], v[192:195], 0
	v_mfma_f32_16x16x32_f16 v[114:117], v[180:183], v[192:195], 0
	v_mfma_f32_16x16x32_f16 v[102:105], v[172:175], v[200:203], 0
	v_mfma_f32_16x16x32_f16 v[98:101], v[180:183], v[200:203], 0
	v_mfma_f32_16x16x32_f16 v[86:89], v[172:175], v[208:211], 0
	v_mfma_f32_16x16x32_f16 v[82:85], v[180:183], v[208:211], 0
	v_mfma_f32_16x16x32_f16 v[70:73], v[172:175], v[216:219], 0
	v_mfma_f32_16x16x32_f16 v[66:69], v[180:183], v[216:219], 0
	v_mfma_f32_16x16x32_f16 v[118:121], v[176:179], v[196:199], v[118:121]
	v_mfma_f32_16x16x32_f16 v[114:117], v[188:191], v[196:199], v[114:117]
	v_mfma_f32_16x16x32_f16 v[102:105], v[176:179], v[204:207], v[102:105]
	v_mfma_f32_16x16x32_f16 v[98:101], v[188:191], v[204:207], v[98:101]
	s_setprio 2
	s_barrier
	v_mfma_f32_16x16x32_f16 v[86:89], v[176:179], v[212:215], v[86:89]
	v_mfma_f32_16x16x32_f16 v[82:85], v[188:191], v[212:215], v[82:85]
	v_mfma_f32_16x16x32_f16 v[70:73], v[176:179], v[220:223], v[70:73]
	v_mfma_f32_16x16x32_f16 v[66:69], v[188:191], v[220:223], v[66:69]
	s_setprio 0
	s_nop 0
	s_add_i32 s66, s50, s42
	v_lshl_add_u64 v[150:151], s[36:37], 0, v[132:133]
	s_mov_b32 m0, s66
	ds_read_b128 v[192:195], v156 offset:16384
	ds_read_b128 v[196:199], v156 offset:17408
	ds_read_b128 v[200:203], v156 offset:18432
	ds_read_b128 v[204:207], v156 offset:19456
	ds_read_b128 v[208:211], v156 offset:20480
	ds_read_b128 v[212:215], v156 offset:21504
	ds_read_b128 v[216:219], v156 offset:22528
	ds_read_b128 v[220:223], v156 offset:23552
	global_load_lds_dwordx4 v[150:151], off
	s_add_i32 m0, s66, 0x2000
	s_add_u32 s66, s36, 0x80000
	v_lshl_add_u64 v[184:185], s[36:37], 0, v[136:137]
	s_addc_u32 s67, s37, 0
	s_add_i32 s68, s51, s42
	global_load_lds_dwordx4 v[184:185], off
	v_lshl_add_u64 v[224:225], s[66:67], 0, v[132:133]
	s_mov_b32 m0, s68
	v_lshl_add_u64 v[226:227], s[38:39], 0, v[134:135]
	global_load_lds_dwordx4 v[224:225], off
	v_lshl_add_u64 v[224:225], s[66:67], 0, v[136:137]
	s_add_i32 m0, s68, 0x2000
	s_nop 0
	global_load_lds_dwordx4 v[224:225], off
	v_lshl_add_u64 v[224:225], s[38:39], 0, v[130:131]
	s_mov_b32 m0, s31
	s_nop 0
	global_load_lds_dwordx4 v[224:225], off
	s_mov_b32 m0, s43
	s_nop 0
	global_load_lds_dwordx4 v[226:227], off
	s_waitcnt vmcnt(8)
	s_waitcnt lgkmcnt(0)
	s_barrier
	s_setprio 1
	s_waitcnt lgkmcnt(0)
	v_mfma_f32_16x16x32_f16 v[62:65], v[146:149], v[192:195], 0
	v_mfma_f32_16x16x32_f16 v[58:61], v[164:167], v[192:195], 0
	v_mfma_f32_16x16x32_f16 v[46:49], v[146:149], v[200:203], 0
	v_mfma_f32_16x16x32_f16 v[42:45], v[164:167], v[200:203], 0
	v_mfma_f32_16x16x32_f16 v[30:33], v[146:149], v[208:211], 0
	v_mfma_f32_16x16x32_f16 v[26:29], v[164:167], v[208:211], 0
	v_mfma_f32_16x16x32_f16 v[14:17], v[146:149], v[216:219], 0
	v_mfma_f32_16x16x32_f16 v[10:13], v[164:167], v[216:219], 0
	v_mfma_f32_16x16x32_f16 v[62:65], v[158:161], v[196:199], v[62:65]
	v_mfma_f32_16x16x32_f16 v[58:61], v[168:171], v[196:199], v[58:61]
	v_mfma_f32_16x16x32_f16 v[46:49], v[158:161], v[204:207], v[46:49]
	v_mfma_f32_16x16x32_f16 v[42:45], v[168:171], v[204:207], v[42:45]
	v_mfma_f32_16x16x32_f16 v[30:33], v[158:161], v[212:215], v[30:33]
	v_mfma_f32_16x16x32_f16 v[26:29], v[168:171], v[212:215], v[26:29]
	v_mfma_f32_16x16x32_f16 v[14:17], v[158:161], v[220:223], v[14:17]
	v_mfma_f32_16x16x32_f16 v[10:13], v[168:171], v[220:223], v[10:13]
	s_setprio 0
	s_setprio 1
	v_mfma_f32_16x16x32_f16 v[54:57], v[172:175], v[192:195], 0
	v_mfma_f32_16x16x32_f16 v[50:53], v[180:183], v[192:195], 0
	v_mfma_f32_16x16x32_f16 v[38:41], v[172:175], v[200:203], 0
	v_mfma_f32_16x16x32_f16 v[34:37], v[180:183], v[200:203], 0
	v_mfma_f32_16x16x32_f16 v[22:25], v[172:175], v[208:211], 0
	v_mfma_f32_16x16x32_f16 v[18:21], v[180:183], v[208:211], 0
	v_mfma_f32_16x16x32_f16 v[6:9], v[172:175], v[216:219], 0
	v_mfma_f32_16x16x32_f16 v[2:5], v[180:183], v[216:219], 0
	v_mfma_f32_16x16x32_f16 v[54:57], v[176:179], v[196:199], v[54:57]
	v_mfma_f32_16x16x32_f16 v[50:53], v[188:191], v[196:199], v[50:53]
	v_mfma_f32_16x16x32_f16 v[38:41], v[176:179], v[204:207], v[38:41]
	v_mfma_f32_16x16x32_f16 v[34:37], v[188:191], v[204:207], v[34:37]
	s_setprio 2
	s_barrier
	v_mfma_f32_16x16x32_f16 v[22:25], v[176:179], v[212:215], v[22:25]
	v_mfma_f32_16x16x32_f16 v[18:21], v[188:191], v[212:215], v[18:21]
	v_mfma_f32_16x16x32_f16 v[6:9], v[176:179], v[220:223], v[6:9]
	v_mfma_f32_16x16x32_f16 v[2:5], v[188:191], v[220:223], v[2:5]
	s_setprio 0
	s_nop 0
	s_add_i32 s66, 0, 0x18000
	v_add_u32_e32 v157, s66, v152
	s_add_i32 s67, 0, 0x1c000
	ds_read_b128 v[146:149], v157
	ds_read_b128 v[158:161], v157 offset:1024
	ds_read_b128 v[164:167], v157 offset:2048
	ds_read_b128 v[168:171], v157 offset:3072
	v_add_u32_e32 v157, s67, v152
	ds_read_b128 v[172:175], v157
	ds_read_b128 v[176:179], v157 offset:1024
	ds_read_b128 v[180:183], v157 offset:2048
	ds_read_b128 v[188:191], v157 offset:3072
	s_add_u32 s38, s38, 0x80000
	s_addc_u32 s39, s39, 0
	s_mov_b32 m0, s44
	v_lshl_add_u64 v[228:229], s[38:39], 0, v[130:131]
	ds_read_b128 v[192:195], v156 offset:32768
	ds_read_b128 v[196:199], v156 offset:33792
	ds_read_b128 v[200:203], v156 offset:34816
	ds_read_b128 v[204:207], v156 offset:35840
	ds_read_b128 v[208:211], v156 offset:36864
	ds_read_b128 v[212:215], v156 offset:37888
	ds_read_b128 v[216:219], v156 offset:38912
	ds_read_b128 v[220:223], v156 offset:39936
	global_load_lds_dwordx4 v[228:229], off
	v_lshl_add_u64 v[228:229], s[38:39], 0, v[134:135]
	s_mov_b32 m0, s45
	s_nop 0
	global_load_lds_dwordx4 v[228:229], off
	s_waitcnt vmcnt(8)
	s_waitcnt lgkmcnt(0)
	s_barrier
	s_setprio 1
	s_waitcnt lgkmcnt(0)
	v_mfma_f32_16x16x32_f16 v[126:129], v[146:149], v[192:195], v[126:129]
	v_mfma_f32_16x16x32_f16 v[122:125], v[164:167], v[192:195], v[122:125]
	v_mfma_f32_16x16x32_f16 v[110:113], v[146:149], v[200:203], v[110:113]
	v_mfma_f32_16x16x32_f16 v[106:109], v[164:167], v[200:203], v[106:109]
	v_mfma_f32_16x16x32_f16 v[94:97], v[146:149], v[208:211], v[94:97]
	v_mfma_f32_16x16x32_f16 v[90:93], v[164:167], v[208:211], v[90:93]
	v_mfma_f32_16x16x32_f16 v[78:81], v[146:149], v[216:219], v[78:81]
	v_mfma_f32_16x16x32_f16 v[74:77], v[164:167], v[216:219], v[74:77]
	v_mfma_f32_16x16x32_f16 v[126:129], v[158:161], v[196:199], v[126:129]
	v_mfma_f32_16x16x32_f16 v[122:125], v[168:171], v[196:199], v[122:125]
	v_mfma_f32_16x16x32_f16 v[110:113], v[158:161], v[204:207], v[110:113]
	v_mfma_f32_16x16x32_f16 v[106:109], v[168:171], v[204:207], v[106:109]
	v_mfma_f32_16x16x32_f16 v[94:97], v[158:161], v[212:215], v[94:97]
	v_mfma_f32_16x16x32_f16 v[90:93], v[168:171], v[212:215], v[90:93]
	v_mfma_f32_16x16x32_f16 v[78:81], v[158:161], v[220:223], v[78:81]
	v_mfma_f32_16x16x32_f16 v[74:77], v[168:171], v[220:223], v[74:77]
	s_setprio 0
	s_setprio 1
	v_mfma_f32_16x16x32_f16 v[118:121], v[172:175], v[192:195], v[118:121]
	v_mfma_f32_16x16x32_f16 v[114:117], v[180:183], v[192:195], v[114:117]
	v_mfma_f32_16x16x32_f16 v[102:105], v[172:175], v[200:203], v[102:105]
	v_mfma_f32_16x16x32_f16 v[98:101], v[180:183], v[200:203], v[98:101]
	v_mfma_f32_16x16x32_f16 v[86:89], v[172:175], v[208:211], v[86:89]
	v_mfma_f32_16x16x32_f16 v[82:85], v[180:183], v[208:211], v[82:85]
	v_mfma_f32_16x16x32_f16 v[70:73], v[172:175], v[216:219], v[70:73]
	v_mfma_f32_16x16x32_f16 v[66:69], v[180:183], v[216:219], v[66:69]
	v_mfma_f32_16x16x32_f16 v[118:121], v[176:179], v[196:199], v[118:121]
	v_mfma_f32_16x16x32_f16 v[114:117], v[188:191], v[196:199], v[114:117]
	v_mfma_f32_16x16x32_f16 v[102:105], v[176:179], v[204:207], v[102:105]
	v_mfma_f32_16x16x32_f16 v[98:101], v[188:191], v[204:207], v[98:101]
	s_setprio 2
	s_barrier
	v_mfma_f32_16x16x32_f16 v[86:89], v[176:179], v[212:215], v[86:89]
	v_mfma_f32_16x16x32_f16 v[82:85], v[188:191], v[212:215], v[82:85]
	v_mfma_f32_16x16x32_f16 v[70:73], v[176:179], v[220:223], v[70:73]
	v_mfma_f32_16x16x32_f16 v[66:69], v[188:191], v[220:223], v[66:69]
	s_setprio 0
	s_nop 0
	s_add_i32 s38, s66, s42
	v_lshl_add_u64 v[150:151], v[150:151], 0, s[10:11]
	s_mov_b32 m0, s38
	ds_read_b128 v[192:195], v156 offset:49152
	ds_read_b128 v[196:199], v156 offset:50176
	ds_read_b128 v[200:203], v156 offset:51200
	ds_read_b128 v[204:207], v156 offset:52224
	ds_read_b128 v[208:211], v156 offset:53248
	ds_read_b128 v[212:215], v156 offset:54272
	ds_read_b128 v[216:219], v156 offset:55296
	ds_read_b128 v[220:223], v156 offset:56320
	global_load_lds_dwordx4 v[150:151], off
	s_add_i32 m0, s38, 0x2000
	s_add_u32 s36, s36, 0x80080
	v_lshl_add_u64 v[150:151], v[184:185], 0, s[10:11]
	s_addc_u32 s37, s37, 0
	s_add_i32 s38, s67, s42
	global_load_lds_dwordx4 v[150:151], off
	v_lshl_add_u64 v[150:151], s[36:37], 0, v[132:133]
	s_mov_b32 m0, s38
	s_nop 0
	global_load_lds_dwordx4 v[150:151], off
	v_lshl_add_u64 v[150:151], s[36:37], 0, v[136:137]
	s_add_i32 m0, s38, 0x2000
	s_nop 0
	global_load_lds_dwordx4 v[150:151], off
	v_lshl_add_u64 v[150:151], v[224:225], 0, s[10:11]
	s_mov_b32 m0, s47
	s_nop 0
	global_load_lds_dwordx4 v[150:151], off
	v_lshl_add_u64 v[150:151], v[226:227], 0, s[10:11]
	s_mov_b32 m0, s48
	s_nop 0
	global_load_lds_dwordx4 v[150:151], off
	s_waitcnt vmcnt(8)
	s_waitcnt lgkmcnt(0)
	s_barrier
	s_setprio 1
	s_waitcnt lgkmcnt(0)
	v_mfma_f32_16x16x32_f16 v[62:65], v[146:149], v[192:195], v[62:65]
	v_mfma_f32_16x16x32_f16 v[58:61], v[164:167], v[192:195], v[58:61]
	v_mfma_f32_16x16x32_f16 v[46:49], v[146:149], v[200:203], v[46:49]
	v_mfma_f32_16x16x32_f16 v[42:45], v[164:167], v[200:203], v[42:45]
	v_mfma_f32_16x16x32_f16 v[30:33], v[146:149], v[208:211], v[30:33]
	v_mfma_f32_16x16x32_f16 v[26:29], v[164:167], v[208:211], v[26:29]
	v_mfma_f32_16x16x32_f16 v[14:17], v[146:149], v[216:219], v[14:17]
	v_mfma_f32_16x16x32_f16 v[10:13], v[164:167], v[216:219], v[10:13]
	v_mfma_f32_16x16x32_f16 v[62:65], v[158:161], v[196:199], v[62:65]
	v_mfma_f32_16x16x32_f16 v[58:61], v[168:171], v[196:199], v[58:61]
	v_mfma_f32_16x16x32_f16 v[46:49], v[158:161], v[204:207], v[46:49]
	v_mfma_f32_16x16x32_f16 v[42:45], v[168:171], v[204:207], v[42:45]
	v_mfma_f32_16x16x32_f16 v[30:33], v[158:161], v[212:215], v[30:33]
	v_mfma_f32_16x16x32_f16 v[26:29], v[168:171], v[212:215], v[26:29]
	v_mfma_f32_16x16x32_f16 v[14:17], v[158:161], v[220:223], v[14:17]
	v_mfma_f32_16x16x32_f16 v[10:13], v[168:171], v[220:223], v[10:13]
	s_setprio 0
	s_setprio 1
	v_mfma_f32_16x16x32_f16 v[54:57], v[172:175], v[192:195], v[54:57]
	v_mfma_f32_16x16x32_f16 v[50:53], v[180:183], v[192:195], v[50:53]
	v_mfma_f32_16x16x32_f16 v[38:41], v[172:175], v[200:203], v[38:41]
	v_mfma_f32_16x16x32_f16 v[34:37], v[180:183], v[200:203], v[34:37]
	v_mfma_f32_16x16x32_f16 v[22:25], v[172:175], v[208:211], v[22:25]
	v_mfma_f32_16x16x32_f16 v[18:21], v[180:183], v[208:211], v[18:21]
	v_mfma_f32_16x16x32_f16 v[6:9], v[172:175], v[216:219], v[6:9]
	v_mfma_f32_16x16x32_f16 v[2:5], v[180:183], v[216:219], v[2:5]
	v_mfma_f32_16x16x32_f16 v[54:57], v[176:179], v[196:199], v[54:57]
	v_mfma_f32_16x16x32_f16 v[50:53], v[188:191], v[196:199], v[50:53]
	v_mfma_f32_16x16x32_f16 v[38:41], v[176:179], v[204:207], v[38:41]
	v_mfma_f32_16x16x32_f16 v[34:37], v[188:191], v[204:207], v[34:37]
	s_setprio 2
	s_barrier
	v_mfma_f32_16x16x32_f16 v[22:25], v[176:179], v[212:215], v[22:25]
	v_mfma_f32_16x16x32_f16 v[18:21], v[188:191], v[212:215], v[18:21]
	v_mfma_f32_16x16x32_f16 v[6:9], v[176:179], v[220:223], v[6:9]
	v_mfma_f32_16x16x32_f16 v[2:5], v[188:191], v[220:223], v[2:5]
	s_setprio 0
	s_nop 0
	s_add_i32 s65, s65, 2
	s_add_u32 s34, s34, 0x100
	s_addc_u32 s35, s35, 0
	s_add_u32 s63, s63, 0x100
	s_addc_u32 s64, s64, 0
	s_cmp_gt_u32 s65, 29
	s_cbranch_scc0 .LBB0_1813
	s_branch .Lpeel_exit_8

.LBB0_1956:
	s_ashr_i32 s19, s18, 31
	s_lshl_b64 s[20:21], s[18:19], 19
	s_add_u32 s20, s29, s20
	s_addc_u32 s21, s30, s21
	s_and_b64 s[26:27], s[4:5], exec
	s_cselect_b32 s19, s21, s23
	s_cselect_b32 s68, s20, s22
	s_lshl_b32 s24, s24, 9
	s_add_i32 s24, s24, 0
	s_add_i32 s24, s24, 0x20000
	v_lshl_add_u32 v2, v190, 1, s24
	v_lshl_add_u32 v3, v191, 1, s24
	ds_read_u16 v4, v2
	ds_read_u16 v5, v3
	ds_read_u16 v3, v3 offset:256
	ds_read_u16 v2, v2 offset:256
	v_mov_b32_e32 v175, v169
	v_mov_b32_e32 v177, v169
	s_add_u32 s69, s22, 0x100
	s_waitcnt lgkmcnt(0)
	v_lshl_or_b32 v198, v4, 11, v163
	v_lshl_or_b32 v199, v5, 11, v163
	v_lshl_or_b32 v200, v2, 11, v163
	v_lshl_or_b32 v201, v3, 11, v163
	v_lshl_add_u64 v[178:179], s[12:13], 0, v[176:177]
	v_lshl_add_u64 v[180:181], s[12:13], 0, v[174:175]
	s_addc_u32 s70, s23, 0
	s_mov_b32 s71, -2
	s_mov_b64 s[22:23], 0
	ds_read_b128 v[26:29], v194
	ds_read_b128 v[30:33], v194 offset:1024
	ds_read_b128 v[18:21], v194 offset:2048
	ds_read_b128 v[22:25], v194 offset:3072
	ds_read_b128 v[10:13], v195
	ds_read_b128 v[14:17], v195 offset:1024
	ds_read_b128 v[2:5], v195 offset:2048
	ds_read_b128 v[6:9], v195 offset:3072
	s_add_u32 s24, s58, s22
	s_addc_u32 s25, s59, s23
	s_add_u32 s26, s24, 0x50a00100
	s_addc_u32 s27, s25, 0
	s_add_u32 s72, s69, s22
	s_addc_u32 s73, s70, s23
	s_cmpk_eq_i32 s22, 0x700
	s_cselect_b64 vcc, -1, 0
	s_and_b64 s[24:25], vcc, exec
	v_cndmask_b32_e32 v168, v202, v198, vcc
	v_cndmask_b32_e32 v186, v172, v199, vcc
	v_cndmask_b32_e32 v175, v174, v200, vcc
	v_cndmask_b32_e32 v177, v176, v201, vcc
	s_cselect_b32 s27, s1, s27
	s_cselect_b32 s26, s0, s26
	s_cselect_b32 s25, s19, s73
	s_cselect_b32 s24, s68, s72
	v_lshl_add_u64 v[182:183], v[180:181], 0, s[22:23]
	s_add_i32 m0, s36, 0xc000
	ds_read_b128 v[204:207], v196
	ds_read_b128 v[208:211], v196 offset:1024
	ds_read_b128 v[212:215], v196 offset:2048
	ds_read_b128 v[216:219], v196 offset:3072
	ds_read_b128 v[220:223], v196 offset:4096
	ds_read_b128 v[224:227], v196 offset:5120
	ds_read_b128 v[228:231], v196 offset:6144
	ds_read_b128 v[232:235], v196 offset:7168
	global_load_lds_dwordx4 v[182:183], off
	v_lshl_add_u64 v[182:183], v[178:179], 0, s[22:23]
	s_add_i32 m0, s36, 0xe000
	s_nop 0
	global_load_lds_dwordx4 v[182:183], off
	s_waitcnt vmcnt(8)
	s_waitcnt lgkmcnt(0)
	s_barrier
	s_setprio 1
	s_waitcnt lgkmcnt(0)
	v_mfma_f32_16x16x128_f8f6f4 v[158:161], v[26:33], v[204:211], 0
	v_mfma_f32_16x16x128_f8f6f4 v[150:153], v[18:25], v[204:211], 0
	v_mfma_f32_16x16x128_f8f6f4 v[142:145], v[26:33], v[212:219], 0
	v_mfma_f32_16x16x128_f8f6f4 v[134:137], v[18:25], v[212:219], 0
	v_mfma_f32_16x16x128_f8f6f4 v[126:129], v[26:33], v[220:227], 0
	v_mfma_f32_16x16x128_f8f6f4 v[118:121], v[18:25], v[220:227], 0
	v_mfma_f32_16x16x128_f8f6f4 v[110:113], v[26:33], v[228:235], 0
	v_mfma_f32_16x16x128_f8f6f4 v[102:105], v[18:25], v[228:235], 0
	s_setprio 0
	s_setprio 1
	v_mfma_f32_16x16x128_f8f6f4 v[154:157], v[10:17], v[204:211], 0
	v_mfma_f32_16x16x128_f8f6f4 v[146:149], v[2:9], v[204:211], 0
	v_mfma_f32_16x16x128_f8f6f4 v[138:141], v[10:17], v[212:219], 0
	v_mfma_f32_16x16x128_f8f6f4 v[130:133], v[2:9], v[212:219], 0
	v_mfma_f32_16x16x128_f8f6f4 v[122:125], v[10:17], v[220:227], 0
	v_mfma_f32_16x16x128_f8f6f4 v[114:117], v[2:9], v[220:227], 0
	s_setprio 2
	s_barrier
	v_mfma_f32_16x16x128_f8f6f4 v[106:109], v[10:17], v[228:235], 0
	v_mfma_f32_16x16x128_f8f6f4 v[98:101], v[2:9], v[228:235], 0
	s_setprio 0
	s_nop 0
	s_add_i32 s72, s44, s28
	v_lshl_add_u64 v[182:183], s[24:25], 0, v[166:167]
	s_mov_b32 m0, s72
	ds_read_b128 v[204:207], v196 offset:16384
	ds_read_b128 v[208:211], v196 offset:17408
	ds_read_b128 v[212:215], v196 offset:18432
	ds_read_b128 v[216:219], v196 offset:19456
	ds_read_b128 v[220:223], v196 offset:20480
	ds_read_b128 v[224:227], v196 offset:21504
	ds_read_b128 v[228:231], v196 offset:22528
	ds_read_b128 v[232:235], v196 offset:23552
	global_load_lds_dwordx4 v[182:183], off
	s_add_i32 m0, s72, 0x2000
	s_add_u32 s72, s24, 0x40000
	v_lshl_add_u64 v[184:185], s[24:25], 0, v[164:165]
	s_addc_u32 s73, s25, 0
	s_add_i32 s74, s45, s28
	global_load_lds_dwordx4 v[184:185], off
	v_lshl_add_u64 v[188:189], s[72:73], 0, v[166:167]
	s_mov_b32 m0, s74
	v_mov_b32_e32 v187, v169
	global_load_lds_dwordx4 v[188:189], off
	v_lshl_add_u64 v[188:189], s[72:73], 0, v[164:165]
	s_add_i32 m0, s74, 0x2000
	s_nop 0
	global_load_lds_dwordx4 v[188:189], off
	s_mov_b32 m0, s36
	v_lshl_add_u64 v[188:189], s[26:27], 0, v[168:169]
	global_load_lds_dwordx4 v168, s[26:27]
	s_mov_b32 m0, s37
	s_nop 0
	global_load_lds_dwordx4 v186, s[26:27]
	s_waitcnt vmcnt(8)
	s_waitcnt lgkmcnt(0)
	v_lshl_add_u64 v[186:187], s[26:27], 0, v[186:187]
	s_barrier
	s_setprio 1
	s_waitcnt lgkmcnt(0)
	v_mfma_f32_16x16x128_f8f6f4 v[94:97], v[26:33], v[204:211], 0
	v_mfma_f32_16x16x128_f8f6f4 v[86:89], v[18:25], v[204:211], 0
	v_mfma_f32_16x16x128_f8f6f4 v[78:81], v[26:33], v[212:219], 0
	v_mfma_f32_16x16x128_f8f6f4 v[70:73], v[18:25], v[212:219], 0
	v_mfma_f32_16x16x128_f8f6f4 v[62:65], v[26:33], v[220:227], 0
	v_mfma_f32_16x16x128_f8f6f4 v[54:57], v[18:25], v[220:227], 0
	v_mfma_f32_16x16x128_f8f6f4 v[46:49], v[26:33], v[228:235], 0
	v_mfma_f32_16x16x128_f8f6f4 v[38:41], v[18:25], v[228:235], 0
	s_setprio 0
	s_setprio 1
	v_mfma_f32_16x16x128_f8f6f4 v[90:93], v[10:17], v[204:211], 0
	v_mfma_f32_16x16x128_f8f6f4 v[82:85], v[2:9], v[204:211], 0
	v_mfma_f32_16x16x128_f8f6f4 v[74:77], v[10:17], v[212:219], 0
	v_mfma_f32_16x16x128_f8f6f4 v[66:69], v[2:9], v[212:219], 0
	v_mfma_f32_16x16x128_f8f6f4 v[58:61], v[10:17], v[220:227], 0
	v_mfma_f32_16x16x128_f8f6f4 v[50:53], v[2:9], v[220:227], 0
	s_setprio 2
	s_barrier
	v_mfma_f32_16x16x128_f8f6f4 v[42:45], v[10:17], v[228:235], 0
	v_mfma_f32_16x16x128_f8f6f4 v[34:37], v[2:9], v[228:235], 0
	s_setprio 0
	s_nop 0
	s_add_i32 s72, 0, 0x18000
	s_add_i32 s73, 0, 0x1c000
	v_add_u32_e32 v14, s72, v192
	v_add_u32_e32 v30, s73, v192
	ds_read_b128 v[2:5], v14
	ds_read_b128 v[6:9], v14 offset:1024
	ds_read_b128 v[10:13], v14 offset:2048
	ds_read_b128 v[14:17], v14 offset:3072
	ds_read_b128 v[18:21], v30
	ds_read_b128 v[22:25], v30 offset:1024
	ds_read_b128 v[26:29], v30 offset:2048
	ds_read_b128 v[30:33], v30 offset:3072
	s_mov_b32 m0, s38
	ds_read_b128 v[204:207], v196 offset:32768
	ds_read_b128 v[208:211], v196 offset:33792
	ds_read_b128 v[212:215], v196 offset:34816
	ds_read_b128 v[216:219], v196 offset:35840
	ds_read_b128 v[220:223], v196 offset:36864
	ds_read_b128 v[224:227], v196 offset:37888
	ds_read_b128 v[228:231], v196 offset:38912
	ds_read_b128 v[232:235], v196 offset:39936
	global_load_lds_dwordx4 v175, s[26:27]
	s_mov_b32 m0, s39
	s_nop 0
	global_load_lds_dwordx4 v177, s[26:27]
	s_waitcnt vmcnt(8)
	s_waitcnt lgkmcnt(0)
	s_barrier
	s_setprio 1
	s_waitcnt lgkmcnt(0)
	v_mfma_f32_16x16x128_f8f6f4 v[158:161], v[2:9], v[204:211], v[158:161]
	v_mfma_f32_16x16x128_f8f6f4 v[150:153], v[10:17], v[204:211], v[150:153]
	v_mfma_f32_16x16x128_f8f6f4 v[142:145], v[2:9], v[212:219], v[142:145]
	v_mfma_f32_16x16x128_f8f6f4 v[134:137], v[10:17], v[212:219], v[134:137]
	v_mfma_f32_16x16x128_f8f6f4 v[126:129], v[2:9], v[220:227], v[126:129]
	v_mfma_f32_16x16x128_f8f6f4 v[118:121], v[10:17], v[220:227], v[118:121]
	v_mfma_f32_16x16x128_f8f6f4 v[110:113], v[2:9], v[228:235], v[110:113]
	v_mfma_f32_16x16x128_f8f6f4 v[102:105], v[10:17], v[228:235], v[102:105]
	s_setprio 0
	s_setprio 1
	v_mfma_f32_16x16x128_f8f6f4 v[154:157], v[18:25], v[204:211], v[154:157]
	v_mfma_f32_16x16x128_f8f6f4 v[146:149], v[26:33], v[204:211], v[146:149]
	v_mfma_f32_16x16x128_f8f6f4 v[138:141], v[18:25], v[212:219], v[138:141]
	v_mfma_f32_16x16x128_f8f6f4 v[130:133], v[26:33], v[212:219], v[130:133]
	v_mfma_f32_16x16x128_f8f6f4 v[122:125], v[18:25], v[220:227], v[122:125]
	v_mfma_f32_16x16x128_f8f6f4 v[114:117], v[26:33], v[220:227], v[114:117]
	s_setprio 2
	s_barrier
	v_mfma_f32_16x16x128_f8f6f4 v[106:109], v[18:25], v[228:235], v[106:109]
	v_mfma_f32_16x16x128_f8f6f4 v[98:101], v[26:33], v[228:235], v[98:101]
	s_setprio 0
	s_nop 0
	s_add_i32 s26, s72, s28
	v_lshl_add_u64 v[182:183], v[182:183], 0, s[10:11]
	s_mov_b32 m0, s26
	ds_read_b128 v[204:207], v196 offset:49152
	ds_read_b128 v[208:211], v196 offset:50176
	ds_read_b128 v[212:215], v196 offset:51200
	ds_read_b128 v[216:219], v196 offset:52224
	ds_read_b128 v[220:223], v196 offset:53248
	ds_read_b128 v[224:227], v196 offset:54272
	ds_read_b128 v[228:231], v196 offset:55296
	ds_read_b128 v[232:235], v196 offset:56320
	global_load_lds_dwordx4 v[182:183], off
	s_add_i32 m0, s26, 0x2000
	s_add_u32 s24, s24, 0x40080
	v_lshl_add_u64 v[182:183], v[184:185], 0, s[10:11]
	s_addc_u32 s25, s25, 0
	s_add_i32 s26, s73, s28
	global_load_lds_dwordx4 v[182:183], off
	v_lshl_add_u64 v[182:183], s[24:25], 0, v[166:167]
	s_mov_b32 m0, s26
	s_nop 0
	global_load_lds_dwordx4 v[182:183], off
	v_lshl_add_u64 v[182:183], s[24:25], 0, v[164:165]
	s_add_i32 m0, s26, 0x2000
	s_nop 0
	global_load_lds_dwordx4 v[182:183], off
	v_lshl_add_u64 v[182:183], v[188:189], 0, s[10:11]
	s_mov_b32 m0, s40
	s_nop 0
	global_load_lds_dwordx4 v[182:183], off
	v_lshl_add_u64 v[182:183], v[186:187], 0, s[10:11]
	s_mov_b32 m0, s41
	s_nop 0
	global_load_lds_dwordx4 v[182:183], off
	s_waitcnt vmcnt(8)
	s_waitcnt lgkmcnt(0)
	s_barrier
	s_setprio 1
	s_waitcnt lgkmcnt(0)
	v_mfma_f32_16x16x128_f8f6f4 v[94:97], v[2:9], v[204:211], v[94:97]
	v_mfma_f32_16x16x128_f8f6f4 v[86:89], v[10:17], v[204:211], v[86:89]
	v_mfma_f32_16x16x128_f8f6f4 v[78:81], v[2:9], v[212:219], v[78:81]
	v_mfma_f32_16x16x128_f8f6f4 v[70:73], v[10:17], v[212:219], v[70:73]
	v_mfma_f32_16x16x128_f8f6f4 v[62:65], v[2:9], v[220:227], v[62:65]
	v_mfma_f32_16x16x128_f8f6f4 v[54:57], v[10:17], v[220:227], v[54:57]
	v_mfma_f32_16x16x128_f8f6f4 v[46:49], v[2:9], v[228:235], v[46:49]
	v_mfma_f32_16x16x128_f8f6f4 v[38:41], v[10:17], v[228:235], v[38:41]
	s_setprio 0
	s_setprio 1
	v_mfma_f32_16x16x128_f8f6f4 v[90:93], v[18:25], v[204:211], v[90:93]
	v_mfma_f32_16x16x128_f8f6f4 v[82:85], v[26:33], v[204:211], v[82:85]
	v_mfma_f32_16x16x128_f8f6f4 v[74:77], v[18:25], v[212:219], v[74:77]
	v_mfma_f32_16x16x128_f8f6f4 v[66:69], v[26:33], v[212:219], v[66:69]
	v_mfma_f32_16x16x128_f8f6f4 v[58:61], v[18:25], v[220:227], v[58:61]
	v_mfma_f32_16x16x128_f8f6f4 v[50:53], v[26:33], v[220:227], v[50:53]
	s_setprio 2
	s_barrier
	v_mfma_f32_16x16x128_f8f6f4 v[42:45], v[18:25], v[228:235], v[42:45]
	v_mfma_f32_16x16x128_f8f6f4 v[34:37], v[26:33], v[228:235], v[34:37]
	s_setprio 0
	s_nop 0
	s_add_i32 s71, s71, 2
	s_add_u32 s22, s22, 0x100
	s_addc_u32 s23, s23, 0
	s_cmp_gt_u32 s71, 13
	s_cbranch_scc0 .LBB0_1957
	s_branch .Lpeel_exit_9

.LBB0_2037:
	s_add_u32 s36, s36, 0xe0080
	s_addc_u32 s37, s37, 0
	v_lshl_add_u64 v[180:181], v[2:3], 0, s[22:23]
	s_mov_b32 s79, -2
	ds_read_b128 v[26:29], v200
	ds_read_b128 v[30:33], v200 offset:1024
	ds_read_b128 v[18:21], v200 offset:2048
	ds_read_b128 v[22:25], v200 offset:3072
	ds_read_b128 v[10:13], v201
	ds_read_b128 v[14:17], v201 offset:1024
	ds_read_b128 v[2:5], v201 offset:2048
	ds_read_b128 v[6:9], v201 offset:3072
	s_add_u32 s38, s36, 0xfff20080
	s_addc_u32 s39, s37, -1
	s_cmp_eq_u32 s79, 52
	s_cselect_b64 vcc, -1, 0
	s_cselect_b32 s39, s7, s39
	s_cselect_b32 s38, s6, s38
	v_cndmask_b32_e32 v183, v181, v179, vcc
	v_cndmask_b32_e32 v182, v180, v178, vcc
	v_lshl_add_u64 v[228:229], s[36:37], 0, v[172:173]
	s_add_i32 m0, s60, 0xc000
	ds_read_b128 v[184:187], v202
	ds_read_b128 v[188:191], v202 offset:1024
	ds_read_b128 v[204:207], v202 offset:2048
	ds_read_b128 v[208:211], v202 offset:3072
	ds_read_b128 v[212:215], v202 offset:4096
	ds_read_b128 v[216:219], v202 offset:5120
	ds_read_b128 v[220:223], v202 offset:6144
	ds_read_b128 v[224:227], v202 offset:7168
	global_load_lds_dwordx4 v[228:229], off
	v_lshl_add_u64 v[228:229], s[36:37], 0, v[174:175]
	s_add_i32 m0, s60, 0xe000
	s_nop 0
	global_load_lds_dwordx4 v[228:229], off
	s_waitcnt vmcnt(8)
	s_waitcnt lgkmcnt(0)
	s_barrier
	s_setprio 1
	s_waitcnt lgkmcnt(0)
	v_mfma_f32_16x16x128_f8f6f4 v[158:161], v[26:33], v[184:191], 0
	v_mfma_f32_16x16x128_f8f6f4 v[154:157], v[18:25], v[184:191], 0
	v_mfma_f32_16x16x128_f8f6f4 v[150:153], v[26:33], v[204:211], 0
	v_mfma_f32_16x16x128_f8f6f4 v[142:145], v[18:25], v[204:211], 0
	v_mfma_f32_16x16x128_f8f6f4 v[134:137], v[26:33], v[212:219], 0
	v_mfma_f32_16x16x128_f8f6f4 v[126:129], v[18:25], v[212:219], 0
	v_mfma_f32_16x16x128_f8f6f4 v[118:121], v[26:33], v[220:227], 0
	v_mfma_f32_16x16x128_f8f6f4 v[110:113], v[18:25], v[220:227], 0
	s_setprio 0
	s_setprio 1
	v_mfma_f32_16x16x128_f8f6f4 v[146:149], v[10:17], v[184:191], 0
	v_mfma_f32_16x16x128_f8f6f4 v[138:141], v[2:9], v[184:191], 0
	v_mfma_f32_16x16x128_f8f6f4 v[130:133], v[10:17], v[204:211], 0
	v_mfma_f32_16x16x128_f8f6f4 v[122:125], v[2:9], v[204:211], 0
	v_mfma_f32_16x16x128_f8f6f4 v[114:117], v[10:17], v[212:219], 0
	v_mfma_f32_16x16x128_f8f6f4 v[106:109], v[2:9], v[212:219], 0
	s_setprio 2
	s_barrier
	v_mfma_f32_16x16x128_f8f6f4 v[102:105], v[10:17], v[220:227], 0
	v_mfma_f32_16x16x128_f8f6f4 v[98:101], v[2:9], v[220:227], 0
	s_setprio 0
	s_nop 0
	s_add_i32 s80, s69, s25
	v_lshl_add_u64 v[184:185], v[182:183], 0, v[170:171]
	s_mov_b32 m0, s80
	ds_read_b128 v[204:207], v202 offset:16384
	ds_read_b128 v[208:211], v202 offset:17408
	ds_read_b128 v[212:215], v202 offset:18432
	ds_read_b128 v[216:219], v202 offset:19456
	ds_read_b128 v[220:223], v202 offset:20480
	ds_read_b128 v[224:227], v202 offset:21504
	ds_read_b128 v[228:231], v202 offset:22528
	ds_read_b128 v[232:235], v202 offset:23552
	global_load_lds_dwordx4 v[184:185], off
	v_lshl_add_u64 v[186:187], v[182:183], 0, v[168:169]
	s_add_i32 m0, s80, 0x2000
	v_lshl_add_u64 v[188:189], v[182:183], 0, s[10:11]
	s_add_i32 s80, s70, s25
	global_load_lds_dwordx4 v[186:187], off
	v_lshl_add_u64 v[190:191], v[188:189], 0, v[170:171]
	s_mov_b32 m0, s80
	v_lshl_add_u64 v[188:189], v[188:189], 0, v[168:169]
	global_load_lds_dwordx4 v[190:191], off
	s_add_i32 m0, s80, 0x2000
	v_lshl_add_u64 v[190:191], s[38:39], 0, v[166:167]
	global_load_lds_dwordx4 v[188:189], off
	v_lshl_add_u64 v[188:189], s[38:39], 0, v[164:165]
	s_mov_b32 m0, s60
	s_nop 0
	global_load_lds_dwordx4 v[188:189], off
	s_mov_b32 m0, s61
	s_nop 0
	global_load_lds_dwordx4 v[190:191], off
	s_waitcnt vmcnt(8)
	s_waitcnt lgkmcnt(0)
	s_barrier
	s_setprio 1
	s_waitcnt lgkmcnt(0)
	v_mfma_f32_16x16x128_f8f6f4 v[94:97], v[26:33], v[204:211], 0
	v_mfma_f32_16x16x128_f8f6f4 v[90:93], v[18:25], v[204:211], 0
	v_mfma_f32_16x16x128_f8f6f4 v[86:89], v[26:33], v[212:219], 0
	v_mfma_f32_16x16x128_f8f6f4 v[78:81], v[18:25], v[212:219], 0
	v_mfma_f32_16x16x128_f8f6f4 v[70:73], v[26:33], v[220:227], 0
	v_mfma_f32_16x16x128_f8f6f4 v[62:65], v[18:25], v[220:227], 0
	v_mfma_f32_16x16x128_f8f6f4 v[54:57], v[26:33], v[228:235], 0
	v_mfma_f32_16x16x128_f8f6f4 v[46:49], v[18:25], v[228:235], 0
	s_setprio 0
	s_setprio 1
	v_mfma_f32_16x16x128_f8f6f4 v[82:85], v[10:17], v[204:211], 0
	v_mfma_f32_16x16x128_f8f6f4 v[74:77], v[2:9], v[204:211], 0
	v_mfma_f32_16x16x128_f8f6f4 v[66:69], v[10:17], v[212:219], 0
	v_mfma_f32_16x16x128_f8f6f4 v[58:61], v[2:9], v[212:219], 0
	v_mfma_f32_16x16x128_f8f6f4 v[50:53], v[10:17], v[220:227], 0
	v_mfma_f32_16x16x128_f8f6f4 v[42:45], v[2:9], v[220:227], 0
	s_setprio 2
	s_barrier
	v_mfma_f32_16x16x128_f8f6f4 v[38:41], v[10:17], v[228:235], 0
	v_mfma_f32_16x16x128_f8f6f4 v[34:37], v[2:9], v[228:235], 0
	s_setprio 0
	s_nop 0
	s_add_i32 s80, 0, 0x18000
	s_add_i32 s81, 0, 0x1c000
	v_add_u32_e32 v14, s80, v198
	v_add_u32_e32 v30, s81, v198
	ds_read_b128 v[2:5], v14
	ds_read_b128 v[6:9], v14 offset:1024
	ds_read_b128 v[10:13], v14 offset:2048
	ds_read_b128 v[14:17], v14 offset:3072
	ds_read_b128 v[18:21], v30
	ds_read_b128 v[22:25], v30 offset:1024
	ds_read_b128 v[26:29], v30 offset:2048
	ds_read_b128 v[30:33], v30 offset:3072
	s_add_u32 s38, s38, 0xe0000
	s_addc_u32 s39, s39, 0
	s_mov_b32 m0, s62
	v_lshl_add_u64 v[236:237], s[38:39], 0, v[164:165]
	ds_read_b128 v[204:207], v202 offset:32768
	ds_read_b128 v[208:211], v202 offset:33792
	ds_read_b128 v[212:215], v202 offset:34816
	ds_read_b128 v[216:219], v202 offset:35840
	ds_read_b128 v[220:223], v202 offset:36864
	ds_read_b128 v[224:227], v202 offset:37888
	ds_read_b128 v[228:231], v202 offset:38912
	ds_read_b128 v[232:235], v202 offset:39936
	global_load_lds_dwordx4 v[236:237], off
	v_lshl_add_u64 v[236:237], s[38:39], 0, v[166:167]
	s_mov_b32 m0, s63
	s_nop 0
	global_load_lds_dwordx4 v[236:237], off
	s_waitcnt vmcnt(8)
	s_waitcnt lgkmcnt(0)
	s_barrier
	s_setprio 1
	s_waitcnt lgkmcnt(0)
	v_mfma_f32_16x16x128_f8f6f4 v[158:161], v[2:9], v[204:211], v[158:161]
	v_mfma_f32_16x16x128_f8f6f4 v[154:157], v[10:17], v[204:211], v[154:157]
	v_mfma_f32_16x16x128_f8f6f4 v[150:153], v[2:9], v[212:219], v[150:153]
	v_mfma_f32_16x16x128_f8f6f4 v[142:145], v[10:17], v[212:219], v[142:145]
	v_mfma_f32_16x16x128_f8f6f4 v[134:137], v[2:9], v[220:227], v[134:137]
	v_mfma_f32_16x16x128_f8f6f4 v[126:129], v[10:17], v[220:227], v[126:129]
	v_mfma_f32_16x16x128_f8f6f4 v[118:121], v[2:9], v[228:235], v[118:121]
	v_mfma_f32_16x16x128_f8f6f4 v[110:113], v[10:17], v[228:235], v[110:113]
	s_setprio 0
	s_setprio 1
	v_mfma_f32_16x16x128_f8f6f4 v[146:149], v[18:25], v[204:211], v[146:149]
	v_mfma_f32_16x16x128_f8f6f4 v[138:141], v[26:33], v[204:211], v[138:141]
	v_mfma_f32_16x16x128_f8f6f4 v[130:133], v[18:25], v[212:219], v[130:133]
	v_mfma_f32_16x16x128_f8f6f4 v[122:125], v[26:33], v[212:219], v[122:125]
	v_mfma_f32_16x16x128_f8f6f4 v[114:117], v[18:25], v[220:227], v[114:117]
	v_mfma_f32_16x16x128_f8f6f4 v[106:109], v[26:33], v[220:227], v[106:109]
	s_setprio 2
	s_barrier
	v_mfma_f32_16x16x128_f8f6f4 v[102:105], v[18:25], v[228:235], v[102:105]
	v_mfma_f32_16x16x128_f8f6f4 v[98:101], v[26:33], v[228:235], v[98:101]
	s_setprio 0
	s_nop 0
	s_add_i32 s38, s80, s25
	v_lshl_add_u64 v[184:185], v[184:185], 0, s[16:17]
	s_mov_b32 m0, s38
	ds_read_b128 v[204:207], v202 offset:49152
	ds_read_b128 v[208:211], v202 offset:50176
	ds_read_b128 v[212:215], v202 offset:51200
	ds_read_b128 v[216:219], v202 offset:52224
	ds_read_b128 v[220:223], v202 offset:53248
	ds_read_b128 v[224:227], v202 offset:54272
	ds_read_b128 v[228:231], v202 offset:55296
	ds_read_b128 v[232:235], v202 offset:56320
	global_load_lds_dwordx4 v[184:185], off
	v_lshl_add_u64 v[184:185], v[186:187], 0, s[16:17]
	s_add_i32 m0, s38, 0x2000
	v_lshl_add_u64 v[182:183], v[182:183], 0, s[18:19]
	s_add_i32 s38, s81, s25
	global_load_lds_dwordx4 v[184:185], off
	v_lshl_add_u64 v[184:185], v[182:183], 0, v[170:171]
	s_mov_b32 m0, s38
	v_lshl_add_u64 v[182:183], v[182:183], 0, v[168:169]
	global_load_lds_dwordx4 v[184:185], off
	s_add_i32 m0, s38, 0x2000
	s_nop 0
	global_load_lds_dwordx4 v[182:183], off
	v_lshl_add_u64 v[182:183], v[188:189], 0, s[16:17]
	s_mov_b32 m0, s66
	s_nop 0
	global_load_lds_dwordx4 v[182:183], off
	v_lshl_add_u64 v[182:183], v[190:191], 0, s[16:17]
	s_mov_b32 m0, s67
	s_nop 0
	global_load_lds_dwordx4 v[182:183], off
	s_waitcnt vmcnt(8)
	s_waitcnt lgkmcnt(0)
	s_barrier
	s_setprio 1
	s_waitcnt lgkmcnt(0)
	v_mfma_f32_16x16x128_f8f6f4 v[94:97], v[2:9], v[204:211], v[94:97]
	v_mfma_f32_16x16x128_f8f6f4 v[90:93], v[10:17], v[204:211], v[90:93]
	v_mfma_f32_16x16x128_f8f6f4 v[86:89], v[2:9], v[212:219], v[86:89]
	v_mfma_f32_16x16x128_f8f6f4 v[78:81], v[10:17], v[212:219], v[78:81]
	v_mfma_f32_16x16x128_f8f6f4 v[70:73], v[2:9], v[220:227], v[70:73]
	v_mfma_f32_16x16x128_f8f6f4 v[62:65], v[10:17], v[220:227], v[62:65]
	v_mfma_f32_16x16x128_f8f6f4 v[54:57], v[2:9], v[228:235], v[54:57]
	v_mfma_f32_16x16x128_f8f6f4 v[46:49], v[10:17], v[228:235], v[46:49]
	s_setprio 0
	s_setprio 1
	v_mfma_f32_16x16x128_f8f6f4 v[82:85], v[18:25], v[204:211], v[82:85]
	v_mfma_f32_16x16x128_f8f6f4 v[74:77], v[26:33], v[204:211], v[74:77]
	v_mfma_f32_16x16x128_f8f6f4 v[66:69], v[18:25], v[212:219], v[66:69]
	v_mfma_f32_16x16x128_f8f6f4 v[58:61], v[26:33], v[212:219], v[58:61]
	v_mfma_f32_16x16x128_f8f6f4 v[50:53], v[18:25], v[220:227], v[50:53]
	v_mfma_f32_16x16x128_f8f6f4 v[42:45], v[26:33], v[220:227], v[42:45]
	s_setprio 2
	s_barrier
	v_mfma_f32_16x16x128_f8f6f4 v[38:41], v[18:25], v[228:235], v[38:41]
	v_mfma_f32_16x16x128_f8f6f4 v[34:37], v[26:33], v[228:235], v[34:37]
	s_setprio 0
	s_nop 0
	s_add_i32 s79, s79, 2
	s_add_u32 s36, s36, 0x100
	s_addc_u32 s37, s37, 0
	s_cmp_gt_u32 s79, 53
	v_lshl_add_u64 v[180:181], v[180:181], 0, s[22:23]
	s_cbranch_scc0 .LBB0_2038
	s_branch .Lpeel_exit_10

.Lpeel_exit_10:
	s_and_b64 vcc, exec, s[20:21]
	s_cbranch_vccz .LBB0_2041
	s_barrier

.LBB0_2057:
	s_add_u32 s26, s26, 0xe0080
	s_addc_u32 s27, s27, 0
	v_lshl_add_u64 v[176:177], v[2:3], 0, s[22:23]
	s_mov_b32 s28, 0
	ds_read_b128 v[26:29], v1
	ds_read_b128 v[30:33], v1 offset:1024
	ds_read_b128 v[18:21], v1 offset:2048
	ds_read_b128 v[22:25], v1 offset:3072
	ds_read_b128 v[10:13], v190
	ds_read_b128 v[14:17], v190 offset:1024
	ds_read_b128 v[2:5], v190 offset:2048
	ds_read_b128 v[6:9], v190 offset:3072
	s_add_i32 s25, s28, 2
	s_add_u32 s80, s26, 0xfff20080
	s_addc_u32 s29, s27, -1
	s_cmp_eq_u32 s69, s28
	s_cselect_b32 s28, s6, s80
	s_cselect_b64 vcc, -1, 0
	s_cselect_b32 s29, s7, s29
	v_cndmask_b32_e32 v179, v177, v175, vcc
	v_cndmask_b32_e32 v178, v176, v174, vcc
	v_lshl_add_u64 v[218:219], s[26:27], 0, v[168:169]
	s_add_i32 m0, s60, 0xc000
	ds_read_b128 v[180:183], v191
	ds_read_b128 v[184:187], v191 offset:1024
	ds_read_b128 v[194:197], v191 offset:2048
	ds_read_b128 v[198:201], v191 offset:3072
	ds_read_b128 v[202:205], v191 offset:4096
	ds_read_b128 v[206:209], v191 offset:5120
	ds_read_b128 v[210:213], v191 offset:6144
	ds_read_b128 v[214:217], v191 offset:7168
	global_load_lds_dwordx4 v[218:219], off
	v_lshl_add_u64 v[218:219], s[26:27], 0, v[170:171]
	s_add_i32 m0, s60, 0xe000
	s_nop 0
	global_load_lds_dwordx4 v[218:219], off
	s_waitcnt vmcnt(8)
	s_waitcnt lgkmcnt(0)
	s_barrier
	s_setprio 1
	s_waitcnt lgkmcnt(0)
	v_mfma_f32_16x16x128_f8f6f4 v[158:161], v[26:33], v[180:187], 0
	v_mfma_f32_16x16x128_f8f6f4 v[154:157], v[18:25], v[180:187], 0
	v_mfma_f32_16x16x128_f8f6f4 v[150:153], v[26:33], v[194:201], 0
	v_mfma_f32_16x16x128_f8f6f4 v[142:145], v[18:25], v[194:201], 0
	v_mfma_f32_16x16x128_f8f6f4 v[134:137], v[26:33], v[202:209], 0
	v_mfma_f32_16x16x128_f8f6f4 v[126:129], v[18:25], v[202:209], 0
	v_mfma_f32_16x16x128_f8f6f4 v[118:121], v[26:33], v[210:217], 0
	v_mfma_f32_16x16x128_f8f6f4 v[110:113], v[18:25], v[210:217], 0
	s_setprio 0
	s_setprio 1
	v_mfma_f32_16x16x128_f8f6f4 v[146:149], v[10:17], v[180:187], 0
	v_mfma_f32_16x16x128_f8f6f4 v[138:141], v[2:9], v[180:187], 0
	v_mfma_f32_16x16x128_f8f6f4 v[130:133], v[10:17], v[194:201], 0
	v_mfma_f32_16x16x128_f8f6f4 v[122:125], v[2:9], v[194:201], 0
	v_mfma_f32_16x16x128_f8f6f4 v[114:117], v[10:17], v[202:209], 0
	v_mfma_f32_16x16x128_f8f6f4 v[106:109], v[2:9], v[202:209], 0
	s_setprio 2
	s_barrier
	v_mfma_f32_16x16x128_f8f6f4 v[102:105], v[10:17], v[210:217], 0
	v_mfma_f32_16x16x128_f8f6f4 v[98:101], v[2:9], v[210:217], 0
	s_setprio 0
	s_nop 0
	s_add_i32 s80, s71, s34
	v_lshl_add_u64 v[180:181], v[178:179], 0, v[164:165]
	s_mov_b32 m0, s80
	ds_read_b128 v[194:197], v191 offset:16384
	ds_read_b128 v[198:201], v191 offset:17408
	ds_read_b128 v[202:205], v191 offset:18432
	ds_read_b128 v[206:209], v191 offset:19456
	ds_read_b128 v[210:213], v191 offset:20480
	ds_read_b128 v[214:217], v191 offset:21504
	ds_read_b128 v[218:221], v191 offset:22528
	ds_read_b128 v[222:225], v191 offset:23552
	global_load_lds_dwordx4 v[180:181], off
	v_lshl_add_u64 v[182:183], v[178:179], 0, v[166:167]
	s_add_i32 m0, s80, 0x2000
	v_lshl_add_u64 v[184:185], v[178:179], 0, s[10:11]
	s_add_i32 s80, s72, s34
	global_load_lds_dwordx4 v[182:183], off
	v_lshl_add_u64 v[186:187], v[184:185], 0, v[164:165]
	s_mov_b32 m0, s80
	v_lshl_add_u64 v[184:185], v[184:185], 0, v[166:167]
	global_load_lds_dwordx4 v[186:187], off
	s_add_i32 m0, s80, 0x2000
	v_lshl_add_u64 v[186:187], s[28:29], 0, v[166:167]
	global_load_lds_dwordx4 v[184:185], off
	v_lshl_add_u64 v[184:185], s[28:29], 0, v[164:165]
	s_mov_b32 m0, s60
	s_nop 0
	global_load_lds_dwordx4 v[184:185], off
	s_mov_b32 m0, s61
	s_nop 0
	global_load_lds_dwordx4 v[186:187], off
	s_waitcnt vmcnt(8)
	s_waitcnt lgkmcnt(0)
	s_barrier
	s_setprio 1
	s_waitcnt lgkmcnt(0)
	v_mfma_f32_16x16x128_f8f6f4 v[94:97], v[26:33], v[194:201], 0
	v_mfma_f32_16x16x128_f8f6f4 v[90:93], v[18:25], v[194:201], 0
	v_mfma_f32_16x16x128_f8f6f4 v[86:89], v[26:33], v[202:209], 0
	v_mfma_f32_16x16x128_f8f6f4 v[78:81], v[18:25], v[202:209], 0
	v_mfma_f32_16x16x128_f8f6f4 v[70:73], v[26:33], v[210:217], 0
	v_mfma_f32_16x16x128_f8f6f4 v[62:65], v[18:25], v[210:217], 0
	v_mfma_f32_16x16x128_f8f6f4 v[54:57], v[26:33], v[218:225], 0
	v_mfma_f32_16x16x128_f8f6f4 v[46:49], v[18:25], v[218:225], 0
	s_setprio 0
	s_setprio 1
	v_mfma_f32_16x16x128_f8f6f4 v[82:85], v[10:17], v[194:201], 0
	v_mfma_f32_16x16x128_f8f6f4 v[74:77], v[2:9], v[194:201], 0
	v_mfma_f32_16x16x128_f8f6f4 v[66:69], v[10:17], v[202:209], 0
	v_mfma_f32_16x16x128_f8f6f4 v[58:61], v[2:9], v[202:209], 0
	v_mfma_f32_16x16x128_f8f6f4 v[50:53], v[10:17], v[210:217], 0
	v_mfma_f32_16x16x128_f8f6f4 v[42:45], v[2:9], v[210:217], 0
	s_setprio 2
	s_barrier
	v_mfma_f32_16x16x128_f8f6f4 v[38:41], v[10:17], v[218:225], 0
	v_mfma_f32_16x16x128_f8f6f4 v[34:37], v[2:9], v[218:225], 0
	s_setprio 0
	s_nop 0
	s_add_i32 s80, 0, 0x18000
	s_add_i32 s81, 0, 0x1c000
	v_add_u32_e32 v14, s80, v189
	v_add_u32_e32 v30, s81, v189
	ds_read_b128 v[2:5], v14
	ds_read_b128 v[6:9], v14 offset:1024
	ds_read_b128 v[10:13], v14 offset:2048
	ds_read_b128 v[14:17], v14 offset:3072
	ds_read_b128 v[18:21], v30
	ds_read_b128 v[22:25], v30 offset:1024
	ds_read_b128 v[26:29], v30 offset:2048
	ds_read_b128 v[30:33], v30 offset:3072
	s_add_u32 s28, s28, 0xe0000
	s_addc_u32 s29, s29, 0
	s_mov_b32 m0, s62
	v_lshl_add_u64 v[226:227], s[28:29], 0, v[164:165]
	ds_read_b128 v[194:197], v191 offset:32768
	ds_read_b128 v[198:201], v191 offset:33792
	ds_read_b128 v[202:205], v191 offset:34816
	ds_read_b128 v[206:209], v191 offset:35840
	ds_read_b128 v[210:213], v191 offset:36864
	ds_read_b128 v[214:217], v191 offset:37888
	ds_read_b128 v[218:221], v191 offset:38912
	ds_read_b128 v[222:225], v191 offset:39936
	global_load_lds_dwordx4 v[226:227], off
	v_lshl_add_u64 v[226:227], s[28:29], 0, v[166:167]
	s_mov_b32 m0, s63
	s_nop 0
	global_load_lds_dwordx4 v[226:227], off
	s_waitcnt vmcnt(8)
	s_waitcnt lgkmcnt(0)
	s_barrier
	s_setprio 1
	s_waitcnt lgkmcnt(0)
	v_mfma_f32_16x16x128_f8f6f4 v[158:161], v[2:9], v[194:201], v[158:161]
	v_mfma_f32_16x16x128_f8f6f4 v[154:157], v[10:17], v[194:201], v[154:157]
	v_mfma_f32_16x16x128_f8f6f4 v[150:153], v[2:9], v[202:209], v[150:153]
	v_mfma_f32_16x16x128_f8f6f4 v[142:145], v[10:17], v[202:209], v[142:145]
	v_mfma_f32_16x16x128_f8f6f4 v[134:137], v[2:9], v[210:217], v[134:137]
	v_mfma_f32_16x16x128_f8f6f4 v[126:129], v[10:17], v[210:217], v[126:129]
	v_mfma_f32_16x16x128_f8f6f4 v[118:121], v[2:9], v[218:225], v[118:121]
	v_mfma_f32_16x16x128_f8f6f4 v[110:113], v[10:17], v[218:225], v[110:113]
	s_setprio 0
	s_setprio 1
	v_mfma_f32_16x16x128_f8f6f4 v[146:149], v[18:25], v[194:201], v[146:149]
	v_mfma_f32_16x16x128_f8f6f4 v[138:141], v[26:33], v[194:201], v[138:141]
	v_mfma_f32_16x16x128_f8f6f4 v[130:133], v[18:25], v[202:209], v[130:133]
	v_mfma_f32_16x16x128_f8f6f4 v[122:125], v[26:33], v[202:209], v[122:125]
	v_mfma_f32_16x16x128_f8f6f4 v[114:117], v[18:25], v[210:217], v[114:117]
	v_mfma_f32_16x16x128_f8f6f4 v[106:109], v[26:33], v[210:217], v[106:109]
	s_setprio 2
	s_barrier
	v_mfma_f32_16x16x128_f8f6f4 v[102:105], v[18:25], v[218:225], v[102:105]
	v_mfma_f32_16x16x128_f8f6f4 v[98:101], v[26:33], v[218:225], v[98:101]
	s_setprio 0
	s_nop 0
	s_add_i32 s28, s80, s34
	v_lshl_add_u64 v[180:181], v[180:181], 0, s[14:15]
	s_mov_b32 m0, s28
	ds_read_b128 v[194:197], v191 offset:49152
	ds_read_b128 v[198:201], v191 offset:50176
	ds_read_b128 v[202:205], v191 offset:51200
	ds_read_b128 v[206:209], v191 offset:52224
	ds_read_b128 v[210:213], v191 offset:53248
	ds_read_b128 v[214:217], v191 offset:54272
	ds_read_b128 v[218:221], v191 offset:55296
	ds_read_b128 v[222:225], v191 offset:56320
	global_load_lds_dwordx4 v[180:181], off
	v_lshl_add_u64 v[180:181], v[182:183], 0, s[14:15]
	s_add_i32 m0, s28, 0x2000
	v_lshl_add_u64 v[178:179], v[178:179], 0, s[16:17]
	s_add_i32 s28, s81, s34
	global_load_lds_dwordx4 v[180:181], off
	v_lshl_add_u64 v[180:181], v[178:179], 0, v[164:165]
	s_mov_b32 m0, s28
	v_lshl_add_u64 v[178:179], v[178:179], 0, v[166:167]
	global_load_lds_dwordx4 v[180:181], off
	s_add_i32 m0, s28, 0x2000
	s_nop 0
	global_load_lds_dwordx4 v[178:179], off
	v_lshl_add_u64 v[178:179], v[184:185], 0, s[14:15]
	s_mov_b32 m0, s65
	s_nop 0
	global_load_lds_dwordx4 v[178:179], off
	v_lshl_add_u64 v[178:179], v[186:187], 0, s[14:15]
	s_mov_b32 m0, s66
	s_nop 0
	global_load_lds_dwordx4 v[178:179], off
	s_waitcnt vmcnt(8)
	s_waitcnt lgkmcnt(0)
	s_barrier
	s_setprio 1
	s_waitcnt lgkmcnt(0)
	v_mfma_f32_16x16x128_f8f6f4 v[94:97], v[2:9], v[194:201], v[94:97]
	v_mfma_f32_16x16x128_f8f6f4 v[90:93], v[10:17], v[194:201], v[90:93]
	v_mfma_f32_16x16x128_f8f6f4 v[86:89], v[2:9], v[202:209], v[86:89]
	v_mfma_f32_16x16x128_f8f6f4 v[78:81], v[10:17], v[202:209], v[78:81]
	v_mfma_f32_16x16x128_f8f6f4 v[70:73], v[2:9], v[210:217], v[70:73]
	v_mfma_f32_16x16x128_f8f6f4 v[62:65], v[10:17], v[210:217], v[62:65]
	v_mfma_f32_16x16x128_f8f6f4 v[54:57], v[2:9], v[218:225], v[54:57]
	v_mfma_f32_16x16x128_f8f6f4 v[46:49], v[10:17], v[218:225], v[46:49]
	s_setprio 0
	s_setprio 1
	v_mfma_f32_16x16x128_f8f6f4 v[82:85], v[18:25], v[194:201], v[82:85]
	v_mfma_f32_16x16x128_f8f6f4 v[74:77], v[26:33], v[194:201], v[74:77]
	v_mfma_f32_16x16x128_f8f6f4 v[66:69], v[18:25], v[202:209], v[66:69]
	v_mfma_f32_16x16x128_f8f6f4 v[58:61], v[26:33], v[202:209], v[58:61]
	v_mfma_f32_16x16x128_f8f6f4 v[50:53], v[18:25], v[210:217], v[50:53]
	v_mfma_f32_16x16x128_f8f6f4 v[42:45], v[26:33], v[210:217], v[42:45]
	s_setprio 2
	s_barrier
	v_mfma_f32_16x16x128_f8f6f4 v[38:41], v[18:25], v[218:225], v[38:41]
	v_mfma_f32_16x16x128_f8f6f4 v[34:37], v[26:33], v[218:225], v[34:37]
	s_setprio 0
	s_nop 0
	s_add_u32 s26, s26, 0x100
	s_addc_u32 s27, s27, 0
	v_lshl_add_u64 v[176:177], v[176:177], 0, s[22:23]
	s_cmp_ge_u32 s25, s67
	s_mov_b32 s28, s25
	s_cbranch_scc0 .LBB0_2058
	s_branch .Lpeel_exit_11
